# write-through (sc0 sc1) stores in the full-line thin phases (dcombine, norms, router, scatter) so the barrier's L2 writeback has less to flush
# speedup vs baseline: 1.0176x; 1.0042x over previous
; #define GAS __attribute__((address_space(1)))
; __device__ __forceinline__ f32x4 bf4_to_f32(u32x2_g a) { return (f32x4){__uint_as_float(a.x << 16), __uint_as_float(a.x & 0xffff0000u), __uint_as_float(a.y << 16), __uint_as_float(a.y & 0xffff0000u)}; }
; #define lane (lane_id())
; template <bool F8, bool SRC16, int NR> __device__ __forceinline__ void norm_rows(const void* srcv, const float* gain, void* dstv, int vcu, int G, int wave, int lane) {
;     ...
;     for (int m0 = gw; m0 < M; m0 += NR * NGW) {
;         f32x4 v[NR][8];
; #pragma unroll
;         for (int q = 0; q < NR; ++q) { const int mq = m0 + q * NGW; const int m = mq < M ? mq : m0;
;             if constexpr (SRC16) { const GAS u32x2_g* xr = (const GAS u32x2_g*)((const bf16*)srcv + (size_t)m * D) + lane;
; #pragma unroll
;                 for (int j = 0; j < 8; ++j) v[q][j] = bf4_to_f32(xr[64 * j]); }
;             else { const GAS f32x4* xr = (const GAS f32x4*)((const float*)srcv + (size_t)m * D) + lane;
; #pragma unroll
;                 for (int j = 0; j < 8; ++j) v[q][j] = xr[64 * j]; } }
; #pragma unroll
;         for (int q = 0; q < NR; ++q) { const int m = m0 + q * NGW; if (m >= M) break;
;             float s = 0.f;
; #pragma unroll
;             for (int j = 0; j < 8; ++j) s += (v[q][j].x * v[q][j].x + v[q][j].y * v[q][j].y) + (v[q][j].z * v[q][j].z + v[q][j].w * v[q][j].w);
;             const float r = 1.0f / sqrtf(wave_sum(s) * (1.0f / D) + EPS);
.LBB0_96:
	s_movk_i32 s0, 0xf000
	s_waitcnt vmcnt(8)
	v_add_co_u32_e32 v34, vcc, s0, v176
	global_load_dwordx4 v[146:149], v[176:177], off offset:-4096
	global_load_dwordx4 v[138:141], v[176:177], off offset:-2048
	global_load_dwordx4 v[142:145], v[176:177], off offset:-3072
	global_load_dwordx4 v[134:137], v[176:177], off offset:-1024
	v_addc_co_u32_e32 v35, vcc, -1, v177, vcc
	global_load_dwordx4 v[158:161], v[34:35], off offset:-3072
	global_load_dwordx4 v[154:157], v[34:35], off offset:-2048
	global_load_dwordx4 v[150:153], v[34:35], off offset:-1024
	global_load_dwordx4 v[130:133], v[176:177], off
	s_add_i32 s15, s68, s18
	s_cmpk_lt_i32 s15, 0x2000
	s_cselect_b32 s0, s15, s18
	s_ashr_i32 s1, s0, 31
	s_add_i32 s14, s50, s18
	s_lshl_b64 s[0:1], s[0:1], 13
	s_cmpk_lt_i32 s14, 0x2000
	s_cselect_b64 s[16:17], -1, 0
	v_lshl_add_u64 v[34:35], v[170:171], 0, s[0:1]
	s_and_b64 s[0:1], s[16:17], exec
	s_cselect_b32 s12, s14, s18
	global_load_dwordx4 v[126:129], v[34:35], off
	global_load_dwordx4 v[122:125], v[34:35], off offset:1024
	global_load_dwordx4 v[118:121], v[34:35], off offset:2048
	global_load_dwordx4 v[114:117], v[34:35], off offset:3072
	v_add_co_u32_e32 v34, vcc, s19, v34
	s_ashr_i32 s13, s12, 31
	s_nop 0
	v_addc_co_u32_e32 v35, vcc, 0, v35, vcc
	s_lshl_b64 s[12:13], s[12:13], 13
	global_load_dwordx4 v[110:113], v[34:35], off
	global_load_dwordx4 v[106:109], v[34:35], off offset:1024
	global_load_dwordx4 v[102:105], v[34:35], off offset:2048
	global_load_dwordx4 v[98:101], v[34:35], off offset:3072
	v_lshl_add_u64 v[34:35], v[170:171], 0, s[12:13]
	s_add_i32 s0, s53, s18
	global_load_dwordx4 v[78:81], v[34:35], off
	global_load_dwordx4 v[74:77], v[34:35], off offset:1024
	global_load_dwordx4 v[70:73], v[34:35], off offset:2048
	global_load_dwordx4 v[66:69], v[34:35], off offset:3072
	v_add_co_u32_e32 v34, vcc, s19, v34
	s_cmpk_lt_i32 s0, 0x2000
	s_nop 0
	v_addc_co_u32_e32 v35, vcc, 0, v35, vcc
	s_cselect_b64 s[12:13], -1, 0
	s_and_b64 s[20:21], s[12:13], exec
	s_cselect_b32 s20, s0, s18
	s_ashr_i32 s21, s20, 31
	s_lshl_b64 s[20:21], s[20:21], 13
	global_load_dwordx4 v[94:97], v[34:35], off
	global_load_dwordx4 v[90:93], v[34:35], off offset:1024
	global_load_dwordx4 v[86:89], v[34:35], off offset:2048
	global_load_dwordx4 v[82:85], v[34:35], off offset:3072
	v_lshl_add_u64 v[34:35], v[170:171], 0, s[20:21]
	s_cmpk_gt_i32 s15, 0x1fff
	s_waitcnt vmcnt(23)
	v_mul_f32_e32 v0, v147, v147
	v_mul_f32_e32 v36, v149, v149
	s_waitcnt vmcnt(21)
	v_mul_f32_e32 v37, v143, v143
	v_mul_f32_e32 v38, v145, v145
	v_mul_f32_e32 v39, v139, v139
	v_mul_f32_e32 v40, v141, v141
	s_waitcnt vmcnt(19)
	v_mul_f32_e32 v43, v159, v159
	v_mul_f32_e32 v44, v161, v161
	s_waitcnt vmcnt(18)
	v_mul_f32_e32 v45, v155, v155
	v_mul_f32_e32 v46, v157, v157
	s_waitcnt vmcnt(17)
	v_mul_f32_e32 v47, v151, v151
	v_mul_f32_e32 v48, v153, v153
	v_fmac_f32_e32 v0, v146, v146
	v_fmac_f32_e32 v36, v148, v148
	v_fmac_f32_e32 v37, v142, v142
	v_fmac_f32_e32 v38, v144, v144
	v_fmac_f32_e32 v39, v138, v138
	v_fmac_f32_e32 v40, v140, v140
	v_fmac_f32_e32 v43, v158, v158
	v_fmac_f32_e32 v44, v160, v160
	v_fmac_f32_e32 v45, v154, v154
	v_fmac_f32_e32 v46, v156, v156
	v_fmac_f32_e32 v47, v150, v150
	v_fmac_f32_e32 v48, v152, v152
	v_add_f32_e32 v0, v0, v36
	v_add_f32_e32 v36, v37, v38
	v_add_f32_e32 v37, v39, v40
	v_add_f32_e32 v38, v43, v44
	v_add_f32_e32 v39, v45, v46
	v_add_f32_e32 v40, v47, v48
	v_add_f32_e32 v38, v39, v38
	v_add_f32_e32 v38, v40, v38
	v_mul_f32_e32 v41, v135, v135
	v_mul_f32_e32 v42, v137, v137
	v_add_f32_e32 v0, v0, v38
	v_fmac_f32_e32 v41, v134, v134
	v_fmac_f32_e32 v42, v136, v136
	v_add_f32_e32 v0, v36, v0
	v_add_f32_e32 v0, v37, v0
	v_add_f32_e32 v36, v41, v42
	v_add_f32_e32 v0, v36, v0
	s_waitcnt vmcnt(16)
	v_mul_f32_e32 v36, v131, v131
	v_mul_f32_e32 v37, v133, v133
	v_fmac_f32_e32 v36, v130, v130
	v_fmac_f32_e32 v37, v132, v132
	v_add_f32_e32 v36, v36, v37
	v_add_f32_e32 v0, v36, v0
	global_load_dwordx4 v[62:65], v[34:35], off
	global_load_dwordx4 v[58:61], v[34:35], off offset:1024
	global_load_dwordx4 v[54:57], v[34:35], off offset:2048
	global_load_dwordx4 v[46:49], v[34:35], off offset:3072
	v_add_f32_dpp v0, v0, v0 quad_perm:[1,0,3,2] row_mask:0xf bank_mask:0xf bound_ctrl:1
	v_add_co_u32_e64 v34, s[36:37], s19, v34
	s_nop 0
	v_add_f32_dpp v0, v0, v0 quad_perm:[2,3,0,1] row_mask:0xf bank_mask:0xf bound_ctrl:1
	ds_swizzle_b32 v36, v0 offset:swizzle(SWAP,4)
	v_addc_co_u32_e64 v35, s[36:37], 0, v35, s[36:37]
	s_waitcnt lgkmcnt(0)
	v_add_f32_e32 v0, v0, v36
	ds_swizzle_b32 v36, v0 offset:swizzle(SWAP,8)
	s_waitcnt lgkmcnt(0)
	v_add_f32_e32 v0, v0, v36
	ds_swizzle_b32 v36, v0 offset:swizzle(SWAP,16)
	s_waitcnt lgkmcnt(0)
; __device__ __forceinline__ unsigned pk4_fp8(float a, float b, float c, float d) { int w = 0; w = __builtin_amdgcn_cvt_pk_fp8_f32(a, b, w, false); w = __builtin_amdgcn_cvt_pk_fp8_f32(c, d, w, true); return (unsigned)w; }
; #define GAS __attribute__((address_space(1)))
; __device__ __forceinline__ unsigned pk2(float lo, float hi) { return f2bf(lo) | (f2bf(hi) << 16); }
; #define lane (lane_id())
; template <bool F8, bool SRC16, int NR> __device__ __forceinline__ void norm_rows(const void* srcv, const float* gain, void* dstv, int vcu, int G, int wave, int lane) {
;     ...
;             const float r = 1.0f / sqrtf(wave_sum(s) * (1.0f / D) + EPS);
;             if constexpr (F8) { GAS unsigned* o4 = (GAS unsigned*)((unsigned char*)dstv + (size_t)m * D) + lane;
; #pragma unroll
;                 for (int j = 0; j < 8; ++j) o4[64 * j] = pg8::pk4_fp8(v[q][j].x * r * g[j].x, v[q][j].y * r * g[j].y, v[q][j].z * r * g[j].z, v[q][j].w * r * g[j].w); }
;             else { GAS unsigned long long* o8 = (GAS unsigned long long*)((bf16*)dstv + (size_t)m * D) + lane;
; #pragma unroll
;                 for (int j = 0; j < 8; ++j) o8[64 * j] = (unsigned long long)pk2(v[q][j].x * r * g[j].x, v[q][j].y * r * g[j].y) | ((unsigned long long)pk2(v[q][j].z * r * g[j].z, v[q][j].w * r * g[j].w) << 32); }
	v_add_f32_e32 v0, v0, v36
	v_mov_b32_e32 v36, v0
	s_nop 1
	v_permlane32_swap_b32_e32 v0, v36
	v_add_f32_e32 v0, v0, v36
	v_fmamk_f32 v0, v0, 0x3a000000, v204
	v_mul_f32_e32 v36, 0x4f800000, v0
	v_cmp_gt_f32_e32 vcc, s9, v0
	s_nop 1
	v_cndmask_b32_e32 v0, v0, v36, vcc
	v_sqrt_f32_e32 v36, v0
	s_nop 0
	v_add_u32_e32 v37, -1, v36
	v_fma_f32 v38, -v37, v36, v0
	v_cmp_ge_f32_e64 s[36:37], 0, v38
	v_add_u32_e32 v38, 1, v36
	s_nop 0
	v_cndmask_b32_e64 v37, v36, v37, s[36:37]
	v_fma_f32 v36, -v38, v36, v0
	v_cmp_lt_f32_e64 s[36:37], 0, v36
	s_nop 1
	v_cndmask_b32_e64 v36, v37, v38, s[36:37]
	v_mul_f32_e32 v37, 0x37800000, v36
	v_cndmask_b32_e32 v36, v36, v37, vcc
	v_cmp_class_f32_e32 vcc, v0, v205
	s_nop 1
	v_cndmask_b32_e32 v0, v36, v0, vcc
	v_div_scale_f32 v162, s[20:21], v0, v0, 1.0
	v_rcp_f32_e32 v163, v162
	global_load_dwordx4 v[50:53], v[34:35], off
	global_load_dwordx4 v[42:45], v[34:35], off offset:1024
	global_load_dwordx4 v[38:41], v[34:35], off offset:2048
	s_nop 0
	global_load_dwordx4 v[34:37], v[34:35], off offset:3072
	v_fma_f32 v164, -v162, v163, 1.0
	v_fmac_f32_e32 v163, v164, v163
	v_div_scale_f32 v164, vcc, 1.0, v0, 1.0
	v_mul_f32_e32 v165, v164, v163
	v_fma_f32 v166, -v162, v165, v164
	v_fmac_f32_e32 v165, v166, v163
	v_fma_f32 v162, -v162, v165, v164
	v_div_fmas_f32 v162, v162, v163, v165
	v_div_fixup_f32 v0, v162, v0, 1.0
	v_mul_f32_e32 v158, v158, v0
	v_mul_f32_e32 v158, v30, v158
	v_mul_f32_e32 v159, v159, v0
	v_mul_f32_e32 v159, v31, v159
	v_bfe_u32 v164, v158, 16, 1
	v_add3_u32 v158, v158, v164, s10
	v_bfe_u32 v164, v159, 16, 1
	v_lshrrev_b32_e32 v158, 16, v158
	v_add3_u32 v159, v159, v164, s10
	v_and_or_b32 v158, v159, s11, v158
	v_mul_f32_e32 v159, v160, v0
	v_mul_f32_e32 v159, v32, v159
	v_mul_f32_e32 v160, v161, v0
	v_mul_f32_e32 v160, v33, v160
	v_bfe_u32 v161, v159, 16, 1
	v_add3_u32 v159, v159, v161, s10
	v_bfe_u32 v161, v160, 16, 1
	v_lshrrev_b32_e32 v159, 16, v159
	v_add3_u32 v160, v160, v161, s10
	v_mul_f32_e32 v154, v154, v0
	v_lshl_add_u64 v[162:163], v[174:175], 0, s[22:23]
	v_and_or_b32 v159, v160, s11, v159
	v_mul_f32_e32 v154, v26, v154
	v_mul_f32_e32 v155, v155, v0
	global_store_dwordx2 v[162:163], v[158:159], off offset:-2048 sc0 sc1
	v_mul_f32_e32 v155, v27, v155
	v_bfe_u32 v158, v154, 16, 1
	v_add3_u32 v154, v154, v158, s10
	v_bfe_u32 v158, v155, 16, 1
	v_lshrrev_b32_e32 v154, 16, v154
	v_add3_u32 v155, v155, v158, s10
	v_and_or_b32 v154, v155, s11, v154
	v_mul_f32_e32 v155, v156, v0
	v_mul_f32_e32 v155, v28, v155
	v_mul_f32_e32 v156, v157, v0
	v_mul_f32_e32 v156, v29, v156
	v_bfe_u32 v157, v155, 16, 1
	v_add3_u32 v155, v155, v157, s10
	v_bfe_u32 v157, v156, 16, 1
	v_lshrrev_b32_e32 v155, 16, v155
	v_add3_u32 v156, v156, v157, s10
	v_mul_f32_e32 v150, v150, v0
	v_and_or_b32 v155, v156, s11, v155
	v_mul_f32_e32 v150, v22, v150
	v_mul_f32_e32 v151, v151, v0
	global_store_dwordx2 v[162:163], v[154:155], off offset:-1536 sc0 sc1
	v_mul_f32_e32 v151, v23, v151
	v_bfe_u32 v154, v150, 16, 1
	v_add3_u32 v150, v150, v154, s10
	v_bfe_u32 v154, v151, 16, 1
	v_lshrrev_b32_e32 v150, 16, v150
	v_add3_u32 v151, v151, v154, s10
	v_and_or_b32 v150, v151, s11, v150
	v_mul_f32_e32 v151, v152, v0
	v_mul_f32_e32 v151, v24, v151
	v_mul_f32_e32 v152, v153, v0
	v_mul_f32_e32 v152, v25, v152
	v_bfe_u32 v153, v151, 16, 1
	v_add3_u32 v151, v151, v153, s10
	v_bfe_u32 v153, v152, 16, 1
	v_lshrrev_b32_e32 v151, 16, v151
	v_add3_u32 v152, v152, v153, s10
	v_mul_f32_e32 v146, v146, v0
	v_and_or_b32 v151, v152, s11, v151
	v_mul_f32_e32 v146, v18, v146
	v_mul_f32_e32 v147, v147, v0
	global_store_dwordx2 v[162:163], v[150:151], off offset:-1024 sc0 sc1
	v_mul_f32_e32 v147, v19, v147
	v_bfe_u32 v150, v146, 16, 1
	v_add3_u32 v146, v146, v150, s10
	v_bfe_u32 v150, v147, 16, 1
	v_lshrrev_b32_e32 v146, 16, v146
	v_add3_u32 v147, v147, v150, s10
	v_and_or_b32 v146, v147, s11, v146
	v_mul_f32_e32 v147, v148, v0
	v_mul_f32_e32 v147, v20, v147
	v_mul_f32_e32 v148, v149, v0
	v_mul_f32_e32 v148, v21, v148
	v_bfe_u32 v149, v147, 16, 1
	v_add3_u32 v147, v147, v149, s10
	v_bfe_u32 v149, v148, 16, 1
	v_lshrrev_b32_e32 v147, 16, v147
	v_add3_u32 v148, v148, v149, s10
	v_mul_f32_e32 v142, v142, v0
	v_and_or_b32 v147, v148, s11, v147
	v_mul_f32_e32 v142, v14, v142
	v_mul_f32_e32 v143, v143, v0
	global_store_dwordx2 v[162:163], v[146:147], off offset:-512 sc0 sc1
	v_mul_f32_e32 v143, v15, v143
	v_bfe_u32 v146, v142, 16, 1
	v_add3_u32 v142, v142, v146, s10
	v_bfe_u32 v146, v143, 16, 1
	v_lshrrev_b32_e32 v142, 16, v142
	v_add3_u32 v143, v143, v146, s10
	v_and_or_b32 v142, v143, s11, v142
	v_mul_f32_e32 v143, v144, v0
	v_mul_f32_e32 v143, v16, v143
	v_mul_f32_e32 v144, v145, v0
	v_mul_f32_e32 v144, v17, v144
	v_bfe_u32 v145, v143, 16, 1
	v_add3_u32 v143, v143, v145, s10
	v_bfe_u32 v145, v144, 16, 1
	v_lshrrev_b32_e32 v143, 16, v143
	v_add3_u32 v144, v144, v145, s10
	v_mul_f32_e32 v138, v138, v0
	v_and_or_b32 v143, v144, s11, v143
	v_mul_f32_e32 v138, v10, v138
	v_mul_f32_e32 v139, v139, v0
	global_store_dwordx2 v[162:163], v[142:143], off sc0 sc1
	v_mul_f32_e32 v139, v11, v139
	v_bfe_u32 v142, v138, 16, 1
	v_add3_u32 v138, v138, v142, s10
	v_bfe_u32 v142, v139, 16, 1
	v_lshrrev_b32_e32 v138, 16, v138
	v_add3_u32 v139, v139, v142, s10
	v_and_or_b32 v138, v139, s11, v138
	v_mul_f32_e32 v139, v140, v0
	v_mul_f32_e32 v139, v12, v139
	v_mul_f32_e32 v140, v141, v0
	v_mul_f32_e32 v140, v13, v140
	v_bfe_u32 v141, v139, 16, 1
	v_add3_u32 v139, v139, v141, s10
	v_bfe_u32 v141, v140, 16, 1
	v_lshrrev_b32_e32 v139, 16, v139
	v_add3_u32 v140, v140, v141, s10
	v_mul_f32_e32 v134, v134, v0
	v_and_or_b32 v139, v140, s11, v139
	v_mul_f32_e32 v134, v6, v134
; __device__ __forceinline__ unsigned pk4_fp8(float a, float b, float c, float d) { int w = 0; w = __builtin_amdgcn_cvt_pk_fp8_f32(a, b, w, false); w = __builtin_amdgcn_cvt_pk_fp8_f32(c, d, w, true); return (unsigned)w; }
; #define GAS __attribute__((address_space(1)))
; __device__ __forceinline__ unsigned pk2(float lo, float hi) { return f2bf(lo) | (f2bf(hi) << 16); }
; #define lane (lane_id())
; template <bool F8, bool SRC16, int NR> __device__ __forceinline__ void norm_rows(const void* srcv, const float* gain, void* dstv, int vcu, int G, int wave, int lane) {
;     ...
;         for (int q = 0; q < NR; ++q) { const int m = m0 + q * NGW; if (m >= M) break;
;             float s = 0.f;
; #pragma unroll
;             for (int j = 0; j < 8; ++j) s += (v[q][j].x * v[q][j].x + v[q][j].y * v[q][j].y) + (v[q][j].z * v[q][j].z + v[q][j].w * v[q][j].w);
;             const float r = 1.0f / sqrtf(wave_sum(s) * (1.0f / D) + EPS);
;             if constexpr (F8) { GAS unsigned* o4 = (GAS unsigned*)((unsigned char*)dstv + (size_t)m * D) + lane;
; #pragma unroll
;                 for (int j = 0; j < 8; ++j) o4[64 * j] = pg8::pk4_fp8(v[q][j].x * r * g[j].x, v[q][j].y * r * g[j].y, v[q][j].z * r * g[j].z, v[q][j].w * r * g[j].w); }
;             else { GAS unsigned long long* o8 = (GAS unsigned long long*)((bf16*)dstv + (size_t)m * D) + lane;
; #pragma unroll
;                 for (int j = 0; j < 8; ++j) o8[64 * j] = (unsigned long long)pk2(v[q][j].x * r * g[j].x, v[q][j].y * r * g[j].y) | ((unsigned long long)pk2(v[q][j].z * r * g[j].z, v[q][j].w * r * g[j].w) << 32); }
	v_mul_f32_e32 v135, v135, v0
	global_store_dwordx2 v[162:163], v[138:139], off offset:512 sc0 sc1
	v_mul_f32_e32 v135, v7, v135
	v_bfe_u32 v138, v134, 16, 1
	v_add3_u32 v134, v134, v138, s10
	v_bfe_u32 v138, v135, 16, 1
	v_lshrrev_b32_e32 v134, 16, v134
	v_add3_u32 v135, v135, v138, s10
	v_and_or_b32 v134, v135, s11, v134
	v_mul_f32_e32 v135, v136, v0
	v_mul_f32_e32 v135, v8, v135
	v_mul_f32_e32 v136, v137, v0
	v_mul_f32_e32 v136, v9, v136
	v_bfe_u32 v137, v135, 16, 1
	v_add3_u32 v135, v135, v137, s10
	v_bfe_u32 v137, v136, 16, 1
	v_lshrrev_b32_e32 v135, 16, v135
	v_add3_u32 v136, v136, v137, s10
	v_mul_f32_e32 v130, v130, v0
	v_and_or_b32 v135, v136, s11, v135
	v_mul_f32_e32 v130, v2, v130
	v_mul_f32_e32 v131, v131, v0
	global_store_dwordx2 v[162:163], v[134:135], off offset:1024 sc0 sc1
	v_mul_f32_e32 v131, v3, v131
	v_bfe_u32 v134, v130, 16, 1
	v_add3_u32 v130, v130, v134, s10
	v_bfe_u32 v134, v131, 16, 1
	v_lshrrev_b32_e32 v130, 16, v130
	v_add3_u32 v131, v131, v134, s10
	v_and_or_b32 v130, v131, s11, v130
	v_mul_f32_e32 v131, v132, v0
	v_mul_f32_e32 v131, v4, v131
	v_mul_f32_e32 v0, v133, v0
	v_mul_f32_e32 v0, v5, v0
	v_bfe_u32 v132, v131, 16, 1
	v_add3_u32 v131, v131, v132, s10
	v_bfe_u32 v132, v0, 16, 1
	v_lshrrev_b32_e32 v131, 16, v131
	v_add3_u32 v0, v0, v132, s10
	v_and_or_b32 v131, v0, s11, v131
	global_store_dwordx2 v[162:163], v[130:131], off offset:1536 sc0 sc1
	s_cbranch_scc1 .LBB0_95
	s_waitcnt vmcnt(31)
	v_mul_f32_e32 v0, v127, v127
	v_mul_f32_e32 v130, v129, v129
	v_fmac_f32_e32 v0, v126, v126
	v_fmac_f32_e32 v130, v128, v128
	v_add_f32_e32 v0, v0, v130
	s_waitcnt vmcnt(30)
	v_mul_f32_e32 v130, v123, v123
	v_mul_f32_e32 v131, v125, v125
	v_fmac_f32_e32 v130, v122, v122
	v_fmac_f32_e32 v131, v124, v124
	v_add_f32_e32 v130, v130, v131
	v_add_f32_e32 v0, v0, v130
	s_waitcnt vmcnt(29)
	v_mul_f32_e32 v130, v119, v119
	v_mul_f32_e32 v131, v121, v121
	v_fmac_f32_e32 v130, v118, v118
	v_fmac_f32_e32 v131, v120, v120
	v_add_f32_e32 v130, v130, v131
	v_add_f32_e32 v0, v0, v130
	s_waitcnt vmcnt(28)
	v_mul_f32_e32 v130, v115, v115
	v_mul_f32_e32 v131, v117, v117
	v_fmac_f32_e32 v130, v114, v114
	v_fmac_f32_e32 v131, v116, v116
	v_add_f32_e32 v130, v130, v131
	v_add_f32_e32 v0, v0, v130
	s_waitcnt vmcnt(27)
	v_mul_f32_e32 v130, v111, v111
	v_mul_f32_e32 v131, v113, v113
	v_fmac_f32_e32 v130, v110, v110
	v_fmac_f32_e32 v131, v112, v112
	v_add_f32_e32 v130, v130, v131
	v_add_f32_e32 v0, v0, v130
	s_waitcnt vmcnt(26)
	v_mul_f32_e32 v130, v107, v107
	v_mul_f32_e32 v131, v109, v109
	v_fmac_f32_e32 v130, v106, v106
	v_fmac_f32_e32 v131, v108, v108
	v_add_f32_e32 v130, v130, v131
	v_add_f32_e32 v0, v0, v130
	s_waitcnt vmcnt(25)
	v_mul_f32_e32 v130, v103, v103
	v_mul_f32_e32 v131, v105, v105
	v_fmac_f32_e32 v130, v102, v102
	v_fmac_f32_e32 v131, v104, v104
	v_add_f32_e32 v130, v130, v131
	v_add_f32_e32 v0, v0, v130
	s_waitcnt vmcnt(24)
	v_mul_f32_e32 v130, v99, v99
	v_mul_f32_e32 v131, v101, v101
	v_fmac_f32_e32 v130, v98, v98
	v_fmac_f32_e32 v131, v100, v100
	v_add_f32_e32 v130, v130, v131
	v_add_f32_e32 v0, v0, v130
	s_nop 1
	v_add_f32_dpp v0, v0, v0 quad_perm:[1,0,3,2] row_mask:0xf bank_mask:0xf bound_ctrl:1
	s_nop 1
	v_add_f32_dpp v0, v0, v0 quad_perm:[2,3,0,1] row_mask:0xf bank_mask:0xf bound_ctrl:1
	ds_swizzle_b32 v130, v0 offset:swizzle(SWAP,4)
	s_waitcnt lgkmcnt(0)
	v_add_f32_e32 v0, v0, v130
	ds_swizzle_b32 v130, v0 offset:swizzle(SWAP,8)
	s_waitcnt lgkmcnt(0)
	v_add_f32_e32 v0, v0, v130
	ds_swizzle_b32 v130, v0 offset:swizzle(SWAP,16)
	s_waitcnt lgkmcnt(0)
	v_add_f32_e32 v0, v0, v130
	v_mov_b32_e32 v130, v0
	s_nop 1
	v_permlane32_swap_b32_e32 v0, v130
	v_add_f32_e32 v0, v0, v130
	v_fmamk_f32 v0, v0, 0x3a000000, v204
	v_mul_f32_e32 v130, 0x4f800000, v0
	v_cmp_gt_f32_e32 vcc, s9, v0
	s_nop 1
	v_cndmask_b32_e32 v0, v0, v130, vcc
	v_sqrt_f32_e32 v130, v0
	s_nop 0
	v_add_u32_e32 v131, -1, v130
	v_fma_f32 v132, -v131, v130, v0
	v_cmp_ge_f32_e64 s[36:37], 0, v132
	v_add_u32_e32 v132, 1, v130
	s_nop 0
	v_cndmask_b32_e64 v131, v130, v131, s[36:37]
	v_fma_f32 v130, -v132, v130, v0
	v_cmp_lt_f32_e64 s[36:37], 0, v130
	s_nop 1
	v_cndmask_b32_e64 v130, v131, v132, s[36:37]
	v_mul_f32_e32 v131, 0x37800000, v130
	v_cndmask_b32_e32 v130, v130, v131, vcc
	v_cmp_class_f32_e32 vcc, v0, v205
	s_nop 1
	v_cndmask_b32_e32 v0, v130, v0, vcc
	v_div_scale_f32 v130, s[20:21], v0, v0, 1.0
	v_rcp_f32_e32 v131, v130
	v_readlane_b32 s20, v253, 15
	v_readlane_b32 s21, v253, 16
	v_fma_f32 v132, -v130, v131, 1.0
	v_fmac_f32_e32 v131, v132, v131
	v_div_scale_f32 v132, vcc, 1.0, v0, 1.0
	v_mul_f32_e32 v133, v132, v131
	v_fma_f32 v134, -v130, v133, v132
	v_fmac_f32_e32 v133, v134, v131
	v_fma_f32 v130, -v130, v133, v132
	v_div_fmas_f32 v130, v130, v131, v133
	v_div_fixup_f32 v0, v130, v0, 1.0
	v_mul_f32_e32 v126, v126, v0
	v_mul_f32_e32 v126, v30, v126
	v_mul_f32_e32 v127, v127, v0
	v_mul_f32_e32 v127, v31, v127
	v_bfe_u32 v132, v126, 16, 1
	v_add3_u32 v126, v126, v132, s10
	v_bfe_u32 v132, v127, 16, 1
	v_lshrrev_b32_e32 v126, 16, v126
	v_add3_u32 v127, v127, v132, s10
	v_and_or_b32 v126, v127, s11, v126
	v_mul_f32_e32 v127, v128, v0
	v_mul_f32_e32 v127, v32, v127
	v_mul_f32_e32 v128, v129, v0
	v_mul_f32_e32 v128, v33, v128
	v_bfe_u32 v129, v127, 16, 1
	v_add3_u32 v127, v127, v129, s10
	v_bfe_u32 v129, v128, 16, 1
	v_lshrrev_b32_e32 v127, 16, v127
	v_add3_u32 v128, v128, v129, s10
	v_mul_f32_e32 v122, v122, v0
	v_lshl_add_u64 v[130:131], v[174:175], 0, s[20:21]
	v_and_or_b32 v127, v128, s11, v127
	v_mul_f32_e32 v122, v26, v122
	v_mul_f32_e32 v123, v123, v0
	global_store_dwordx2 v[130:131], v[126:127], off offset:-2048 sc0 sc1
	v_mul_f32_e32 v123, v27, v123
; __device__ __forceinline__ unsigned pk4_fp8(float a, float b, float c, float d) { int w = 0; w = __builtin_amdgcn_cvt_pk_fp8_f32(a, b, w, false); w = __builtin_amdgcn_cvt_pk_fp8_f32(c, d, w, true); return (unsigned)w; }
; #define GAS __attribute__((address_space(1)))
; __device__ __forceinline__ unsigned pk2(float lo, float hi) { return f2bf(lo) | (f2bf(hi) << 16); }
; #define lane (lane_id())
; template <bool F8, bool SRC16, int NR> __device__ __forceinline__ void norm_rows(const void* srcv, const float* gain, void* dstv, int vcu, int G, int wave, int lane) {
;     ...
;             if constexpr (F8) { GAS unsigned* o4 = (GAS unsigned*)((unsigned char*)dstv + (size_t)m * D) + lane;
; #pragma unroll
;                 for (int j = 0; j < 8; ++j) o4[64 * j] = pg8::pk4_fp8(v[q][j].x * r * g[j].x, v[q][j].y * r * g[j].y, v[q][j].z * r * g[j].z, v[q][j].w * r * g[j].w); }
;             else { GAS unsigned long long* o8 = (GAS unsigned long long*)((bf16*)dstv + (size_t)m * D) + lane;
; #pragma unroll
;                 for (int j = 0; j < 8; ++j) o8[64 * j] = (unsigned long long)pk2(v[q][j].x * r * g[j].x, v[q][j].y * r * g[j].y) | ((unsigned long long)pk2(v[q][j].z * r * g[j].z, v[q][j].w * r * g[j].w) << 32); }
	v_bfe_u32 v126, v122, 16, 1
	v_add3_u32 v122, v122, v126, s10
	v_bfe_u32 v126, v123, 16, 1
	v_lshrrev_b32_e32 v122, 16, v122
	v_add3_u32 v123, v123, v126, s10
	v_and_or_b32 v122, v123, s11, v122
	v_mul_f32_e32 v123, v124, v0
	v_mul_f32_e32 v123, v28, v123
	v_mul_f32_e32 v124, v125, v0
	v_mul_f32_e32 v124, v29, v124
	v_bfe_u32 v125, v123, 16, 1
	v_add3_u32 v123, v123, v125, s10
	v_bfe_u32 v125, v124, 16, 1
	v_lshrrev_b32_e32 v123, 16, v123
	v_add3_u32 v124, v124, v125, s10
	v_mul_f32_e32 v118, v118, v0
	v_and_or_b32 v123, v124, s11, v123
	v_mul_f32_e32 v118, v22, v118
	v_mul_f32_e32 v119, v119, v0
	global_store_dwordx2 v[130:131], v[122:123], off offset:-1536 sc0 sc1
	v_mul_f32_e32 v119, v23, v119
	v_bfe_u32 v122, v118, 16, 1
	v_add3_u32 v118, v118, v122, s10
	v_bfe_u32 v122, v119, 16, 1
	v_lshrrev_b32_e32 v118, 16, v118
	v_add3_u32 v119, v119, v122, s10
	v_and_or_b32 v118, v119, s11, v118
	v_mul_f32_e32 v119, v120, v0
	v_mul_f32_e32 v119, v24, v119
	v_mul_f32_e32 v120, v121, v0
	v_mul_f32_e32 v120, v25, v120
	v_bfe_u32 v121, v119, 16, 1
	v_add3_u32 v119, v119, v121, s10
	v_bfe_u32 v121, v120, 16, 1
	v_lshrrev_b32_e32 v119, 16, v119
	v_add3_u32 v120, v120, v121, s10
	v_mul_f32_e32 v114, v114, v0
	v_and_or_b32 v119, v120, s11, v119
	v_mul_f32_e32 v114, v18, v114
	v_mul_f32_e32 v115, v115, v0
	global_store_dwordx2 v[130:131], v[118:119], off offset:-1024 sc0 sc1
	v_mul_f32_e32 v115, v19, v115
	v_bfe_u32 v118, v114, 16, 1
	v_add3_u32 v114, v114, v118, s10
	v_bfe_u32 v118, v115, 16, 1
	v_lshrrev_b32_e32 v114, 16, v114
	v_add3_u32 v115, v115, v118, s10
	v_and_or_b32 v114, v115, s11, v114
	v_mul_f32_e32 v115, v116, v0
	v_mul_f32_e32 v115, v20, v115
	v_mul_f32_e32 v116, v117, v0
	v_mul_f32_e32 v116, v21, v116
	v_bfe_u32 v117, v115, 16, 1
	v_add3_u32 v115, v115, v117, s10
	v_bfe_u32 v117, v116, 16, 1
	v_lshrrev_b32_e32 v115, 16, v115
	v_add3_u32 v116, v116, v117, s10
	v_mul_f32_e32 v110, v110, v0
	v_and_or_b32 v115, v116, s11, v115
	v_mul_f32_e32 v110, v14, v110
	v_mul_f32_e32 v111, v111, v0
	global_store_dwordx2 v[130:131], v[114:115], off offset:-512 sc0 sc1
	v_mul_f32_e32 v111, v15, v111
	v_bfe_u32 v114, v110, 16, 1
	v_add3_u32 v110, v110, v114, s10
	v_bfe_u32 v114, v111, 16, 1
	v_lshrrev_b32_e32 v110, 16, v110
	v_add3_u32 v111, v111, v114, s10
	v_and_or_b32 v110, v111, s11, v110
	v_mul_f32_e32 v111, v112, v0
	v_mul_f32_e32 v111, v16, v111
	v_mul_f32_e32 v112, v113, v0
	v_mul_f32_e32 v112, v17, v112
	v_bfe_u32 v113, v111, 16, 1
	v_add3_u32 v111, v111, v113, s10
	v_bfe_u32 v113, v112, 16, 1
	v_lshrrev_b32_e32 v111, 16, v111
	v_add3_u32 v112, v112, v113, s10
	v_mul_f32_e32 v106, v106, v0
	v_and_or_b32 v111, v112, s11, v111
	v_mul_f32_e32 v106, v10, v106
	v_mul_f32_e32 v107, v107, v0
	global_store_dwordx2 v[130:131], v[110:111], off sc0 sc1
	v_mul_f32_e32 v107, v11, v107
	v_bfe_u32 v110, v106, 16, 1
	v_add3_u32 v106, v106, v110, s10
	v_bfe_u32 v110, v107, 16, 1
	v_lshrrev_b32_e32 v106, 16, v106
	v_add3_u32 v107, v107, v110, s10
	v_and_or_b32 v106, v107, s11, v106
	v_mul_f32_e32 v107, v108, v0
	v_mul_f32_e32 v107, v12, v107
	v_mul_f32_e32 v108, v109, v0
	v_mul_f32_e32 v108, v13, v108
	v_bfe_u32 v109, v107, 16, 1
	v_add3_u32 v107, v107, v109, s10
	v_bfe_u32 v109, v108, 16, 1
	v_lshrrev_b32_e32 v107, 16, v107
	v_add3_u32 v108, v108, v109, s10
	v_mul_f32_e32 v102, v102, v0
	v_and_or_b32 v107, v108, s11, v107
	v_mul_f32_e32 v102, v6, v102
	v_mul_f32_e32 v103, v103, v0
	global_store_dwordx2 v[130:131], v[106:107], off offset:512 sc0 sc1
	v_mul_f32_e32 v103, v7, v103
	v_bfe_u32 v106, v102, 16, 1
	v_add3_u32 v102, v102, v106, s10
	v_bfe_u32 v106, v103, 16, 1
	v_lshrrev_b32_e32 v102, 16, v102
	v_add3_u32 v103, v103, v106, s10
	v_and_or_b32 v102, v103, s11, v102
	v_mul_f32_e32 v103, v104, v0
	v_mul_f32_e32 v103, v8, v103
	v_mul_f32_e32 v104, v105, v0
	v_mul_f32_e32 v104, v9, v104
	v_bfe_u32 v105, v103, 16, 1
	v_add3_u32 v103, v103, v105, s10
	v_bfe_u32 v105, v104, 16, 1
	v_lshrrev_b32_e32 v103, 16, v103
	v_add3_u32 v104, v104, v105, s10
	v_mul_f32_e32 v98, v98, v0
	v_and_or_b32 v103, v104, s11, v103
	v_mul_f32_e32 v98, v2, v98
	v_mul_f32_e32 v99, v99, v0
	global_store_dwordx2 v[130:131], v[102:103], off offset:1024 sc0 sc1
	v_mul_f32_e32 v99, v3, v99
	v_bfe_u32 v102, v98, 16, 1
	v_add3_u32 v98, v98, v102, s10
	v_bfe_u32 v102, v99, 16, 1
	v_lshrrev_b32_e32 v98, 16, v98
	v_add3_u32 v99, v99, v102, s10
	v_and_or_b32 v98, v99, s11, v98
	v_mul_f32_e32 v99, v100, v0
	v_mul_f32_e32 v99, v4, v99
	v_mul_f32_e32 v0, v101, v0
	v_mul_f32_e32 v0, v5, v0
	v_bfe_u32 v100, v99, 16, 1
	v_add3_u32 v99, v99, v100, s10
	v_bfe_u32 v100, v0, 16, 1
	v_lshrrev_b32_e32 v99, 16, v99
	v_add3_u32 v0, v0, v100, s10
	v_and_or_b32 v99, v0, s11, v99
	s_andn2_b64 vcc, exec, s[16:17]
	global_store_dwordx2 v[130:131], v[98:99], off offset:1536 sc0 sc1
	s_cbranch_vccnz .LBB0_95
; __device__ __forceinline__ unsigned pk4_fp8(float a, float b, float c, float d) { int w = 0; w = __builtin_amdgcn_cvt_pk_fp8_f32(a, b, w, false); w = __builtin_amdgcn_cvt_pk_fp8_f32(c, d, w, true); return (unsigned)w; }
; #define GAS __attribute__((address_space(1)))
; __device__ __forceinline__ unsigned pk2(float lo, float hi) { return f2bf(lo) | (f2bf(hi) << 16); }
; #define lane (lane_id())
; template <bool F8, bool SRC16, int NR> __device__ __forceinline__ void norm_rows(const void* srcv, const float* gain, void* dstv, int vcu, int G, int wave, int lane) {
;     ...
;         for (int q = 0; q < NR; ++q) { const int m = m0 + q * NGW; if (m >= M) break;
;             float s = 0.f;
; #pragma unroll
;             for (int j = 0; j < 8; ++j) s += (v[q][j].x * v[q][j].x + v[q][j].y * v[q][j].y) + (v[q][j].z * v[q][j].z + v[q][j].w * v[q][j].w);
;             const float r = 1.0f / sqrtf(wave_sum(s) * (1.0f / D) + EPS);
;             if constexpr (F8) { GAS unsigned* o4 = (GAS unsigned*)((unsigned char*)dstv + (size_t)m * D) + lane;
; #pragma unroll
;                 for (int j = 0; j < 8; ++j) o4[64 * j] = pg8::pk4_fp8(v[q][j].x * r * g[j].x, v[q][j].y * r * g[j].y, v[q][j].z * r * g[j].z, v[q][j].w * r * g[j].w); }
;             else { GAS unsigned long long* o8 = (GAS unsigned long long*)((bf16*)dstv + (size_t)m * D) + lane;
; #pragma unroll
;                 for (int j = 0; j < 8; ++j) o8[64 * j] = (unsigned long long)pk2(v[q][j].x * r * g[j].x, v[q][j].y * r * g[j].y) | ((unsigned long long)pk2(v[q][j].z * r * g[j].z, v[q][j].w * r * g[j].w) << 32); }
	s_waitcnt vmcnt(31)
	v_mul_f32_e32 v0, v79, v79
	v_mul_f32_e32 v98, v81, v81
	v_fmac_f32_e32 v0, v78, v78
	v_fmac_f32_e32 v98, v80, v80
	v_add_f32_e32 v0, v0, v98
	s_waitcnt vmcnt(30)
	v_mul_f32_e32 v98, v75, v75
	v_mul_f32_e32 v99, v77, v77
	v_fmac_f32_e32 v98, v74, v74
	v_fmac_f32_e32 v99, v76, v76
	v_add_f32_e32 v98, v98, v99
	v_add_f32_e32 v0, v0, v98
	s_waitcnt vmcnt(29)
	v_mul_f32_e32 v98, v71, v71
	v_mul_f32_e32 v99, v73, v73
	v_fmac_f32_e32 v98, v70, v70
	v_fmac_f32_e32 v99, v72, v72
	v_add_f32_e32 v98, v98, v99
	v_add_f32_e32 v0, v0, v98
	s_waitcnt vmcnt(28)
	v_mul_f32_e32 v98, v67, v67
	v_mul_f32_e32 v99, v69, v69
	v_fmac_f32_e32 v98, v66, v66
	v_fmac_f32_e32 v99, v68, v68
	v_add_f32_e32 v98, v98, v99
	v_add_f32_e32 v0, v0, v98
	s_waitcnt vmcnt(27)
	v_mul_f32_e32 v98, v95, v95
	v_mul_f32_e32 v99, v97, v97
	v_fmac_f32_e32 v98, v94, v94
	v_fmac_f32_e32 v99, v96, v96
	v_add_f32_e32 v98, v98, v99
	v_add_f32_e32 v0, v0, v98
	s_waitcnt vmcnt(26)
	v_mul_f32_e32 v98, v91, v91
	v_mul_f32_e32 v99, v93, v93
	v_fmac_f32_e32 v98, v90, v90
	v_fmac_f32_e32 v99, v92, v92
	v_add_f32_e32 v98, v98, v99
	v_add_f32_e32 v0, v0, v98
	s_waitcnt vmcnt(25)
	v_mul_f32_e32 v98, v87, v87
	v_mul_f32_e32 v99, v89, v89
	v_fmac_f32_e32 v98, v86, v86
	v_fmac_f32_e32 v99, v88, v88
	v_add_f32_e32 v98, v98, v99
	v_add_f32_e32 v0, v0, v98
	s_waitcnt vmcnt(24)
	v_mul_f32_e32 v98, v83, v83
	v_mul_f32_e32 v99, v85, v85
	v_fmac_f32_e32 v98, v82, v82
	v_fmac_f32_e32 v99, v84, v84
	v_add_f32_e32 v98, v98, v99
	v_add_f32_e32 v0, v0, v98
	s_ashr_i32 s15, s14, 31
	s_lshl_b64 s[14:15], s[14:15], 12
	v_add_f32_dpp v0, v0, v0 quad_perm:[1,0,3,2] row_mask:0xf bank_mask:0xf bound_ctrl:1
	s_nop 1
	v_add_f32_dpp v0, v0, v0 quad_perm:[2,3,0,1] row_mask:0xf bank_mask:0xf bound_ctrl:1
	ds_swizzle_b32 v98, v0 offset:swizzle(SWAP,4)
	s_waitcnt lgkmcnt(0)
	v_add_f32_e32 v0, v0, v98
	ds_swizzle_b32 v98, v0 offset:swizzle(SWAP,8)
	s_waitcnt lgkmcnt(0)
	v_add_f32_e32 v0, v0, v98
	ds_swizzle_b32 v98, v0 offset:swizzle(SWAP,16)
	s_waitcnt lgkmcnt(0)
	v_add_f32_e32 v0, v0, v98
	v_mov_b32_e32 v98, v0
	s_nop 1
	v_permlane32_swap_b32_e32 v0, v98
	v_add_f32_e32 v0, v0, v98
	v_fmamk_f32 v0, v0, 0x3a000000, v204
	v_mul_f32_e32 v98, 0x4f800000, v0
	v_cmp_gt_f32_e32 vcc, s9, v0
	s_nop 1
	v_cndmask_b32_e32 v0, v0, v98, vcc
	v_sqrt_f32_e32 v98, v0
	s_nop 0
	v_add_u32_e32 v99, -1, v98
	v_fma_f32 v100, -v99, v98, v0
	v_cmp_ge_f32_e64 s[36:37], 0, v100
	v_add_u32_e32 v100, 1, v98
	s_nop 0
	v_cndmask_b32_e64 v99, v98, v99, s[36:37]
	v_fma_f32 v98, -v100, v98, v0
	v_cmp_lt_f32_e64 s[36:37], 0, v98
	s_nop 1
	v_cndmask_b32_e64 v98, v99, v100, s[36:37]
	v_mul_f32_e32 v99, 0x37800000, v98
	v_cndmask_b32_e32 v98, v98, v99, vcc
	v_cmp_class_f32_e32 vcc, v0, v205
	s_nop 1
	v_cndmask_b32_e32 v0, v98, v0, vcc
	v_div_scale_f32 v98, s[16:17], v0, v0, 1.0
	v_rcp_f32_e32 v99, v98
	s_nop 0
	v_fma_f32 v100, -v98, v99, 1.0
	v_fmac_f32_e32 v99, v100, v99
	v_div_scale_f32 v100, vcc, 1.0, v0, 1.0
	v_mul_f32_e32 v101, v100, v99
	v_fma_f32 v102, -v98, v101, v100
	v_fmac_f32_e32 v101, v102, v99
	v_fma_f32 v98, -v98, v101, v100
	v_div_fmas_f32 v98, v98, v99, v101
	v_div_fixup_f32 v0, v98, v0, 1.0
	v_mul_f32_e32 v78, v78, v0
	v_mul_f32_e32 v78, v30, v78
	v_mul_f32_e32 v79, v79, v0
	v_mul_f32_e32 v79, v31, v79
	v_bfe_u32 v100, v78, 16, 1
	v_add3_u32 v78, v78, v100, s10
	v_bfe_u32 v100, v79, 16, 1
	v_lshrrev_b32_e32 v78, 16, v78
	v_add3_u32 v79, v79, v100, s10
	v_and_or_b32 v78, v79, s11, v78
	v_mul_f32_e32 v79, v80, v0
	v_mul_f32_e32 v79, v32, v79
	v_mul_f32_e32 v80, v81, v0
	v_mul_f32_e32 v80, v33, v80
	v_bfe_u32 v81, v79, 16, 1
	v_add3_u32 v79, v79, v81, s10
	v_bfe_u32 v81, v80, 16, 1
	v_lshrrev_b32_e32 v79, 16, v79
	v_add3_u32 v80, v80, v81, s10
	v_mul_f32_e32 v74, v74, v0
	v_lshl_add_u64 v[98:99], v[172:173], 0, s[14:15]
	v_and_or_b32 v79, v80, s11, v79
	v_mul_f32_e32 v74, v26, v74
	v_mul_f32_e32 v75, v75, v0
	global_store_dwordx2 v[98:99], v[78:79], off sc0 sc1
	v_mul_f32_e32 v75, v27, v75
	v_bfe_u32 v78, v74, 16, 1
	v_add3_u32 v74, v74, v78, s10
	v_bfe_u32 v78, v75, 16, 1
	v_lshrrev_b32_e32 v74, 16, v74
	v_add3_u32 v75, v75, v78, s10
	v_and_or_b32 v74, v75, s11, v74
	v_mul_f32_e32 v75, v76, v0
	v_mul_f32_e32 v75, v28, v75
	v_mul_f32_e32 v76, v77, v0
	v_mul_f32_e32 v76, v29, v76
	v_bfe_u32 v77, v75, 16, 1
	v_add3_u32 v75, v75, v77, s10
	v_bfe_u32 v77, v76, 16, 1
	v_lshrrev_b32_e32 v75, 16, v75
	v_add3_u32 v76, v76, v77, s10
	v_mul_f32_e32 v70, v70, v0
	v_and_or_b32 v75, v76, s11, v75
	v_mul_f32_e32 v70, v22, v70
	v_mul_f32_e32 v71, v71, v0
	global_store_dwordx2 v[98:99], v[74:75], off offset:512 sc0 sc1
	v_mul_f32_e32 v71, v23, v71
	v_bfe_u32 v74, v70, 16, 1
	v_add3_u32 v70, v70, v74, s10
	v_bfe_u32 v74, v71, 16, 1
	v_lshrrev_b32_e32 v70, 16, v70
	v_add3_u32 v71, v71, v74, s10
	v_and_or_b32 v70, v71, s11, v70
	v_mul_f32_e32 v71, v72, v0
	v_mul_f32_e32 v71, v24, v71
	v_mul_f32_e32 v72, v73, v0
	v_mul_f32_e32 v72, v25, v72
	v_bfe_u32 v73, v71, 16, 1
	v_add3_u32 v71, v71, v73, s10
	v_bfe_u32 v73, v72, 16, 1
	v_lshrrev_b32_e32 v71, 16, v71
	v_add3_u32 v72, v72, v73, s10
	v_mul_f32_e32 v66, v66, v0
	v_and_or_b32 v71, v72, s11, v71
	v_mul_f32_e32 v66, v18, v66
	v_mul_f32_e32 v67, v67, v0
	global_store_dwordx2 v[98:99], v[70:71], off offset:1024 sc0 sc1
	v_mul_f32_e32 v67, v19, v67
	v_bfe_u32 v70, v66, 16, 1
	v_add3_u32 v66, v66, v70, s10
	v_bfe_u32 v70, v67, 16, 1
	v_lshrrev_b32_e32 v66, 16, v66
	v_add3_u32 v67, v67, v70, s10
	v_and_or_b32 v66, v67, s11, v66
	v_mul_f32_e32 v67, v68, v0
	v_mul_f32_e32 v67, v20, v67
	v_mul_f32_e32 v68, v69, v0
	v_mul_f32_e32 v68, v21, v68
	v_bfe_u32 v69, v67, 16, 1
	v_add3_u32 v67, v67, v69, s10
; __device__ __forceinline__ unsigned pk4_fp8(float a, float b, float c, float d) { int w = 0; w = __builtin_amdgcn_cvt_pk_fp8_f32(a, b, w, false); w = __builtin_amdgcn_cvt_pk_fp8_f32(c, d, w, true); return (unsigned)w; }
; #define GAS __attribute__((address_space(1)))
; __device__ __forceinline__ unsigned pk2(float lo, float hi) { return f2bf(lo) | (f2bf(hi) << 16); }
; #define lane (lane_id())
; template <bool F8, bool SRC16, int NR> __device__ __forceinline__ void norm_rows(const void* srcv, const float* gain, void* dstv, int vcu, int G, int wave, int lane) {
;     ...
;         for (int q = 0; q < NR; ++q) { const int m = m0 + q * NGW; if (m >= M) break;
;             float s = 0.f;
; #pragma unroll
;             for (int j = 0; j < 8; ++j) s += (v[q][j].x * v[q][j].x + v[q][j].y * v[q][j].y) + (v[q][j].z * v[q][j].z + v[q][j].w * v[q][j].w);
;             const float r = 1.0f / sqrtf(wave_sum(s) * (1.0f / D) + EPS);
;             if constexpr (F8) { GAS unsigned* o4 = (GAS unsigned*)((unsigned char*)dstv + (size_t)m * D) + lane;
; #pragma unroll
;                 for (int j = 0; j < 8; ++j) o4[64 * j] = pg8::pk4_fp8(v[q][j].x * r * g[j].x, v[q][j].y * r * g[j].y, v[q][j].z * r * g[j].z, v[q][j].w * r * g[j].w); }
;             else { GAS unsigned long long* o8 = (GAS unsigned long long*)((bf16*)dstv + (size_t)m * D) + lane;
; #pragma unroll
;                 for (int j = 0; j < 8; ++j) o8[64 * j] = (unsigned long long)pk2(v[q][j].x * r * g[j].x, v[q][j].y * r * g[j].y) | ((unsigned long long)pk2(v[q][j].z * r * g[j].z, v[q][j].w * r * g[j].w) << 32); }
	v_bfe_u32 v69, v68, 16, 1
	v_lshrrev_b32_e32 v67, 16, v67
	v_add3_u32 v68, v68, v69, s10
	v_and_or_b32 v67, v68, s11, v67
	global_store_dwordx2 v[98:99], v[66:67], off offset:1536 sc0 sc1
	v_mul_f32_e32 v66, v94, v0
	v_mul_f32_e32 v66, v14, v66
	v_mul_f32_e32 v67, v95, v0
	v_mul_f32_e32 v67, v15, v67
	v_bfe_u32 v68, v66, 16, 1
	v_add3_u32 v66, v66, v68, s10
	v_bfe_u32 v68, v67, 16, 1
	v_lshrrev_b32_e32 v66, 16, v66
	v_add3_u32 v67, v67, v68, s10
	v_and_or_b32 v66, v67, s11, v66
	v_mul_f32_e32 v67, v96, v0
	v_mul_f32_e32 v67, v16, v67
	v_mul_f32_e32 v68, v97, v0
	v_mul_f32_e32 v68, v17, v68
	v_bfe_u32 v69, v67, 16, 1
	v_add3_u32 v67, v67, v69, s10
	v_bfe_u32 v69, v68, 16, 1
	v_lshrrev_b32_e32 v67, 16, v67
	v_add3_u32 v68, v68, v69, s10
	v_and_or_b32 v67, v68, s11, v67
	global_store_dwordx2 v[98:99], v[66:67], off offset:2048 sc0 sc1
	v_mul_f32_e32 v66, v90, v0
	v_mul_f32_e32 v66, v10, v66
	v_mul_f32_e32 v67, v91, v0
	v_mul_f32_e32 v67, v11, v67
	v_bfe_u32 v68, v66, 16, 1
	v_add3_u32 v66, v66, v68, s10
	v_bfe_u32 v68, v67, 16, 1
	v_lshrrev_b32_e32 v66, 16, v66
	v_add3_u32 v67, v67, v68, s10
	v_and_or_b32 v66, v67, s11, v66
	v_mul_f32_e32 v67, v92, v0
	v_mul_f32_e32 v67, v12, v67
	v_mul_f32_e32 v68, v93, v0
	v_mul_f32_e32 v68, v13, v68
	v_bfe_u32 v69, v67, 16, 1
	v_add3_u32 v67, v67, v69, s10
	v_bfe_u32 v69, v68, 16, 1
	v_lshrrev_b32_e32 v67, 16, v67
	v_add3_u32 v68, v68, v69, s10
	v_and_or_b32 v67, v68, s11, v67
	global_store_dwordx2 v[98:99], v[66:67], off offset:2560 sc0 sc1
	v_mul_f32_e32 v66, v86, v0
	v_mul_f32_e32 v66, v6, v66
	v_mul_f32_e32 v67, v87, v0
	v_mul_f32_e32 v67, v7, v67
	v_bfe_u32 v68, v66, 16, 1
	v_add3_u32 v66, v66, v68, s10
	v_bfe_u32 v68, v67, 16, 1
	v_lshrrev_b32_e32 v66, 16, v66
	v_add3_u32 v67, v67, v68, s10
	v_and_or_b32 v66, v67, s11, v66
	v_mul_f32_e32 v67, v88, v0
	v_mul_f32_e32 v67, v8, v67
	v_mul_f32_e32 v68, v89, v0
	v_mul_f32_e32 v68, v9, v68
	v_bfe_u32 v69, v67, 16, 1
	v_add3_u32 v67, v67, v69, s10
	v_bfe_u32 v69, v68, 16, 1
	v_lshrrev_b32_e32 v67, 16, v67
	v_add3_u32 v68, v68, v69, s10
	v_and_or_b32 v67, v68, s11, v67
	global_store_dwordx2 v[98:99], v[66:67], off offset:3072 sc0 sc1
	v_mul_f32_e32 v66, v82, v0
	v_mul_f32_e32 v66, v2, v66
	v_mul_f32_e32 v67, v83, v0
	v_mul_f32_e32 v67, v3, v67
	v_bfe_u32 v68, v66, 16, 1
	v_add3_u32 v66, v66, v68, s10
	v_bfe_u32 v68, v67, 16, 1
	v_lshrrev_b32_e32 v66, 16, v66
	v_add3_u32 v67, v67, v68, s10
	v_and_or_b32 v66, v67, s11, v66
	v_mul_f32_e32 v67, v84, v0
	v_mul_f32_e32 v67, v4, v67
	v_mul_f32_e32 v0, v85, v0
	v_mul_f32_e32 v0, v5, v0
	v_bfe_u32 v68, v67, 16, 1
	v_add3_u32 v67, v67, v68, s10
	v_bfe_u32 v68, v0, 16, 1
	v_lshrrev_b32_e32 v67, 16, v67
	v_add3_u32 v0, v0, v68, s10
	v_and_or_b32 v67, v0, s11, v67
	s_andn2_b64 vcc, exec, s[12:13]
	global_store_dwordx2 v[98:99], v[66:67], off offset:3584 sc0 sc1
	s_cbranch_vccnz .LBB0_95
	s_waitcnt vmcnt(31)
	v_mul_f32_e32 v0, v63, v63
	v_mul_f32_e32 v66, v65, v65
	v_fmac_f32_e32 v0, v62, v62
	v_fmac_f32_e32 v66, v64, v64
	v_add_f32_e32 v0, v0, v66
	s_waitcnt vmcnt(30)
	v_mul_f32_e32 v66, v59, v59
	v_mul_f32_e32 v67, v61, v61
	v_fmac_f32_e32 v66, v58, v58
	v_fmac_f32_e32 v67, v60, v60
	v_add_f32_e32 v66, v66, v67
	v_add_f32_e32 v0, v0, v66
	s_waitcnt vmcnt(29)
	v_mul_f32_e32 v66, v55, v55
	v_mul_f32_e32 v67, v57, v57
	v_fmac_f32_e32 v66, v54, v54
	v_fmac_f32_e32 v67, v56, v56
	v_add_f32_e32 v66, v66, v67
	v_add_f32_e32 v0, v0, v66
	s_waitcnt vmcnt(28)
	v_mul_f32_e32 v66, v47, v47
	v_mul_f32_e32 v67, v49, v49
	v_fmac_f32_e32 v66, v46, v46
	v_fmac_f32_e32 v67, v48, v48
	v_add_f32_e32 v66, v66, v67
	v_add_f32_e32 v0, v0, v66
	s_waitcnt vmcnt(27)
	v_mul_f32_e32 v66, v51, v51
	v_mul_f32_e32 v67, v53, v53
	v_fmac_f32_e32 v66, v50, v50
	v_fmac_f32_e32 v67, v52, v52
	v_add_f32_e32 v66, v66, v67
	v_add_f32_e32 v0, v0, v66
	s_waitcnt vmcnt(26)
	v_mul_f32_e32 v66, v43, v43
	v_mul_f32_e32 v67, v45, v45
	v_fmac_f32_e32 v66, v42, v42
	v_fmac_f32_e32 v67, v44, v44
	v_add_f32_e32 v66, v66, v67
	v_add_f32_e32 v0, v0, v66
	s_waitcnt vmcnt(25)
	v_mul_f32_e32 v66, v39, v39
	v_mul_f32_e32 v67, v41, v41
	v_fmac_f32_e32 v66, v38, v38
	v_fmac_f32_e32 v67, v40, v40
	v_add_f32_e32 v66, v66, v67
	v_add_f32_e32 v0, v0, v66
	s_waitcnt vmcnt(24)
	v_mul_f32_e32 v66, v35, v35
	v_mul_f32_e32 v67, v37, v37
	v_fmac_f32_e32 v66, v34, v34
	v_fmac_f32_e32 v67, v36, v36
	v_add_f32_e32 v66, v66, v67
	v_add_f32_e32 v0, v0, v66
	s_ashr_i32 s1, s0, 31
	s_lshl_b64 s[0:1], s[0:1], 12
	v_add_f32_dpp v0, v0, v0 quad_perm:[1,0,3,2] row_mask:0xf bank_mask:0xf bound_ctrl:1
	s_nop 1
	v_add_f32_dpp v0, v0, v0 quad_perm:[2,3,0,1] row_mask:0xf bank_mask:0xf bound_ctrl:1
	ds_swizzle_b32 v66, v0 offset:swizzle(SWAP,4)
	s_waitcnt lgkmcnt(0)
	v_add_f32_e32 v0, v0, v66
	ds_swizzle_b32 v66, v0 offset:swizzle(SWAP,8)
	s_waitcnt lgkmcnt(0)
	v_add_f32_e32 v0, v0, v66
	ds_swizzle_b32 v66, v0 offset:swizzle(SWAP,16)
	s_waitcnt lgkmcnt(0)
; __device__ __forceinline__ unsigned pk4_fp8(float a, float b, float c, float d) { int w = 0; w = __builtin_amdgcn_cvt_pk_fp8_f32(a, b, w, false); w = __builtin_amdgcn_cvt_pk_fp8_f32(c, d, w, true); return (unsigned)w; }
; #define GAS __attribute__((address_space(1)))
; __device__ __forceinline__ unsigned pk2(float lo, float hi) { return f2bf(lo) | (f2bf(hi) << 16); }
; #define lane (lane_id())
; template <bool F8, bool SRC16, int NR> __device__ __forceinline__ void norm_rows(const void* srcv, const float* gain, void* dstv, int vcu, int G, int wave, int lane) {
;     ...
;         for (int q = 0; q < NR; ++q) { const int m = m0 + q * NGW; if (m >= M) break;
;             float s = 0.f;
; #pragma unroll
;             for (int j = 0; j < 8; ++j) s += (v[q][j].x * v[q][j].x + v[q][j].y * v[q][j].y) + (v[q][j].z * v[q][j].z + v[q][j].w * v[q][j].w);
;             const float r = 1.0f / sqrtf(wave_sum(s) * (1.0f / D) + EPS);
;             if constexpr (F8) { GAS unsigned* o4 = (GAS unsigned*)((unsigned char*)dstv + (size_t)m * D) + lane;
; #pragma unroll
;                 for (int j = 0; j < 8; ++j) o4[64 * j] = pg8::pk4_fp8(v[q][j].x * r * g[j].x, v[q][j].y * r * g[j].y, v[q][j].z * r * g[j].z, v[q][j].w * r * g[j].w); }
;             else { GAS unsigned long long* o8 = (GAS unsigned long long*)((bf16*)dstv + (size_t)m * D) + lane;
; #pragma unroll
;                 for (int j = 0; j < 8; ++j) o8[64 * j] = (unsigned long long)pk2(v[q][j].x * r * g[j].x, v[q][j].y * r * g[j].y) | ((unsigned long long)pk2(v[q][j].z * r * g[j].z, v[q][j].w * r * g[j].w) << 32); }
	v_add_f32_e32 v0, v0, v66
	v_mov_b32_e32 v66, v0
	s_nop 1
	v_permlane32_swap_b32_e32 v0, v66
	v_add_f32_e32 v0, v0, v66
	v_fmamk_f32 v0, v0, 0x3a000000, v204
	v_mul_f32_e32 v66, 0x4f800000, v0
	v_cmp_gt_f32_e32 vcc, s9, v0
	s_nop 1
	v_cndmask_b32_e32 v0, v0, v66, vcc
	v_sqrt_f32_e32 v66, v0
	s_nop 0
	v_add_u32_e32 v67, -1, v66
	v_fma_f32 v68, -v67, v66, v0
	v_cmp_ge_f32_e64 s[36:37], 0, v68
	v_add_u32_e32 v68, 1, v66
	s_nop 0
	v_cndmask_b32_e64 v67, v66, v67, s[36:37]
	v_fma_f32 v66, -v68, v66, v0
	v_cmp_lt_f32_e64 s[36:37], 0, v66
	s_nop 1
	v_cndmask_b32_e64 v66, v67, v68, s[36:37]
	v_mul_f32_e32 v67, 0x37800000, v66
	v_cndmask_b32_e32 v66, v66, v67, vcc
	v_cmp_class_f32_e32 vcc, v0, v205
	s_nop 1
	v_cndmask_b32_e32 v0, v66, v0, vcc
	v_div_scale_f32 v66, s[12:13], v0, v0, 1.0
	v_rcp_f32_e32 v67, v66
	s_nop 0
	v_fma_f32 v68, -v66, v67, 1.0
	v_fmac_f32_e32 v67, v68, v67
	v_div_scale_f32 v68, vcc, 1.0, v0, 1.0
	v_mul_f32_e32 v69, v68, v67
	v_fma_f32 v70, -v66, v69, v68
	v_fmac_f32_e32 v69, v70, v67
	v_fma_f32 v66, -v66, v69, v68
	v_div_fmas_f32 v66, v66, v67, v69
	v_div_fixup_f32 v0, v66, v0, 1.0
	v_mul_f32_e32 v62, v62, v0
	v_mul_f32_e32 v62, v30, v62
	v_mul_f32_e32 v63, v63, v0
	v_mul_f32_e32 v63, v31, v63
	v_bfe_u32 v68, v62, 16, 1
	v_add3_u32 v62, v62, v68, s10
	v_bfe_u32 v68, v63, 16, 1
	v_lshrrev_b32_e32 v62, 16, v62
	v_add3_u32 v63, v63, v68, s10
	v_and_or_b32 v62, v63, s11, v62
	v_mul_f32_e32 v63, v64, v0
	v_mul_f32_e32 v63, v32, v63
	v_mul_f32_e32 v64, v65, v0
	v_mul_f32_e32 v64, v33, v64
	v_bfe_u32 v65, v63, 16, 1
	v_add3_u32 v63, v63, v65, s10
	v_bfe_u32 v65, v64, 16, 1
	v_lshrrev_b32_e32 v63, 16, v63
	v_add3_u32 v64, v64, v65, s10
	v_mul_f32_e32 v58, v58, v0
	v_lshl_add_u64 v[66:67], v[172:173], 0, s[0:1]
	v_and_or_b32 v63, v64, s11, v63
	v_mul_f32_e32 v58, v26, v58
	v_mul_f32_e32 v59, v59, v0
	global_store_dwordx2 v[66:67], v[62:63], off sc0 sc1
	v_mul_f32_e32 v59, v27, v59
	v_bfe_u32 v62, v58, 16, 1
	v_add3_u32 v58, v58, v62, s10
	v_bfe_u32 v62, v59, 16, 1
	v_lshrrev_b32_e32 v58, 16, v58
	v_add3_u32 v59, v59, v62, s10
	v_and_or_b32 v58, v59, s11, v58
	v_mul_f32_e32 v59, v60, v0
	v_mul_f32_e32 v59, v28, v59
	v_mul_f32_e32 v60, v61, v0
	v_mul_f32_e32 v60, v29, v60
	v_bfe_u32 v61, v59, 16, 1
	v_add3_u32 v59, v59, v61, s10
	v_bfe_u32 v61, v60, 16, 1
	v_lshrrev_b32_e32 v59, 16, v59
	v_add3_u32 v60, v60, v61, s10
	v_mul_f32_e32 v54, v54, v0
	v_and_or_b32 v59, v60, s11, v59
	v_mul_f32_e32 v54, v22, v54
	v_mul_f32_e32 v55, v55, v0
	global_store_dwordx2 v[66:67], v[58:59], off offset:512 sc0 sc1
	v_mul_f32_e32 v55, v23, v55
	v_bfe_u32 v58, v54, 16, 1
	v_add3_u32 v54, v54, v58, s10
	v_bfe_u32 v58, v55, 16, 1
	v_lshrrev_b32_e32 v54, 16, v54
	v_add3_u32 v55, v55, v58, s10
	v_and_or_b32 v54, v55, s11, v54
	v_mul_f32_e32 v55, v56, v0
	v_mul_f32_e32 v55, v24, v55
	v_mul_f32_e32 v56, v57, v0
	v_mul_f32_e32 v56, v25, v56
	v_bfe_u32 v57, v55, 16, 1
	v_add3_u32 v55, v55, v57, s10
	v_bfe_u32 v57, v56, 16, 1
	v_lshrrev_b32_e32 v55, 16, v55
	v_add3_u32 v56, v56, v57, s10
	v_mul_f32_e32 v46, v46, v0
	v_and_or_b32 v55, v56, s11, v55
	v_mul_f32_e32 v46, v18, v46
	v_mul_f32_e32 v47, v47, v0
	global_store_dwordx2 v[66:67], v[54:55], off offset:1024 sc0 sc1
	v_mul_f32_e32 v47, v19, v47
	v_bfe_u32 v54, v46, 16, 1
	v_add3_u32 v46, v46, v54, s10
	v_bfe_u32 v54, v47, 16, 1
	v_lshrrev_b32_e32 v46, 16, v46
	v_add3_u32 v47, v47, v54, s10
	v_and_or_b32 v46, v47, s11, v46
	v_mul_f32_e32 v47, v48, v0
	v_mul_f32_e32 v47, v20, v47
	v_mul_f32_e32 v48, v49, v0
	v_mul_f32_e32 v48, v21, v48
	v_bfe_u32 v49, v47, 16, 1
	v_add3_u32 v47, v47, v49, s10
	v_bfe_u32 v49, v48, 16, 1
	v_lshrrev_b32_e32 v47, 16, v47
	v_add3_u32 v48, v48, v49, s10
	v_and_or_b32 v47, v48, s11, v47
	global_store_dwordx2 v[66:67], v[46:47], off offset:1536 sc0 sc1
	v_mul_f32_e32 v46, v50, v0
	v_mul_f32_e32 v46, v14, v46
	v_mul_f32_e32 v47, v51, v0
	v_mul_f32_e32 v47, v15, v47
	v_bfe_u32 v48, v46, 16, 1
	v_add3_u32 v46, v46, v48, s10
	v_bfe_u32 v48, v47, 16, 1
	v_lshrrev_b32_e32 v46, 16, v46
	v_add3_u32 v47, v47, v48, s10
	v_and_or_b32 v46, v47, s11, v46
	v_mul_f32_e32 v47, v52, v0
	v_mul_f32_e32 v47, v16, v47
	v_mul_f32_e32 v48, v53, v0
	v_mul_f32_e32 v48, v17, v48
	v_bfe_u32 v49, v47, 16, 1
	v_add3_u32 v47, v47, v49, s10
	v_bfe_u32 v49, v48, 16, 1
	v_lshrrev_b32_e32 v47, 16, v47
	v_add3_u32 v48, v48, v49, s10
	v_mul_f32_e32 v42, v42, v0
	v_and_or_b32 v47, v48, s11, v47
	v_mul_f32_e32 v42, v10, v42
	v_mul_f32_e32 v43, v43, v0
	global_store_dwordx2 v[66:67], v[46:47], off offset:2048 sc0 sc1
	v_mul_f32_e32 v43, v11, v43
	v_bfe_u32 v46, v42, 16, 1
	v_add3_u32 v42, v42, v46, s10
	v_bfe_u32 v46, v43, 16, 1
	v_lshrrev_b32_e32 v42, 16, v42
	v_add3_u32 v43, v43, v46, s10
	v_and_or_b32 v42, v43, s11, v42
	v_mul_f32_e32 v43, v44, v0
	v_mul_f32_e32 v43, v12, v43
	v_mul_f32_e32 v44, v45, v0
	v_mul_f32_e32 v44, v13, v44
	v_bfe_u32 v45, v43, 16, 1
	v_add3_u32 v43, v43, v45, s10
	v_bfe_u32 v45, v44, 16, 1
	v_lshrrev_b32_e32 v43, 16, v43
	v_add3_u32 v44, v44, v45, s10
	v_mul_f32_e32 v38, v38, v0
	v_and_or_b32 v43, v44, s11, v43
	v_mul_f32_e32 v38, v6, v38
	v_mul_f32_e32 v39, v39, v0
	global_store_dwordx2 v[66:67], v[42:43], off offset:2560 sc0 sc1
	v_mul_f32_e32 v39, v7, v39
	v_bfe_u32 v42, v38, 16, 1
	v_add3_u32 v38, v38, v42, s10
	v_bfe_u32 v42, v39, 16, 1
	v_lshrrev_b32_e32 v38, 16, v38
	v_add3_u32 v39, v39, v42, s10
	v_and_or_b32 v38, v39, s11, v38
	v_mul_f32_e32 v39, v40, v0
	v_mul_f32_e32 v39, v8, v39
	v_mul_f32_e32 v40, v41, v0
	v_mul_f32_e32 v40, v9, v40
	v_bfe_u32 v41, v39, 16, 1
	v_add3_u32 v39, v39, v41, s10
	v_bfe_u32 v41, v40, 16, 1
	v_lshrrev_b32_e32 v39, 16, v39
	v_add3_u32 v40, v40, v41, s10
	v_mul_f32_e32 v34, v34, v0
	v_and_or_b32 v39, v40, s11, v39
	v_mul_f32_e32 v34, v2, v34
	v_mul_f32_e32 v35, v35, v0
	global_store_dwordx2 v[66:67], v[38:39], off offset:3072 sc0 sc1
	v_mul_f32_e32 v35, v3, v35
	v_bfe_u32 v38, v34, 16, 1
	v_add3_u32 v34, v34, v38, s10
	v_bfe_u32 v38, v35, 16, 1
	v_lshrrev_b32_e32 v34, 16, v34
	v_add3_u32 v35, v35, v38, s10
	v_and_or_b32 v34, v35, s11, v34
	v_mul_f32_e32 v35, v36, v0
	v_mul_f32_e32 v35, v4, v35
	v_mul_f32_e32 v0, v37, v0
	v_mul_f32_e32 v0, v5, v0
	v_bfe_u32 v36, v35, 16, 1
	v_add3_u32 v35, v35, v36, s10
	v_bfe_u32 v36, v0, 16, 1
	v_lshrrev_b32_e32 v35, 16, v35
	v_add3_u32 v0, v0, v36, s10
	v_and_or_b32 v35, v0, s11, v35
	global_store_dwordx2 v[66:67], v[34:35], off offset:3584 sc0 sc1
	s_branch .LBB0_95

; __device__ __forceinline__ void dcombine_phase(const Ptrs& P, const float* gain, int vcu, int G, int wave, int lane, const bool ob8) {
;     ...
;         for (int q = 0; q < NQ; ++q) { if (it0 + q * NGW >= NIT) break;
;             const float mx = fmaxf(fmaxf(ls[q][0], ls[q][1]), fmaxf(ls[q][2], ls[q][3]));
;             float w0 = __builtin_amdgcn_exp2f(ls[q][0] - mx), w1 = __builtin_amdgcn_exp2f(ls[q][1] - mx), w2 = __builtin_amdgcn_exp2f(ls[q][2] - mx), w3 = __builtin_amdgcn_exp2f(ls[q][3] - mx);
;             const float inv = 1.0f / (w0 + w1 + w2 + w3); w0 *= inv; w1 *= inv; w2 *= inv; w3 *= inv;
;             float acc[8];
; #pragma unroll
;             for (int e = 0; e < 8; ++e) acc[e] = 0.f;
; #pragma unroll
;             for (int p = 0; p < 4; ++p) { const v4u r_ = raw[q][p]; const float w = (p == 0) ? w0 : ((p == 1) ? w1 : ((p == 2) ? w2 : w3));
;                 acc[0] += w * bf2f_u((unsigned short)(r_.x & 0xffff)); acc[1] += w * bf2f_u((unsigned short)(r_.x >> 16)); acc[2] += w * bf2f_u((unsigned short)(r_.y & 0xffff)); acc[3] += w * bf2f_u((unsigned short)(r_.y >> 16));
;                 acc[4] += w * bf2f_u((unsigned short)(r_.z & 0xffff)); acc[5] += w * bf2f_u((unsigned short)(r_.z >> 16)); acc[6] += w * bf2f_u((unsigned short)(r_.w & 0xffff)); acc[7] += w * bf2f_u((unsigned short)(r_.w >> 16)); }
;             float ss = 0.f;
; #pragma unroll
;             for (int e = 0; e < 8; ++e) ss = fmaf(acc[e], acc[e], ss);
;             ss += xor_get<1>(ss); ss += xor_get<2>(ss); ss += xor_get<4>(ss); ss += xor_get<8>(ss);
;             const float rn = 1.0f / sqrtf(ss * (1.0f / 128.0f) + EPS);
;             const f32x4 g0 = *(const f32x4*)(gain + hh[q] * 128 + 8 * c), g1 = *(const f32x4*)(gain + hh[q] * 128 + 8 * c + 4);
;             v4u o; o.x = pk2(acc[0] * rn * g0.x, acc[1] * rn * g0.y); o.y = pk2(acc[2] * rn * g0.z, acc[3] * rn * g0.w); o.z = pk2(acc[4] * rn * g1.x, acc[5] * rn * g1.y); o.w = pk2(acc[6] * rn * g1.z, acc[7] * rn * g1.w);
;             if (ob8) { typedef unsigned u32x2_o __attribute__((ext_vector_type(2))); u32x2_o o8; o8.x = pg8::pk4_fp8(acc[0] * rn * g0.x, acc[1] * rn * g0.y, acc[2] * rn * g0.z, acc[3] * rn * g0.w); o8.y = pg8::pk4_fp8(acc[4] * rn * g1.x, acc[5] * rn * g1.y, acc[6] * rn * g1.z, acc[7] * rn * g1.w);
;                 *(GAS u32x2_o*)((unsigned char*)P.OB + (size_t)tok[q] * D + hh[q] * 128 + 8 * c) = o8; }
.LBB0_1230:
	s_or_b64 exec, exec, s[18:19]
	s_waitcnt vmcnt(19)
	v_max_f32_e32 v92, v109, v109
	v_max_f32_e32 v93, v108, v108
	v_max_f32_e32 v92, v93, v92
	v_max3_f32 v92, v106, v107, v92
	v_sub_f32_e32 v93, v106, v92
	v_sub_f32_e32 v94, v107, v92
	v_exp_f32_e32 v93, v93
	v_exp_f32_e32 v112, v94
	v_sub_f32_e32 v94, v108, v92
	v_exp_f32_e32 v113, v94
	v_sub_f32_e32 v92, v109, v92
	v_exp_f32_e32 v123, v92
	v_add_f32_e32 v92, v93, v112
	v_add_f32_e32 v92, v113, v92
	v_lshlrev_b32_e32 v109, 16, v65
	v_add_f32_e32 v92, v123, v92
	v_div_scale_f32 v94, s[18:19], v92, v92, 1.0
	v_rcp_f32_e32 v95, v94
	v_and_b32_e32 v111, 0xffff0000, v65
	v_and_b32_e32 v110, 0xffff0000, v64
	v_lshlrev_b32_e32 v115, 16, v59
	v_fma_f32 v106, -v94, v95, 1.0
	v_fmac_f32_e32 v95, v106, v95
	v_div_scale_f32 v106, vcc, 1.0, v92, 1.0
	v_mul_f32_e32 v107, v106, v95
	v_fma_f32 v108, -v94, v107, v106
	v_fmac_f32_e32 v107, v108, v95
	v_fma_f32 v94, -v94, v107, v106
	v_div_fmas_f32 v94, v94, v95, v107
	v_div_fixup_f32 v128, v94, v92, 1.0
	v_lshlrev_b32_e32 v95, 16, v63
	v_lshlrev_b32_e32 v94, 16, v62
	v_and_b32_e32 v107, 0xffff0000, v63
	v_and_b32_e32 v106, 0xffff0000, v62
	v_lshl_add_u64 v[62:63], v[90:91], 2, v[68:69]
	v_lshlrev_b32_e32 v108, 16, v64
	v_lshlrev_b32_e32 v114, 16, v58
	v_and_b32_e32 v117, 0xffff0000, v59
	v_and_b32_e32 v116, 0xffff0000, v58
	v_lshlrev_b32_e32 v119, 16, v61
	v_lshlrev_b32_e32 v118, 16, v60
	v_and_b32_e32 v121, 0xffff0000, v61
	v_and_b32_e32 v120, 0xffff0000, v60
	global_load_dwordx4 v[58:61], v[62:63], off offset:16
	s_nop 0
	global_load_dwordx4 v[62:65], v[62:63], off
	v_mul_f32_e32 v92, v93, v128
	v_mul_f32_e32 v112, v112, v128
	v_pk_fma_f32 v[94:95], v[92:93], v[94:95], 0 op_sel_hi:[0,1,0]
	v_pk_fma_f32 v[106:107], v[92:93], v[106:107], 0 op_sel_hi:[0,1,0]
	v_mul_f32_e32 v122, v113, v128
	s_waitcnt vmcnt(20)
	v_lshlrev_b32_e32 v124, 16, v54
	v_and_b32_e32 v54, 0xffff0000, v54
	v_lshlrev_b32_e32 v125, 16, v55
	v_and_b32_e32 v55, 0xffff0000, v55
	v_pk_fma_f32 v[94:95], v[112:113], v[114:115], v[94:95] op_sel_hi:[0,1,1]
	v_pk_fma_f32 v[106:107], v[112:113], v[116:117], v[106:107] op_sel_hi:[0,1,1]
	v_mul_f32_e32 v128, v123, v128
	v_pk_fma_f32 v[94:95], v[122:123], v[124:125], v[94:95] op_sel_hi:[0,1,1]
	v_pk_fma_f32 v[54:55], v[122:123], v[54:55], v[106:107] op_sel_hi:[0,1,1]
	v_lshlrev_b32_e32 v107, 16, v51
	v_lshlrev_b32_e32 v106, 16, v50
	v_pk_fma_f32 v[94:95], v[128:129], v[106:107], v[94:95] op_sel_hi:[0,1,1]
	v_and_b32_e32 v51, 0xffff0000, v51
	v_and_b32_e32 v50, 0xffff0000, v50
	v_pk_fma_f32 v[50:51], v[128:129], v[50:51], v[54:55] op_sel_hi:[0,1,1]
	v_fma_f32 v106, v94, v94, 0
	v_pk_fma_f32 v[54:55], v[92:93], v[108:109], 0 op_sel_hi:[0,1,0]
	v_pk_fma_f32 v[92:93], v[92:93], v[110:111], 0 op_sel_hi:[0,1,0]
	v_lshlrev_b32_e32 v126, 16, v56
	v_and_b32_e32 v56, 0xffff0000, v56
	v_lshlrev_b32_e32 v127, 16, v57
	v_and_b32_e32 v57, 0xffff0000, v57
	v_fmac_f32_e32 v106, v50, v50
	v_pk_fma_f32 v[54:55], v[112:113], v[118:119], v[54:55] op_sel_hi:[0,1,1]
	v_pk_fma_f32 v[92:93], v[112:113], v[120:121], v[92:93] op_sel_hi:[0,1,1]
	v_fmac_f32_e32 v106, v95, v95
	v_pk_fma_f32 v[54:55], v[122:123], v[126:127], v[54:55] op_sel_hi:[0,1,1]
	v_pk_fma_f32 v[56:57], v[122:123], v[56:57], v[92:93] op_sel_hi:[0,1,1]
	v_lshlrev_b32_e32 v93, 16, v53
	v_lshlrev_b32_e32 v92, 16, v52
	v_fmac_f32_e32 v106, v51, v51
	v_pk_fma_f32 v[54:55], v[128:129], v[92:93], v[54:55] op_sel_hi:[0,1,1]
	v_and_b32_e32 v53, 0xffff0000, v53
	v_and_b32_e32 v52, 0xffff0000, v52
	v_pk_fma_f32 v[52:53], v[128:129], v[52:53], v[56:57] op_sel_hi:[0,1,1]
	v_fmac_f32_e32 v106, v54, v54
	v_fmac_f32_e32 v106, v52, v52
	v_fmac_f32_e32 v106, v55, v55
	v_fmac_f32_e32 v106, v53, v53
	s_cmpk_gt_i32 s23, 0x57ff
	s_nop 0
	v_add_f32_dpp v56, v106, v106 quad_perm:[1,0,3,2] row_mask:0xf bank_mask:0xf bound_ctrl:1
	s_nop 1
	v_add_f32_dpp v56, v56, v56 quad_perm:[2,3,0,1] row_mask:0xf bank_mask:0xf bound_ctrl:1
	ds_swizzle_b32 v57, v56 offset:swizzle(SWAP,4)
	s_waitcnt lgkmcnt(0)
	v_add_f32_e32 v56, v56, v57
	ds_swizzle_b32 v57, v56 offset:swizzle(SWAP,8)
	s_waitcnt lgkmcnt(0)
	v_add_f32_e32 v56, v56, v57
	v_fmamk_f32 v56, v56, 0x3c000000, v204
	v_mul_f32_e32 v57, 0x4f800000, v56
	v_cmp_gt_f32_e32 vcc, s9, v56
	s_nop 1
	v_cndmask_b32_e32 v56, v56, v57, vcc
	v_sqrt_f32_e32 v57, v56
	s_nop 0
	v_add_u32_e32 v92, -1, v57
	v_fma_f32 v93, -v92, v57, v56
	v_cmp_ge_f32_e64 s[38:39], 0, v93
	v_add_u32_e32 v93, 1, v57
	s_nop 0
	v_cndmask_b32_e64 v92, v57, v92, s[38:39]
	v_fma_f32 v57, -v93, v57, v56
	v_cmp_lt_f32_e64 s[38:39], 0, v57
	s_nop 1
	v_cndmask_b32_e64 v57, v92, v93, s[38:39]
	v_mul_f32_e32 v92, 0x37800000, v57
	v_cndmask_b32_e32 v57, v57, v92, vcc
	v_cmp_class_f32_e32 vcc, v56, v205
	s_nop 1
	v_cndmask_b32_e32 v92, v57, v56, vcc
	v_div_scale_f32 v93, s[18:19], v92, v92, 1.0
	v_rcp_f32_e32 v106, v93
	s_waitcnt vmcnt(0)
	v_mov_b32_e32 v56, v62
	v_mov_b32_e32 v57, v64
	v_mov_b32_e32 v64, v63
	v_fma_f32 v62, -v93, v106, 1.0
	v_fmac_f32_e32 v106, v62, v106
	v_div_scale_f32 v62, vcc, 1.0, v92, 1.0
	v_mul_f32_e32 v63, v62, v106
	v_fma_f32 v107, -v93, v63, v62
	v_fmac_f32_e32 v63, v107, v106
	v_fma_f32 v62, -v93, v63, v62
	v_div_fmas_f32 v62, v62, v106, v63
	v_div_fixup_f32 v62, v62, v92, 1.0
	v_pk_mul_f32 v[50:51], v[50:51], v[62:63] op_sel_hi:[1,0]
	v_pk_mul_f32 v[54:55], v[54:55], v[62:63] op_sel_hi:[1,0]
	v_pk_mul_f32 v[50:51], v[64:65], v[50:51]
	v_mov_b32_e32 v64, v58
	v_mov_b32_e32 v65, v60
	v_pk_mul_f32 v[52:53], v[52:53], v[62:63] op_sel_hi:[1,0]
	v_mov_b32_e32 v60, v59
	v_pk_mul_f32 v[54:55], v[64:65], v[54:55]
	v_pk_mul_f32 v[52:53], v[60:61], v[52:53]
	v_bfe_u32 v60, v51, 16, 1
	v_bfe_u32 v61, v50, 16, 1
	v_add3_u32 v50, v50, v61, s10
	v_add3_u32 v51, v51, v60, s10
	v_bfe_u32 v60, v54, 16, 1
	v_bfe_u32 v61, v55, 16, 1
	v_pk_mul_f32 v[92:93], v[94:95], v[62:63] op_sel_hi:[1,0]
	v_bfe_u32 v58, v53, 16, 1
	v_bfe_u32 v59, v52, 16, 1
	v_add3_u32 v55, v55, v61, s10
	v_add3_u32 v54, v54, v60, s10
	v_pk_mul_f32 v[56:57], v[56:57], v[92:93]
	v_add3_u32 v52, v52, v59, s10
	v_add3_u32 v53, v53, v58, s10
	v_lshrrev_b32_e32 v54, 16, v54
	v_lshrrev_b32_e32 v55, 16, v55
	v_bfe_u32 v58, v56, 16, 1
	v_bfe_u32 v59, v57, 16, 1
	v_and_or_b32 v53, v53, s11, v55
	v_and_or_b32 v52, v52, s11, v54
	v_lshlrev_b64 v[54:55], 12, v[88:89]
	v_add3_u32 v57, v57, v59, s10
	v_add3_u32 v56, v56, v58, s10
	v_lshl_add_u64 v[54:55], s[0:1], 0, v[54:55]
	v_lshrrev_b32_e32 v56, 16, v56
	v_lshrrev_b32_e32 v57, 16, v57
	v_lshl_add_u64 v[54:55], v[90:91], 1, v[54:55]
	v_and_or_b32 v51, v51, s11, v57
	v_and_or_b32 v50, v50, s11, v56
	v_lshl_add_u64 v[54:55], v[54:55], 0, v[0:1]
	global_store_dwordx4 v[54:55], v[50:53], off sc0 sc1
	s_cbranch_scc1 .LBB0_1221
; __device__ __forceinline__ void dcombine_phase(const Ptrs& P, const float* gain, int vcu, int G, int wave, int lane, const bool ob8) {
;     ...
;         for (int q = 0; q < NQ; ++q) { if (it0 + q * NGW >= NIT) break;
;             const float mx = fmaxf(fmaxf(ls[q][0], ls[q][1]), fmaxf(ls[q][2], ls[q][3]));
;             float w0 = __builtin_amdgcn_exp2f(ls[q][0] - mx), w1 = __builtin_amdgcn_exp2f(ls[q][1] - mx), w2 = __builtin_amdgcn_exp2f(ls[q][2] - mx), w3 = __builtin_amdgcn_exp2f(ls[q][3] - mx);
;             const float inv = 1.0f / (w0 + w1 + w2 + w3); w0 *= inv; w1 *= inv; w2 *= inv; w3 *= inv;
;             float acc[8];
; #pragma unroll
;             for (int e = 0; e < 8; ++e) acc[e] = 0.f;
; #pragma unroll
;             for (int p = 0; p < 4; ++p) { const v4u r_ = raw[q][p]; const float w = (p == 0) ? w0 : ((p == 1) ? w1 : ((p == 2) ? w2 : w3));
;                 acc[0] += w * bf2f_u((unsigned short)(r_.x & 0xffff)); acc[1] += w * bf2f_u((unsigned short)(r_.x >> 16)); acc[2] += w * bf2f_u((unsigned short)(r_.y & 0xffff)); acc[3] += w * bf2f_u((unsigned short)(r_.y >> 16));
;                 acc[4] += w * bf2f_u((unsigned short)(r_.z & 0xffff)); acc[5] += w * bf2f_u((unsigned short)(r_.z >> 16)); acc[6] += w * bf2f_u((unsigned short)(r_.w & 0xffff)); acc[7] += w * bf2f_u((unsigned short)(r_.w >> 16)); }
;             float ss = 0.f;
; #pragma unroll
;             for (int e = 0; e < 8; ++e) ss = fmaf(acc[e], acc[e], ss);
;             ss += xor_get<1>(ss); ss += xor_get<2>(ss); ss += xor_get<4>(ss); ss += xor_get<8>(ss);
;             const float rn = 1.0f / sqrtf(ss * (1.0f / 128.0f) + EPS);
;             const f32x4 g0 = *(const f32x4*)(gain + hh[q] * 128 + 8 * c), g1 = *(const f32x4*)(gain + hh[q] * 128 + 8 * c + 4);
;             v4u o; o.x = pk2(acc[0] * rn * g0.x, acc[1] * rn * g0.y); o.y = pk2(acc[2] * rn * g0.z, acc[3] * rn * g0.w); o.z = pk2(acc[4] * rn * g1.x, acc[5] * rn * g1.y); o.w = pk2(acc[6] * rn * g1.z, acc[7] * rn * g1.w);
;             if (ob8) { typedef unsigned u32x2_o __attribute__((ext_vector_type(2))); u32x2_o o8; o8.x = pg8::pk4_fp8(acc[0] * rn * g0.x, acc[1] * rn * g0.y, acc[2] * rn * g0.z, acc[3] * rn * g0.w); o8.y = pg8::pk4_fp8(acc[4] * rn * g1.x, acc[5] * rn * g1.y, acc[6] * rn * g1.z, acc[7] * rn * g1.w);
;                 *(GAS u32x2_o*)((unsigned char*)P.OB + (size_t)tok[q] * D + hh[q] * 128 + 8 * c) = o8; }
	s_nop 0
	v_max_f32_e32 v50, v102, v102
	v_max_f32_e32 v51, v105, v105
	v_max_f32_e32 v50, v51, v50
	v_max3_f32 v50, v103, v104, v50
	v_sub_f32_e32 v51, v103, v50
	v_sub_f32_e32 v52, v104, v50
	v_exp_f32_e32 v51, v51
	v_exp_f32_e32 v60, v52
	v_sub_f32_e32 v52, v105, v50
	v_exp_f32_e32 v61, v52
	v_sub_f32_e32 v50, v102, v50
	v_exp_f32_e32 v93, v50
	v_add_f32_e32 v50, v51, v60
	v_add_f32_e32 v50, v61, v50
	v_lshlrev_b32_e32 v57, 16, v49
	v_add_f32_e32 v50, v93, v50
	v_div_scale_f32 v52, s[18:19], v50, v50, 1.0
	v_rcp_f32_e32 v53, v52
	v_and_b32_e32 v59, 0xffff0000, v49
	v_and_b32_e32 v58, 0xffff0000, v48
	v_lshlrev_b32_e32 v63, 16, v43
	v_fma_f32 v54, -v52, v53, 1.0
	v_fmac_f32_e32 v53, v54, v53
	v_div_scale_f32 v54, vcc, 1.0, v50, 1.0
	v_mul_f32_e32 v55, v54, v53
	v_fma_f32 v56, -v52, v55, v54
	v_fmac_f32_e32 v55, v56, v53
	v_fma_f32 v52, -v52, v55, v54
	v_div_fmas_f32 v52, v52, v53, v55
	v_div_fixup_f32 v104, v52, v50, 1.0
	v_lshlrev_b32_e32 v53, 16, v47
	v_lshlrev_b32_e32 v52, 16, v46
	v_and_b32_e32 v55, 0xffff0000, v47
	v_and_b32_e32 v54, 0xffff0000, v46
	v_lshl_add_u64 v[46:47], v[86:87], 2, v[68:69]
	v_lshlrev_b32_e32 v56, 16, v48
	v_lshlrev_b32_e32 v62, 16, v42
	v_and_b32_e32 v65, 0xffff0000, v43
	v_and_b32_e32 v64, 0xffff0000, v42
	v_lshlrev_b32_e32 v89, 16, v45
	v_lshlrev_b32_e32 v88, 16, v44
	v_and_b32_e32 v91, 0xffff0000, v45
	v_and_b32_e32 v90, 0xffff0000, v44
	global_load_dwordx4 v[42:45], v[46:47], off offset:16
	s_nop 0
	global_load_dwordx4 v[46:49], v[46:47], off
	v_mul_f32_e32 v50, v51, v104
	v_mul_f32_e32 v60, v60, v104
	v_pk_fma_f32 v[52:53], v[50:51], v[52:53], 0 op_sel_hi:[0,1,0]
	v_pk_fma_f32 v[54:55], v[50:51], v[54:55], 0 op_sel_hi:[0,1,0]
	v_mul_f32_e32 v92, v61, v104
	v_lshlrev_b32_e32 v94, 16, v38
	v_and_b32_e32 v38, 0xffff0000, v38
	v_lshlrev_b32_e32 v95, 16, v39
	v_and_b32_e32 v39, 0xffff0000, v39
	v_pk_fma_f32 v[52:53], v[60:61], v[62:63], v[52:53] op_sel_hi:[0,1,1]
	v_pk_fma_f32 v[54:55], v[60:61], v[64:65], v[54:55] op_sel_hi:[0,1,1]
	v_mul_f32_e32 v104, v93, v104
	v_pk_fma_f32 v[52:53], v[92:93], v[94:95], v[52:53] op_sel_hi:[0,1,1]
	v_pk_fma_f32 v[38:39], v[92:93], v[38:39], v[54:55] op_sel_hi:[0,1,1]
	v_lshlrev_b32_e32 v55, 16, v23
	v_lshlrev_b32_e32 v54, 16, v22
	v_pk_fma_f32 v[52:53], v[104:105], v[54:55], v[52:53] op_sel_hi:[0,1,1]
	v_and_b32_e32 v23, 0xffff0000, v23
	v_and_b32_e32 v22, 0xffff0000, v22
	v_pk_fma_f32 v[22:23], v[104:105], v[22:23], v[38:39] op_sel_hi:[0,1,1]
	v_fma_f32 v54, v52, v52, 0
	v_pk_fma_f32 v[38:39], v[50:51], v[56:57], 0 op_sel_hi:[0,1,0]
	v_pk_fma_f32 v[50:51], v[50:51], v[58:59], 0 op_sel_hi:[0,1,0]
	v_lshlrev_b32_e32 v102, 16, v40
	v_and_b32_e32 v40, 0xffff0000, v40
	v_lshlrev_b32_e32 v103, 16, v41
	v_and_b32_e32 v41, 0xffff0000, v41
	v_fmac_f32_e32 v54, v22, v22
	v_pk_fma_f32 v[38:39], v[60:61], v[88:89], v[38:39] op_sel_hi:[0,1,1]
	v_pk_fma_f32 v[50:51], v[60:61], v[90:91], v[50:51] op_sel_hi:[0,1,1]
	v_fmac_f32_e32 v54, v53, v53
	v_pk_fma_f32 v[38:39], v[92:93], v[102:103], v[38:39] op_sel_hi:[0,1,1]
	v_pk_fma_f32 v[40:41], v[92:93], v[40:41], v[50:51] op_sel_hi:[0,1,1]
	v_lshlrev_b32_e32 v51, 16, v25
	v_lshlrev_b32_e32 v50, 16, v24
	v_fmac_f32_e32 v54, v23, v23
	v_pk_fma_f32 v[38:39], v[104:105], v[50:51], v[38:39] op_sel_hi:[0,1,1]
	v_and_b32_e32 v25, 0xffff0000, v25
	v_and_b32_e32 v24, 0xffff0000, v24
	v_pk_fma_f32 v[24:25], v[104:105], v[24:25], v[40:41] op_sel_hi:[0,1,1]
	v_fmac_f32_e32 v54, v38, v38
	v_fmac_f32_e32 v54, v24, v24
	v_fmac_f32_e32 v54, v39, v39
	v_fmac_f32_e32 v54, v25, v25
	s_cmpk_gt_i32 s22, 0x57ff
	s_nop 0
	v_add_f32_dpp v40, v54, v54 quad_perm:[1,0,3,2] row_mask:0xf bank_mask:0xf bound_ctrl:1
	s_nop 1
	v_add_f32_dpp v40, v40, v40 quad_perm:[2,3,0,1] row_mask:0xf bank_mask:0xf bound_ctrl:1
	ds_swizzle_b32 v41, v40 offset:swizzle(SWAP,4)
	s_waitcnt lgkmcnt(0)
	v_add_f32_e32 v40, v40, v41
	ds_swizzle_b32 v41, v40 offset:swizzle(SWAP,8)
	s_waitcnt lgkmcnt(0)
	v_add_f32_e32 v40, v40, v41
	v_fmamk_f32 v40, v40, 0x3c000000, v204
	v_mul_f32_e32 v41, 0x4f800000, v40
	v_cmp_gt_f32_e32 vcc, s9, v40
	s_nop 1
	v_cndmask_b32_e32 v40, v40, v41, vcc
	v_sqrt_f32_e32 v41, v40
	s_nop 0
	v_add_u32_e32 v50, -1, v41
	v_fma_f32 v51, -v50, v41, v40
	v_cmp_ge_f32_e64 s[38:39], 0, v51
	v_add_u32_e32 v51, 1, v41
	s_nop 0
	v_cndmask_b32_e64 v50, v41, v50, s[38:39]
	v_fma_f32 v41, -v51, v41, v40
	v_cmp_lt_f32_e64 s[38:39], 0, v41
	s_nop 1
	v_cndmask_b32_e64 v41, v50, v51, s[38:39]
	v_mul_f32_e32 v50, 0x37800000, v41
	v_cndmask_b32_e32 v41, v41, v50, vcc
	v_cmp_class_f32_e32 vcc, v40, v205
	s_nop 1
	v_cndmask_b32_e32 v50, v41, v40, vcc
	v_div_scale_f32 v51, s[18:19], v50, v50, 1.0
	v_rcp_f32_e32 v54, v51
	s_waitcnt vmcnt(0)
	v_mov_b32_e32 v40, v46
	v_mov_b32_e32 v41, v48
	v_mov_b32_e32 v48, v47
	v_fma_f32 v46, -v51, v54, 1.0
	v_fmac_f32_e32 v54, v46, v54
	v_div_scale_f32 v46, vcc, 1.0, v50, 1.0
	v_mul_f32_e32 v47, v46, v54
	v_fma_f32 v55, -v51, v47, v46
	v_fmac_f32_e32 v47, v55, v54
	v_fma_f32 v46, -v51, v47, v46
	v_div_fmas_f32 v46, v46, v54, v47
	v_div_fixup_f32 v46, v46, v50, 1.0
	v_pk_mul_f32 v[22:23], v[22:23], v[46:47] op_sel_hi:[1,0]
	v_pk_mul_f32 v[38:39], v[38:39], v[46:47] op_sel_hi:[1,0]
	v_pk_mul_f32 v[22:23], v[48:49], v[22:23]
	v_mov_b32_e32 v48, v42
	v_mov_b32_e32 v49, v44
	v_pk_mul_f32 v[24:25], v[24:25], v[46:47] op_sel_hi:[1,0]
	v_mov_b32_e32 v44, v43
	v_pk_mul_f32 v[38:39], v[48:49], v[38:39]
	v_pk_mul_f32 v[24:25], v[44:45], v[24:25]
	v_bfe_u32 v44, v23, 16, 1
	v_bfe_u32 v45, v22, 16, 1
	v_add3_u32 v22, v22, v45, s10
	v_add3_u32 v23, v23, v44, s10
	v_bfe_u32 v44, v38, 16, 1
	v_bfe_u32 v45, v39, 16, 1
	v_pk_mul_f32 v[50:51], v[52:53], v[46:47] op_sel_hi:[1,0]
	v_bfe_u32 v42, v25, 16, 1
	v_bfe_u32 v43, v24, 16, 1
	v_add3_u32 v39, v39, v45, s10
	v_add3_u32 v38, v38, v44, s10
	v_pk_mul_f32 v[40:41], v[40:41], v[50:51]
	v_add3_u32 v24, v24, v43, s10
	v_add3_u32 v25, v25, v42, s10
	v_lshrrev_b32_e32 v38, 16, v38
	v_lshrrev_b32_e32 v39, 16, v39
	v_bfe_u32 v42, v40, 16, 1
	v_bfe_u32 v43, v41, 16, 1
	v_and_or_b32 v25, v25, s11, v39
	v_and_or_b32 v24, v24, s11, v38
	v_lshlrev_b64 v[38:39], 12, v[84:85]
	v_add3_u32 v41, v41, v43, s10
	v_add3_u32 v40, v40, v42, s10
	v_lshl_add_u64 v[38:39], s[0:1], 0, v[38:39]
	v_lshrrev_b32_e32 v40, 16, v40
	v_lshrrev_b32_e32 v41, 16, v41
	v_lshl_add_u64 v[38:39], v[86:87], 1, v[38:39]
	v_and_or_b32 v23, v23, s11, v41
	v_and_or_b32 v22, v22, s11, v40
	v_lshl_add_u64 v[38:39], v[38:39], 0, v[0:1]
	global_store_dwordx4 v[38:39], v[22:25], off sc0 sc1
	s_cbranch_scc1 .LBB0_1221
; __device__ __forceinline__ void dcombine_phase(const Ptrs& P, const float* gain, int vcu, int G, int wave, int lane, const bool ob8) {
;     ...
;         for (int q = 0; q < NQ; ++q) { if (it0 + q * NGW >= NIT) break;
;             const float mx = fmaxf(fmaxf(ls[q][0], ls[q][1]), fmaxf(ls[q][2], ls[q][3]));
;             float w0 = __builtin_amdgcn_exp2f(ls[q][0] - mx), w1 = __builtin_amdgcn_exp2f(ls[q][1] - mx), w2 = __builtin_amdgcn_exp2f(ls[q][2] - mx), w3 = __builtin_amdgcn_exp2f(ls[q][3] - mx);
;             const float inv = 1.0f / (w0 + w1 + w2 + w3); w0 *= inv; w1 *= inv; w2 *= inv; w3 *= inv;
;             float acc[8];
; #pragma unroll
;             for (int e = 0; e < 8; ++e) acc[e] = 0.f;
; #pragma unroll
;             for (int p = 0; p < 4; ++p) { const v4u r_ = raw[q][p]; const float w = (p == 0) ? w0 : ((p == 1) ? w1 : ((p == 2) ? w2 : w3));
;                 acc[0] += w * bf2f_u((unsigned short)(r_.x & 0xffff)); acc[1] += w * bf2f_u((unsigned short)(r_.x >> 16)); acc[2] += w * bf2f_u((unsigned short)(r_.y & 0xffff)); acc[3] += w * bf2f_u((unsigned short)(r_.y >> 16));
;                 acc[4] += w * bf2f_u((unsigned short)(r_.z & 0xffff)); acc[5] += w * bf2f_u((unsigned short)(r_.z >> 16)); acc[6] += w * bf2f_u((unsigned short)(r_.w & 0xffff)); acc[7] += w * bf2f_u((unsigned short)(r_.w >> 16)); }
;             float ss = 0.f;
; #pragma unroll
;             for (int e = 0; e < 8; ++e) ss = fmaf(acc[e], acc[e], ss);
;             ss += xor_get<1>(ss); ss += xor_get<2>(ss); ss += xor_get<4>(ss); ss += xor_get<8>(ss);
;             const float rn = 1.0f / sqrtf(ss * (1.0f / 128.0f) + EPS);
;             const f32x4 g0 = *(const f32x4*)(gain + hh[q] * 128 + 8 * c), g1 = *(const f32x4*)(gain + hh[q] * 128 + 8 * c + 4);
;             v4u o; o.x = pk2(acc[0] * rn * g0.x, acc[1] * rn * g0.y); o.y = pk2(acc[2] * rn * g0.z, acc[3] * rn * g0.w); o.z = pk2(acc[4] * rn * g1.x, acc[5] * rn * g1.y); o.w = pk2(acc[6] * rn * g1.z, acc[7] * rn * g1.w);
;             if (ob8) { typedef unsigned u32x2_o __attribute__((ext_vector_type(2))); u32x2_o o8; o8.x = pg8::pk4_fp8(acc[0] * rn * g0.x, acc[1] * rn * g0.y, acc[2] * rn * g0.z, acc[3] * rn * g0.w); o8.y = pg8::pk4_fp8(acc[4] * rn * g1.x, acc[5] * rn * g1.y, acc[6] * rn * g1.z, acc[7] * rn * g1.w);
;                 *(GAS u32x2_o*)((unsigned char*)P.OB + (size_t)tok[q] * D + hh[q] * 128 + 8 * c) = o8; }
	s_nop 0
	v_max_f32_e32 v22, v101, v101
	v_max_f32_e32 v23, v100, v100
	v_max_f32_e32 v22, v23, v22
	v_max3_f32 v22, v98, v99, v22
	v_sub_f32_e32 v23, v98, v22
	v_sub_f32_e32 v24, v99, v22
	v_exp_f32_e32 v23, v23
	v_exp_f32_e32 v24, v24
	v_sub_f32_e32 v25, v100, v22
	v_exp_f32_e32 v39, v25
	v_sub_f32_e32 v22, v101, v22
	v_exp_f32_e32 v45, v22
	v_add_f32_e32 v22, v23, v24
	v_add_f32_e32 v22, v39, v22
	v_lshlrev_b32_e32 v47, 16, v31
	v_add_f32_e32 v22, v45, v22
	v_div_scale_f32 v25, s[18:19], v22, v22, 1.0
	v_rcp_f32_e32 v38, v25
	v_lshlrev_b32_e32 v46, 16, v30
	v_and_b32_e32 v49, 0xffff0000, v31
	v_and_b32_e32 v48, 0xffff0000, v30
	v_fma_f32 v40, -v25, v38, 1.0
	v_fmac_f32_e32 v38, v40, v38
	v_div_scale_f32 v40, vcc, 1.0, v22, 1.0
	v_mul_f32_e32 v41, v40, v38
	v_fma_f32 v42, -v25, v41, v40
	v_fmac_f32_e32 v41, v42, v38
	v_fma_f32 v25, -v25, v41, v40
	v_div_fmas_f32 v25, v25, v38, v41
	v_div_fixup_f32 v55, v25, v22, 1.0
	v_lshl_add_u64 v[30:31], v[82:83], 2, v[68:69]
	v_mul_f32_e32 v38, v23, v55
	v_mul_f32_e32 v44, v24, v55
	v_lshlrev_b32_e32 v51, 16, v33
	v_lshlrev_b32_e32 v50, 16, v32
	v_and_b32_e32 v53, 0xffff0000, v33
	v_and_b32_e32 v52, 0xffff0000, v32
	global_load_dwordx4 v[22:25], v[30:31], off offset:16
	s_nop 0
	global_load_dwordx4 v[30:33], v[30:31], off
	v_lshlrev_b32_e32 v41, 16, v35
	v_lshlrev_b32_e32 v40, 16, v34
	v_and_b32_e32 v35, 0xffff0000, v35
	v_and_b32_e32 v34, 0xffff0000, v34
	v_pk_fma_f32 v[40:41], v[38:39], v[40:41], 0 op_sel_hi:[0,1,0]
	v_pk_fma_f32 v[34:35], v[38:39], v[34:35], 0 op_sel_hi:[0,1,0]
	v_mul_f32_e32 v54, v39, v55
	v_lshlrev_b32_e32 v56, 16, v26
	v_and_b32_e32 v26, 0xffff0000, v26
	v_lshlrev_b32_e32 v57, 16, v27
	v_and_b32_e32 v27, 0xffff0000, v27
	v_pk_fma_f32 v[40:41], v[44:45], v[46:47], v[40:41] op_sel_hi:[0,1,1]
	v_pk_fma_f32 v[34:35], v[44:45], v[48:49], v[34:35] op_sel_hi:[0,1,1]
	v_mul_f32_e32 v60, v45, v55
	v_pk_fma_f32 v[40:41], v[54:55], v[56:57], v[40:41] op_sel_hi:[0,1,1]
	v_pk_fma_f32 v[26:27], v[54:55], v[26:27], v[34:35] op_sel_hi:[0,1,1]
	v_lshlrev_b32_e32 v35, 16, v19
	v_lshlrev_b32_e32 v34, 16, v18
	v_pk_fma_f32 v[34:35], v[60:61], v[34:35], v[40:41] op_sel_hi:[0,1,1]
	v_and_b32_e32 v19, 0xffff0000, v19
	v_and_b32_e32 v18, 0xffff0000, v18
	v_pk_fma_f32 v[18:19], v[60:61], v[18:19], v[26:27] op_sel_hi:[0,1,1]
	v_fma_f32 v39, v34, v34, 0
	v_fmac_f32_e32 v39, v18, v18
	v_fmac_f32_e32 v39, v35, v35
	v_lshlrev_b32_e32 v43, 16, v37
	v_lshlrev_b32_e32 v42, 16, v36
	v_and_b32_e32 v37, 0xffff0000, v37
	v_and_b32_e32 v36, 0xffff0000, v36
	v_fmac_f32_e32 v39, v19, v19
	v_pk_fma_f32 v[26:27], v[38:39], v[42:43], 0 op_sel_hi:[0,1,0]
	v_pk_fma_f32 v[36:37], v[38:39], v[36:37], 0 op_sel_hi:[0,1,0]
	v_lshlrev_b32_e32 v58, 16, v28
	v_and_b32_e32 v28, 0xffff0000, v28
	v_lshlrev_b32_e32 v59, 16, v29
	v_and_b32_e32 v29, 0xffff0000, v29
	v_pk_fma_f32 v[26:27], v[44:45], v[50:51], v[26:27] op_sel_hi:[0,1,1]
	v_pk_fma_f32 v[36:37], v[44:45], v[52:53], v[36:37] op_sel_hi:[0,1,1]
	v_pk_fma_f32 v[26:27], v[54:55], v[58:59], v[26:27] op_sel_hi:[0,1,1]
	v_pk_fma_f32 v[28:29], v[54:55], v[28:29], v[36:37] op_sel_hi:[0,1,1]
	v_lshlrev_b32_e32 v37, 16, v21
	v_lshlrev_b32_e32 v36, 16, v20
	v_pk_fma_f32 v[26:27], v[60:61], v[36:37], v[26:27] op_sel_hi:[0,1,1]
	v_and_b32_e32 v21, 0xffff0000, v21
	v_and_b32_e32 v20, 0xffff0000, v20
	v_pk_fma_f32 v[20:21], v[60:61], v[20:21], v[28:29] op_sel_hi:[0,1,1]
	v_fmac_f32_e32 v39, v26, v26
	v_fmac_f32_e32 v39, v20, v20
	v_fmac_f32_e32 v39, v27, v27
	v_fmac_f32_e32 v39, v21, v21
	s_cmpk_gt_i32 s21, 0x57ff
	s_nop 0
	v_add_f32_dpp v28, v39, v39 quad_perm:[1,0,3,2] row_mask:0xf bank_mask:0xf bound_ctrl:1
	s_nop 1
	v_add_f32_dpp v28, v28, v28 quad_perm:[2,3,0,1] row_mask:0xf bank_mask:0xf bound_ctrl:1
	ds_swizzle_b32 v29, v28 offset:swizzle(SWAP,4)
	s_waitcnt lgkmcnt(0)
	v_add_f32_e32 v28, v28, v29
	ds_swizzle_b32 v29, v28 offset:swizzle(SWAP,8)
	s_waitcnt lgkmcnt(0)
	v_add_f32_e32 v28, v28, v29
	v_fmamk_f32 v28, v28, 0x3c000000, v204
	v_mul_f32_e32 v29, 0x4f800000, v28
	v_cmp_gt_f32_e32 vcc, s9, v28
	s_nop 1
	v_cndmask_b32_e32 v28, v28, v29, vcc
	v_sqrt_f32_e32 v29, v28
	s_nop 0
	v_add_u32_e32 v36, -1, v29
	v_fma_f32 v37, -v36, v29, v28
	v_cmp_ge_f32_e64 s[38:39], 0, v37
	v_add_u32_e32 v37, 1, v29
	s_nop 0
	v_cndmask_b32_e64 v36, v29, v36, s[38:39]
	v_fma_f32 v29, -v37, v29, v28
	v_cmp_lt_f32_e64 s[38:39], 0, v29
	s_nop 1
	v_cndmask_b32_e64 v29, v36, v37, s[38:39]
	v_mul_f32_e32 v36, 0x37800000, v29
	v_cndmask_b32_e32 v29, v29, v36, vcc
	v_cmp_class_f32_e32 vcc, v28, v205
	s_nop 1
	v_cndmask_b32_e32 v36, v29, v28, vcc
	v_div_scale_f32 v37, s[18:19], v36, v36, 1.0
	v_rcp_f32_e32 v38, v37
	s_waitcnt vmcnt(0)
	v_mov_b32_e32 v28, v30
	v_mov_b32_e32 v29, v32
	v_mov_b32_e32 v32, v31
	v_fma_f32 v30, -v37, v38, 1.0
	v_fmac_f32_e32 v38, v30, v38
	v_div_scale_f32 v30, vcc, 1.0, v36, 1.0
	v_mul_f32_e32 v31, v30, v38
	v_fma_f32 v39, -v37, v31, v30
	v_fmac_f32_e32 v31, v39, v38
	v_fma_f32 v30, -v37, v31, v30
	v_div_fmas_f32 v30, v30, v38, v31
	v_div_fixup_f32 v30, v30, v36, 1.0
	v_pk_mul_f32 v[18:19], v[18:19], v[30:31] op_sel_hi:[1,0]
	v_pk_mul_f32 v[20:21], v[20:21], v[30:31] op_sel_hi:[1,0]
	v_pk_mul_f32 v[18:19], v[32:33], v[18:19]
	v_mov_b32_e32 v33, v24
	v_mov_b32_e32 v24, v23
	v_pk_mul_f32 v[34:35], v[34:35], v[30:31] op_sel_hi:[1,0]
	v_pk_mul_f32 v[20:21], v[24:25], v[20:21]
	v_pk_mul_f32 v[28:29], v[28:29], v[34:35]
	v_mov_b32_e32 v32, v22
	v_bfe_u32 v22, v21, 16, 1
	v_bfe_u32 v23, v20, 16, 1
	v_add3_u32 v20, v20, v23, s10
	v_add3_u32 v21, v21, v22, s10
	v_bfe_u32 v22, v28, 16, 1
	v_bfe_u32 v23, v29, 16, 1
	v_pk_mul_f32 v[26:27], v[26:27], v[30:31] op_sel_hi:[1,0]
	v_bfe_u32 v24, v19, 16, 1
	v_bfe_u32 v25, v18, 16, 1
	v_add3_u32 v23, v29, v23, s10
	v_add3_u32 v22, v28, v22, s10
	v_pk_mul_f32 v[26:27], v[32:33], v[26:27]
	v_add3_u32 v18, v18, v25, s10
	v_add3_u32 v19, v19, v24, s10
	v_lshrrev_b32_e32 v22, 16, v22
	v_lshrrev_b32_e32 v23, 16, v23
	v_bfe_u32 v24, v26, 16, 1
	v_bfe_u32 v25, v27, 16, 1
	v_and_or_b32 v19, v19, s11, v23
	v_and_or_b32 v18, v18, s11, v22
	v_lshlrev_b64 v[22:23], 12, v[80:81]
	v_add3_u32 v25, v27, v25, s10
	v_add3_u32 v24, v26, v24, s10
	v_lshl_add_u64 v[22:23], s[0:1], 0, v[22:23]
	v_lshrrev_b32_e32 v24, 16, v24
	v_lshrrev_b32_e32 v25, 16, v25
	v_lshl_add_u64 v[22:23], v[82:83], 1, v[22:23]
	v_and_or_b32 v21, v21, s11, v25
	v_and_or_b32 v20, v20, s11, v24
	v_lshl_add_u64 v[22:23], v[22:23], 0, v[0:1]
	global_store_dwordx4 v[22:23], v[18:21], off sc0 sc1
	s_cbranch_scc1 .LBB0_1221
; __device__ __forceinline__ void dcombine_phase(const Ptrs& P, const float* gain, int vcu, int G, int wave, int lane, const bool ob8) {
;     ...
;         for (int q = 0; q < NQ; ++q) { if (it0 + q * NGW >= NIT) break;
;             const float mx = fmaxf(fmaxf(ls[q][0], ls[q][1]), fmaxf(ls[q][2], ls[q][3]));
;             float w0 = __builtin_amdgcn_exp2f(ls[q][0] - mx), w1 = __builtin_amdgcn_exp2f(ls[q][1] - mx), w2 = __builtin_amdgcn_exp2f(ls[q][2] - mx), w3 = __builtin_amdgcn_exp2f(ls[q][3] - mx);
;             const float inv = 1.0f / (w0 + w1 + w2 + w3); w0 *= inv; w1 *= inv; w2 *= inv; w3 *= inv;
;             float acc[8];
; #pragma unroll
;             for (int e = 0; e < 8; ++e) acc[e] = 0.f;
; #pragma unroll
;             for (int p = 0; p < 4; ++p) { const v4u r_ = raw[q][p]; const float w = (p == 0) ? w0 : ((p == 1) ? w1 : ((p == 2) ? w2 : w3));
;                 acc[0] += w * bf2f_u((unsigned short)(r_.x & 0xffff)); acc[1] += w * bf2f_u((unsigned short)(r_.x >> 16)); acc[2] += w * bf2f_u((unsigned short)(r_.y & 0xffff)); acc[3] += w * bf2f_u((unsigned short)(r_.y >> 16));
;                 acc[4] += w * bf2f_u((unsigned short)(r_.z & 0xffff)); acc[5] += w * bf2f_u((unsigned short)(r_.z >> 16)); acc[6] += w * bf2f_u((unsigned short)(r_.w & 0xffff)); acc[7] += w * bf2f_u((unsigned short)(r_.w >> 16)); }
;             float ss = 0.f;
; #pragma unroll
;             for (int e = 0; e < 8; ++e) ss = fmaf(acc[e], acc[e], ss);
;             ss += xor_get<1>(ss); ss += xor_get<2>(ss); ss += xor_get<4>(ss); ss += xor_get<8>(ss);
;             const float rn = 1.0f / sqrtf(ss * (1.0f / 128.0f) + EPS);
;             const f32x4 g0 = *(const f32x4*)(gain + hh[q] * 128 + 8 * c), g1 = *(const f32x4*)(gain + hh[q] * 128 + 8 * c + 4);
;             v4u o; o.x = pk2(acc[0] * rn * g0.x, acc[1] * rn * g0.y); o.y = pk2(acc[2] * rn * g0.z, acc[3] * rn * g0.w); o.z = pk2(acc[4] * rn * g1.x, acc[5] * rn * g1.y); o.w = pk2(acc[6] * rn * g1.z, acc[7] * rn * g1.w);
;             if (ob8) { typedef unsigned u32x2_o __attribute__((ext_vector_type(2))); u32x2_o o8; o8.x = pg8::pk4_fp8(acc[0] * rn * g0.x, acc[1] * rn * g0.y, acc[2] * rn * g0.z, acc[3] * rn * g0.w); o8.y = pg8::pk4_fp8(acc[4] * rn * g1.x, acc[5] * rn * g1.y, acc[6] * rn * g1.z, acc[7] * rn * g1.w);
;                 *(GAS u32x2_o*)((unsigned char*)P.OB + (size_t)tok[q] * D + hh[q] * 128 + 8 * c) = o8; }
	s_nop 0
	v_max_f32_e32 v18, v73, v73
	v_max_f32_e32 v19, v97, v97
	v_max_f32_e32 v18, v19, v18
	v_max3_f32 v18, v75, v96, v18
	v_sub_f32_e32 v19, v75, v18
	v_sub_f32_e32 v20, v96, v18
	v_exp_f32_e32 v19, v19
	v_exp_f32_e32 v28, v20
	v_sub_f32_e32 v20, v97, v18
	v_exp_f32_e32 v29, v20
	v_sub_f32_e32 v18, v73, v18
	v_exp_f32_e32 v39, v18
	v_add_f32_e32 v18, v19, v28
	v_add_f32_e32 v18, v29, v18
	v_lshlrev_b32_e32 v25, 16, v17
	v_add_f32_e32 v18, v39, v18
	v_div_scale_f32 v20, s[18:19], v18, v18, 1.0
	v_rcp_f32_e32 v21, v20
	v_and_b32_e32 v27, 0xffff0000, v17
	v_and_b32_e32 v26, 0xffff0000, v16
	v_lshlrev_b32_e32 v31, 16, v11
	v_fma_f32 v22, -v20, v21, 1.0
	v_fmac_f32_e32 v21, v22, v21
	v_div_scale_f32 v22, vcc, 1.0, v18, 1.0
	v_mul_f32_e32 v23, v22, v21
	v_fma_f32 v24, -v20, v23, v22
	v_fmac_f32_e32 v23, v24, v21
	v_fma_f32 v20, -v20, v23, v22
	v_div_fmas_f32 v20, v20, v21, v23
	v_div_fixup_f32 v44, v20, v18, 1.0
	v_lshlrev_b32_e32 v21, 16, v15
	v_lshlrev_b32_e32 v20, 16, v14
	v_and_b32_e32 v23, 0xffff0000, v15
	v_and_b32_e32 v22, 0xffff0000, v14
	v_lshl_add_u64 v[14:15], v[78:79], 2, v[68:69]
	v_lshlrev_b32_e32 v24, 16, v16
	v_lshlrev_b32_e32 v30, 16, v10
	v_and_b32_e32 v33, 0xffff0000, v11
	v_and_b32_e32 v32, 0xffff0000, v10
	v_lshlrev_b32_e32 v35, 16, v13
	v_lshlrev_b32_e32 v34, 16, v12
	v_and_b32_e32 v37, 0xffff0000, v13
	v_and_b32_e32 v36, 0xffff0000, v12
	global_load_dwordx4 v[10:13], v[14:15], off offset:16
	s_nop 0
	global_load_dwordx4 v[14:17], v[14:15], off
	v_mul_f32_e32 v18, v19, v44
	v_mul_f32_e32 v28, v28, v44
	v_pk_fma_f32 v[20:21], v[18:19], v[20:21], 0 op_sel_hi:[0,1,0]
	v_pk_fma_f32 v[22:23], v[18:19], v[22:23], 0 op_sel_hi:[0,1,0]
	v_mul_f32_e32 v38, v29, v44
	v_lshlrev_b32_e32 v40, 16, v6
	v_and_b32_e32 v6, 0xffff0000, v6
	v_lshlrev_b32_e32 v41, 16, v7
	v_and_b32_e32 v7, 0xffff0000, v7
	v_pk_fma_f32 v[20:21], v[28:29], v[30:31], v[20:21] op_sel_hi:[0,1,1]
	v_pk_fma_f32 v[22:23], v[28:29], v[32:33], v[22:23] op_sel_hi:[0,1,1]
	v_mul_f32_e32 v44, v39, v44
	v_pk_fma_f32 v[20:21], v[38:39], v[40:41], v[20:21] op_sel_hi:[0,1,1]
	v_pk_fma_f32 v[6:7], v[38:39], v[6:7], v[22:23] op_sel_hi:[0,1,1]
	v_lshlrev_b32_e32 v23, 16, v3
	v_lshlrev_b32_e32 v22, 16, v2
	v_pk_fma_f32 v[20:21], v[44:45], v[22:23], v[20:21] op_sel_hi:[0,1,1]
	v_and_b32_e32 v3, 0xffff0000, v3
	v_and_b32_e32 v2, 0xffff0000, v2
	v_pk_fma_f32 v[2:3], v[44:45], v[2:3], v[6:7] op_sel_hi:[0,1,1]
	v_fma_f32 v22, v20, v20, 0
	v_pk_fma_f32 v[6:7], v[18:19], v[24:25], 0 op_sel_hi:[0,1,0]
	v_pk_fma_f32 v[18:19], v[18:19], v[26:27], 0 op_sel_hi:[0,1,0]
	v_lshlrev_b32_e32 v42, 16, v8
	v_and_b32_e32 v8, 0xffff0000, v8
	v_lshlrev_b32_e32 v43, 16, v9
	v_and_b32_e32 v9, 0xffff0000, v9
	v_fmac_f32_e32 v22, v2, v2
	v_pk_fma_f32 v[6:7], v[28:29], v[34:35], v[6:7] op_sel_hi:[0,1,1]
	v_pk_fma_f32 v[18:19], v[28:29], v[36:37], v[18:19] op_sel_hi:[0,1,1]
	v_fmac_f32_e32 v22, v21, v21
	v_pk_fma_f32 v[6:7], v[38:39], v[42:43], v[6:7] op_sel_hi:[0,1,1]
	v_pk_fma_f32 v[8:9], v[38:39], v[8:9], v[18:19] op_sel_hi:[0,1,1]
	v_lshlrev_b32_e32 v19, 16, v5
	v_lshlrev_b32_e32 v18, 16, v4
	v_fmac_f32_e32 v22, v3, v3
	v_pk_fma_f32 v[6:7], v[44:45], v[18:19], v[6:7] op_sel_hi:[0,1,1]
	v_and_b32_e32 v5, 0xffff0000, v5
	v_and_b32_e32 v4, 0xffff0000, v4
	v_pk_fma_f32 v[4:5], v[44:45], v[4:5], v[8:9] op_sel_hi:[0,1,1]
	v_fmac_f32_e32 v22, v6, v6
	v_fmac_f32_e32 v22, v4, v4
	v_fmac_f32_e32 v22, v7, v7
	v_fmac_f32_e32 v22, v5, v5
	s_nop 1
	v_add_f32_dpp v8, v22, v22 quad_perm:[1,0,3,2] row_mask:0xf bank_mask:0xf bound_ctrl:1
	s_nop 1
	v_add_f32_dpp v8, v8, v8 quad_perm:[2,3,0,1] row_mask:0xf bank_mask:0xf bound_ctrl:1
	ds_swizzle_b32 v9, v8 offset:swizzle(SWAP,4)
	s_waitcnt lgkmcnt(0)
	v_add_f32_e32 v8, v8, v9
	ds_swizzle_b32 v9, v8 offset:swizzle(SWAP,8)
	s_waitcnt lgkmcnt(0)
	v_add_f32_e32 v8, v8, v9
	v_fmamk_f32 v8, v8, 0x3c000000, v204
	v_mul_f32_e32 v9, 0x4f800000, v8
	v_cmp_gt_f32_e32 vcc, s9, v8
	s_nop 1
	v_cndmask_b32_e32 v8, v8, v9, vcc
	v_sqrt_f32_e32 v9, v8
	s_nop 0
	v_add_u32_e32 v18, -1, v9
	v_fma_f32 v19, -v18, v9, v8
	v_cmp_ge_f32_e64 s[38:39], 0, v19
	v_add_u32_e32 v19, 1, v9
	s_nop 0
	v_cndmask_b32_e64 v18, v9, v18, s[38:39]
	v_fma_f32 v9, -v19, v9, v8
	v_cmp_lt_f32_e64 s[38:39], 0, v9
	s_nop 1
	v_cndmask_b32_e64 v9, v18, v19, s[38:39]
	v_mul_f32_e32 v18, 0x37800000, v9
	v_cndmask_b32_e32 v9, v9, v18, vcc
	v_cmp_class_f32_e32 vcc, v8, v205
	s_nop 1
	v_cndmask_b32_e32 v18, v9, v8, vcc
	v_div_scale_f32 v19, s[18:19], v18, v18, 1.0
	v_rcp_f32_e32 v22, v19
	s_waitcnt vmcnt(0)
	v_mov_b32_e32 v8, v14
	v_mov_b32_e32 v9, v16
	v_mov_b32_e32 v16, v15
	v_fma_f32 v14, -v19, v22, 1.0
	v_fmac_f32_e32 v22, v14, v22
	v_div_scale_f32 v14, vcc, 1.0, v18, 1.0
	v_mul_f32_e32 v15, v14, v22
	v_fma_f32 v23, -v19, v15, v14
	v_fmac_f32_e32 v15, v23, v22
	v_fma_f32 v14, -v19, v15, v14
	v_div_fmas_f32 v14, v14, v22, v15
	v_div_fixup_f32 v14, v14, v18, 1.0
	v_pk_mul_f32 v[2:3], v[2:3], v[14:15] op_sel_hi:[1,0]
	v_pk_mul_f32 v[6:7], v[6:7], v[14:15] op_sel_hi:[1,0]
	v_pk_mul_f32 v[2:3], v[16:17], v[2:3]
	v_mov_b32_e32 v16, v10
	v_mov_b32_e32 v17, v12
	v_pk_mul_f32 v[4:5], v[4:5], v[14:15] op_sel_hi:[1,0]
	v_mov_b32_e32 v12, v11
	v_pk_mul_f32 v[6:7], v[16:17], v[6:7]
	v_pk_mul_f32 v[4:5], v[12:13], v[4:5]
	v_bfe_u32 v12, v3, 16, 1
	v_bfe_u32 v13, v2, 16, 1
	v_add3_u32 v2, v2, v13, s10
	v_add3_u32 v3, v3, v12, s10
	v_bfe_u32 v12, v6, 16, 1
	v_bfe_u32 v13, v7, 16, 1
	v_pk_mul_f32 v[18:19], v[20:21], v[14:15] op_sel_hi:[1,0]
	v_bfe_u32 v10, v5, 16, 1
	v_bfe_u32 v11, v4, 16, 1
	v_add3_u32 v7, v7, v13, s10
	v_add3_u32 v6, v6, v12, s10
	v_pk_mul_f32 v[8:9], v[8:9], v[18:19]
	v_add3_u32 v4, v4, v11, s10
	v_add3_u32 v5, v5, v10, s10
	v_lshrrev_b32_e32 v6, 16, v6
	v_lshrrev_b32_e32 v7, 16, v7
	v_bfe_u32 v10, v8, 16, 1
	v_bfe_u32 v11, v9, 16, 1
	v_and_or_b32 v5, v5, s11, v7
	v_and_or_b32 v4, v4, s11, v6
	v_lshlrev_b64 v[6:7], 12, v[76:77]
	v_add3_u32 v9, v9, v11, s10
	v_add3_u32 v8, v8, v10, s10
	v_lshl_add_u64 v[6:7], s[0:1], 0, v[6:7]
	v_lshrrev_b32_e32 v8, 16, v8
	v_lshrrev_b32_e32 v9, 16, v9
	v_lshl_add_u64 v[6:7], v[78:79], 1, v[6:7]
	v_and_or_b32 v3, v3, s11, v9
	v_and_or_b32 v2, v2, s11, v8
	v_lshl_add_u64 v[6:7], v[6:7], 0, v[0:1]
	global_store_dwordx4 v[6:7], v[2:5], off sc0 sc1
	s_branch .LBB0_1221

; #define GAS __attribute__((address_space(1)))
; __device__ __forceinline__ f32x4 bf4_to_f32(u32x2_g a) { return (f32x4){__uint_as_float(a.x << 16), __uint_as_float(a.x & 0xffff0000u), __uint_as_float(a.y << 16), __uint_as_float(a.y & 0xffff0000u)}; }
; #define lane (lane_id())
; __device__ __forceinline__ void router_phase(const Ptrs& P, const float* gain, LAS unsigned char* lds, int vcu, int G, int tid, int wave, int lane) {
;     ...
;         const GAS u32x2_g* xr = (const GAS u32x2_g*)(P.H + (size_t)m * D) + lane;
;         f32x4 v[8]; float s = 0.f;
; #pragma unroll
;         for (int j = 0; j < 8; ++j) { v[j] = bf4_to_f32(xr[64 * j]); s += (v[j].x * v[j].x + v[j].y * v[j].y) + (v[j].z * v[j].z + v[j].w * v[j].w); }
;         const float r = 1.0f / sqrtf(wave_sum(s) * (1.0f / D) + EPS);
;         float lg[8];
; #pragma unroll
;         for (int e = 0; e < 8; ++e) lg[e] = 0.f;
;         GAS unsigned* o4 = (GAS unsigned*)(P.AB8 + (size_t)m * D) + lane;
; #pragma unroll
;         for (int j = 0; j < 8; ++j) { const f32x4 g = ((const GAS f32x4*)gain)[lane + 64 * j];
;             const float f0 = v[j].x * r * g.x, f1 = v[j].y * r * g.y, f2 = v[j].z * r * g.z, f3 = v[j].w * r * g.w;
.LBB0_1475:
	global_load_dwordx2 v[2:3], v[48:49], off offset:-2048
	global_load_dwordx2 v[54:55], v[48:49], off offset:1536
	s_waitcnt vmcnt(1)
	v_and_b32_e32 v33, 0xffff0000, v2
	v_and_b32_e32 v31, 0xffff0000, v3
	v_lshlrev_b32_e32 v35, 16, v2
	v_lshlrev_b32_e32 v32, 16, v3
	v_mul_f32_e32 v2, v33, v33
	v_mul_f32_e32 v3, v31, v31
	v_fmac_f32_e32 v2, v35, v35
	v_fmac_f32_e32 v3, v32, v32
	v_add_f32_e32 v4, v2, v3
	global_load_dwordx2 v[2:3], v[48:49], off offset:-1536
	s_waitcnt vmcnt(1)
	v_lshlrev_b32_e32 v5, 16, v54
	s_waitcnt vmcnt(0)
	v_and_b32_e32 v29, 0xffff0000, v2
	v_and_b32_e32 v27, 0xffff0000, v3
	v_lshlrev_b32_e32 v30, 16, v2
	v_lshlrev_b32_e32 v28, 16, v3
	v_mul_f32_e32 v2, v29, v29
	v_mul_f32_e32 v3, v27, v27
	v_fmac_f32_e32 v2, v30, v30
	v_fmac_f32_e32 v3, v28, v28
	v_add_f32_e32 v2, v2, v3
	v_add_f32_e32 v4, v4, v2
	global_load_dwordx2 v[2:3], v[48:49], off offset:-1024
	s_waitcnt vmcnt(0)
	v_and_b32_e32 v25, 0xffff0000, v2
	v_and_b32_e32 v23, 0xffff0000, v3
	v_lshlrev_b32_e32 v26, 16, v2
	v_lshlrev_b32_e32 v24, 16, v3
	v_mul_f32_e32 v2, v25, v25
	v_mul_f32_e32 v3, v23, v23
	v_fmac_f32_e32 v2, v26, v26
	v_fmac_f32_e32 v3, v24, v24
	v_add_f32_e32 v2, v2, v3
	v_add_f32_e32 v4, v4, v2
	global_load_dwordx2 v[2:3], v[48:49], off offset:-512
	s_waitcnt vmcnt(0)
	v_and_b32_e32 v21, 0xffff0000, v2
	v_and_b32_e32 v19, 0xffff0000, v3
	v_lshlrev_b32_e32 v22, 16, v2
	v_lshlrev_b32_e32 v20, 16, v3
	v_mul_f32_e32 v2, v21, v21
	v_mul_f32_e32 v3, v19, v19
	v_fmac_f32_e32 v2, v22, v22
	v_fmac_f32_e32 v3, v20, v20
	v_add_f32_e32 v2, v2, v3
	v_add_f32_e32 v4, v4, v2
	global_load_dwordx2 v[2:3], v[48:49], off
	s_waitcnt vmcnt(0)
	v_and_b32_e32 v17, 0xffff0000, v2
	v_and_b32_e32 v15, 0xffff0000, v3
	v_lshlrev_b32_e32 v18, 16, v2
	v_lshlrev_b32_e32 v16, 16, v3
	v_mul_f32_e32 v2, v17, v17
	v_mul_f32_e32 v3, v15, v15
	v_fmac_f32_e32 v2, v18, v18
	v_fmac_f32_e32 v3, v16, v16
	v_add_f32_e32 v2, v2, v3
	v_add_f32_e32 v4, v4, v2
	global_load_dwordx2 v[2:3], v[48:49], off offset:512
	s_waitcnt vmcnt(0)
	v_and_b32_e32 v13, 0xffff0000, v2
	v_and_b32_e32 v11, 0xffff0000, v3
	v_lshlrev_b32_e32 v14, 16, v2
	v_lshlrev_b32_e32 v12, 16, v3
	v_mul_f32_e32 v2, v13, v13
	v_mul_f32_e32 v3, v11, v11
	v_fmac_f32_e32 v2, v14, v14
	v_fmac_f32_e32 v3, v12, v12
	v_add_f32_e32 v2, v2, v3
	v_add_f32_e32 v4, v4, v2
	global_load_dwordx2 v[2:3], v[48:49], off offset:1024
	s_waitcnt vmcnt(0)
	v_and_b32_e32 v9, 0xffff0000, v2
	v_and_b32_e32 v7, 0xffff0000, v3
	v_lshlrev_b32_e32 v10, 16, v2
	v_lshlrev_b32_e32 v8, 16, v3
	v_mul_f32_e32 v2, v9, v9
	v_mul_f32_e32 v3, v7, v7
	v_fmac_f32_e32 v2, v10, v10
	v_fmac_f32_e32 v3, v8, v8
	v_add_f32_e32 v2, v2, v3
	v_add_f32_e32 v6, v4, v2
	v_and_b32_e32 v4, 0xffff0000, v54
	v_and_b32_e32 v2, 0xffff0000, v55
	v_lshlrev_b32_e32 v3, 16, v55
	v_mul_f32_e32 v53, v4, v4
	v_mul_f32_e32 v54, v2, v2
	v_fmac_f32_e32 v53, v5, v5
	v_fmac_f32_e32 v54, v3, v3
	v_add_f32_e32 v53, v53, v54
	v_add_f32_e32 v6, v6, v53
	s_nop 1
	v_add_f32_dpp v6, v6, v6 quad_perm:[1,0,3,2] row_mask:0xf bank_mask:0xf bound_ctrl:1
	s_nop 1
	v_add_f32_dpp v6, v6, v6 quad_perm:[2,3,0,1] row_mask:0xf bank_mask:0xf bound_ctrl:1
	ds_swizzle_b32 v53, v6 offset:swizzle(SWAP,4)
	s_waitcnt lgkmcnt(0)
	v_add_f32_e32 v6, v6, v53
	ds_swizzle_b32 v53, v6 offset:swizzle(SWAP,8)
	s_waitcnt lgkmcnt(0)
	v_add_f32_e32 v6, v6, v53
	ds_swizzle_b32 v53, v6 offset:swizzle(SWAP,16)
	s_waitcnt lgkmcnt(0)
	v_add_f32_e32 v6, v6, v53
	v_mov_b32_e32 v53, v6
	s_nop 1
	v_permlane32_swap_b32_e32 v6, v53
	v_add_f32_e32 v6, v6, v53
	v_fmamk_f32 v6, v6, 0x3a000000, v204
	v_cmp_gt_f32_e32 vcc, s9, v6
	v_mul_f32_e32 v53, 0x4f800000, v6
	s_nop 0
	v_cndmask_b32_e32 v6, v6, v53, vcc
	v_sqrt_f32_e32 v53, v6
	s_nop 0
	v_add_u32_e32 v54, -1, v53
	v_fma_f32 v55, -v54, v53, v6
	v_cmp_ge_f32_e64 s[40:41], 0, v55
	v_add_u32_e32 v55, 1, v53
	s_nop 0
	v_cndmask_b32_e64 v54, v53, v54, s[40:41]
	v_fma_f32 v53, -v55, v53, v6
	v_cmp_lt_f32_e64 s[40:41], 0, v53
	s_nop 1
	v_cndmask_b32_e64 v53, v54, v55, s[40:41]
	v_mul_f32_e32 v54, 0x37800000, v53
	v_cndmask_b32_e32 v53, v53, v54, vcc
	v_cmp_class_f32_e32 vcc, v6, v205
	s_nop 1
	v_cndmask_b32_e32 v6, v53, v6, vcc
	v_div_scale_f32 v53, s[28:29], v6, v6, 1.0
	v_rcp_f32_e32 v54, v53
	s_nop 0
	v_fma_f32 v55, -v53, v54, 1.0
	v_fmac_f32_e32 v54, v55, v54
	v_div_scale_f32 v55, vcc, 1.0, v6, 1.0
	v_mul_f32_e32 v56, v55, v54
	v_fma_f32 v57, -v53, v56, v55
	v_fmac_f32_e32 v56, v57, v54
	v_fma_f32 v53, -v53, v56, v55
	v_div_fmas_f32 v53, v53, v54, v56
	global_load_dwordx4 v[54:57], v[38:39], off
	v_div_fixup_f32 v6, v53, v6, 1.0
	v_mul_f32_e32 v35, v6, v35
	v_mul_f32_e32 v33, v6, v33
	v_mov_b32_e32 v53, v1
	v_mul_f32_e32 v32, v6, v32
	v_mul_f32_e32 v31, v6, v31
	v_mul_f32_e32 v30, v6, v30
	v_mul_f32_e32 v29, v6, v29
	v_mul_f32_e32 v28, v6, v28
	v_mul_f32_e32 v27, v6, v27
	v_mul_f32_e32 v26, v6, v26
	v_mul_f32_e32 v25, v6, v25
	v_mul_f32_e32 v24, v6, v24
	v_mul_f32_e32 v23, v6, v23
	v_mul_f32_e32 v22, v6, v22
	v_mul_f32_e32 v21, v6, v21
	v_mul_f32_e32 v20, v6, v20
	v_mul_f32_e32 v19, v6, v19
	v_mul_f32_e32 v18, v6, v18
	v_mul_f32_e32 v17, v6, v17
	v_mul_f32_e32 v16, v6, v16
	v_mul_f32_e32 v15, v6, v15
	v_mul_f32_e32 v14, v6, v14
	v_mul_f32_e32 v13, v6, v13
	v_mul_f32_e32 v12, v6, v12
	v_mul_f32_e32 v11, v6, v11
	v_mul_f32_e32 v10, v6, v10
	v_mul_f32_e32 v9, v6, v9
	v_mul_f32_e32 v8, v6, v8
	v_mul_f32_e32 v7, v6, v7
	v_mul_f32_e32 v5, v6, v5
	v_mul_f32_e32 v4, v6, v4
	v_mul_f32_e32 v2, v6, v2
	v_mul_f32_e32 v3, v6, v3
	s_waitcnt vmcnt(0)
; __device__ __forceinline__ unsigned pk4_fp8(float a, float b, float c, float d) { int w = 0; w = __builtin_amdgcn_cvt_pk_fp8_f32(a, b, w, false); w = __builtin_amdgcn_cvt_pk_fp8_f32(c, d, w, true); return (unsigned)w; }
; #define GAS __attribute__((address_space(1)))
; #define LAS __attribute__((address_space(3)))
; #define lane (lane_id())
; __device__ __forceinline__ void router_phase(const Ptrs& P, const float* gain, LAS unsigned char* lds, int vcu, int G, int tid, int wave, int lane) {
;     ...
;         for (int j = 0; j < 8; ++j) { const f32x4 g = ((const GAS f32x4*)gain)[lane + 64 * j];
;             const float f0 = v[j].x * r * g.x, f1 = v[j].y * r * g.y, f2 = v[j].z * r * g.z, f3 = v[j].w * r * g.w;
;             o4[64 * j] = pg8::pk4_fp8(f0, f1, f2, f3);
;             const LAS f32x4* rw = LT + 256 * j + 4 * lane;
;             const f32x4 a0 = rw[0], a1 = rw[D], b0 = rw[1], b1 = rw[D + 1], c0 = rw[2], c1 = rw[D + 2], d0 = rw[3], d1 = rw[D + 3];
;             lg[0] += f0 * a0.x + f1 * b0.x + f2 * c0.x + f3 * d0.x; lg[1] += f0 * a0.y + f1 * b0.y + f2 * c0.y + f3 * d0.y;
;             lg[2] += f0 * a0.z + f1 * b0.z + f2 * c0.z + f3 * d0.z; lg[3] += f0 * a0.w + f1 * b0.w + f2 * c0.w + f3 * d0.w;
;             lg[4] += f0 * a1.x + f1 * b1.x + f2 * c1.x + f3 * d1.x; lg[5] += f0 * a1.y + f1 * b1.y + f2 * c1.y + f3 * d1.y;
;             lg[6] += f0 * a1.z + f1 * b1.z + f2 * c1.z + f3 * d1.z; lg[7] += f0 * a1.w + f1 * b1.w + f2 * c1.w + f3 * d1.w; }
	v_mul_f32_e32 v35, v54, v35
	v_mul_f32_e32 v33, v55, v33
	v_cvt_pk_fp8_f32 v53, v35, v33
	v_mul_f32_e32 v32, v56, v32
	v_mul_f32_e32 v31, v57, v31
	v_cvt_pk_fp8_f32 v53, v32, v31 op_sel:[0,0,1]
	global_store_dword v[50:51], v53, off offset:-1024 sc0 sc1
	ds_read_b128 v[54:57], v37 offset:36864
	ds_read_b128 v[58:61], v37 offset:36880
	ds_read_b128 v[62:65], v37 offset:36896
	ds_read_b128 v[66:69], v37 offset:4096
	ds_read_b128 v[70:73], v37 offset:4112
	ds_read_b128 v[74:77], v37 offset:4128
	ds_read_b128 v[78:81], v37 offset:4144
	ds_read_b128 v[82:85], v37 offset:36912
	s_waitcnt lgkmcnt(6)
	v_mul_f32_e32 v58, v33, v58
	s_waitcnt lgkmcnt(3)
	v_mul_f32_e32 v53, v70, v33
	v_fmac_f32_e32 v53, v66, v35
	v_mul_f32_e32 v66, v71, v33
	v_fmac_f32_e32 v66, v67, v35
	v_fmac_f32_e32 v58, v54, v35
	v_mul_f32_e32 v54, v33, v59
	s_waitcnt lgkmcnt(2)
	v_fmac_f32_e32 v66, v32, v75
	v_fmac_f32_e32 v54, v55, v35
	s_waitcnt lgkmcnt(1)
	v_fmac_f32_e32 v66, v31, v79
	v_fmac_f32_e32 v54, v32, v63
	v_add_f32_e32 v86, 0, v66
	v_mul_f32_e32 v66, v72, v33
	s_waitcnt lgkmcnt(0)
	v_fmac_f32_e32 v54, v31, v83
	v_fmac_f32_e32 v66, v68, v35
	v_add_f32_e32 v83, 0, v54
	v_mul_f32_e32 v54, v33, v60
	v_fmac_f32_e32 v66, v32, v76
	v_fmac_f32_e32 v54, v56, v35
	v_fmac_f32_e32 v66, v31, v80
	v_fmac_f32_e32 v54, v32, v64
	v_add_f32_e32 v87, 0, v66
	v_mul_f32_e32 v66, v73, v33
	v_fmac_f32_e32 v54, v31, v84
	v_mul_f32_e32 v33, v33, v61
	v_add_f32_e32 v84, 0, v54
	v_fmac_f32_e32 v33, v57, v35
	global_load_dwordx4 v[54:57], v[38:39], off offset:1024
	v_fmac_f32_e32 v33, v32, v65
	v_fmac_f32_e32 v66, v69, v35
	v_fmac_f32_e32 v33, v31, v85
	v_fmac_f32_e32 v53, v32, v74
	v_fmac_f32_e32 v66, v32, v77
	v_fmac_f32_e32 v58, v32, v62
	v_add_f32_e32 v32, 0, v33
	v_fmac_f32_e32 v66, v31, v81
	v_fmac_f32_e32 v58, v31, v82
	v_fmac_f32_e32 v53, v31, v78
	v_add_f32_e32 v88, 0, v66
	v_add_f32_e32 v82, 0, v58
	v_add_f32_e32 v53, 0, v53
	s_waitcnt vmcnt(0)
	v_mul_f32_e32 v33, v30, v54
	v_mul_f32_e32 v35, v29, v55
	v_mul_f32_e32 v85, v28, v56
	v_mov_b32_e32 v28, v1
	v_cvt_pk_fp8_f32 v28, v33, v35
	v_mul_f32_e32 v27, v27, v57
	v_cvt_pk_fp8_f32 v28, v85, v27 op_sel:[0,0,1]
	global_store_dword v[50:51], v28, off offset:-768 sc0 sc1
	ds_read_b128 v[28:31], v37 offset:40960
	ds_read_b128 v[54:57], v37 offset:40976
	ds_read_b128 v[58:61], v37 offset:40992
	ds_read_b128 v[62:65], v37 offset:8192
	ds_read_b128 v[66:69], v37 offset:8208
	ds_read_b128 v[70:73], v37 offset:8224
	ds_read_b128 v[74:77], v37 offset:8240
	ds_read_b128 v[78:81], v37 offset:41008
	s_waitcnt lgkmcnt(6)
	v_mul_f32_e32 v54, v35, v54
	v_fmac_f32_e32 v54, v33, v28
	v_mul_f32_e32 v28, v35, v55
	v_fmac_f32_e32 v28, v33, v29
	s_waitcnt lgkmcnt(5)
	v_fmac_f32_e32 v28, v85, v59
	s_waitcnt lgkmcnt(0)
	v_fmac_f32_e32 v28, v27, v79
	v_add_f32_e32 v79, v83, v28
	v_mul_f32_e32 v28, v35, v56
	v_fmac_f32_e32 v28, v33, v30
	v_fmac_f32_e32 v28, v85, v60
	v_fmac_f32_e32 v28, v27, v80
	v_add_f32_e32 v80, v84, v28
	v_mul_f32_e32 v28, v35, v57
	v_fmac_f32_e32 v28, v33, v31
	v_fmac_f32_e32 v28, v85, v61
	v_fmac_f32_e32 v28, v27, v81
	v_add_f32_e32 v32, v32, v28
	global_load_dwordx4 v[28:31], v[38:39], off offset:2048
	v_mul_f32_e32 v66, v35, v66
	v_fmac_f32_e32 v66, v33, v62
	v_mul_f32_e32 v62, v35, v67
	v_fmac_f32_e32 v62, v33, v63
	v_fmac_f32_e32 v62, v85, v71
	v_fmac_f32_e32 v62, v27, v75
	v_add_f32_e32 v86, v86, v62
	v_mul_f32_e32 v62, v35, v68
	v_fmac_f32_e32 v62, v33, v64
	v_fmac_f32_e32 v62, v85, v72
	v_fmac_f32_e32 v62, v27, v76
	v_add_f32_e32 v87, v87, v62
	v_mul_f32_e32 v62, v35, v69
	v_fmac_f32_e32 v62, v33, v65
	v_fmac_f32_e32 v66, v85, v70
	v_fmac_f32_e32 v62, v85, v73
	v_fmac_f32_e32 v54, v85, v58
	v_fmac_f32_e32 v66, v27, v74
	v_fmac_f32_e32 v62, v27, v77
	v_fmac_f32_e32 v54, v27, v78
	v_add_f32_e32 v53, v53, v66
	v_add_f32_e32 v88, v88, v62
	v_add_f32_e32 v78, v82, v54
	s_waitcnt vmcnt(0)
	v_mul_f32_e32 v33, v26, v28
	v_mul_f32_e32 v35, v25, v29
	v_mul_f32_e32 v81, v24, v30
	v_mov_b32_e32 v24, v1
	v_cvt_pk_fp8_f32 v24, v33, v35
	v_mul_f32_e32 v23, v23, v31
	v_cvt_pk_fp8_f32 v24, v81, v23 op_sel:[0,0,1]
	global_store_dword v[50:51], v24, off offset:-512 sc0 sc1
	ds_read_b128 v[24:27], v37 offset:45056
	ds_read_b128 v[28:31], v37 offset:45072
	ds_read_b128 v[54:57], v37 offset:45088
	ds_read_b128 v[58:61], v37 offset:12288
	ds_read_b128 v[62:65], v37 offset:12304
	ds_read_b128 v[66:69], v37 offset:12320
	ds_read_b128 v[70:73], v37 offset:12336
	ds_read_b128 v[74:77], v37 offset:45104
	s_waitcnt lgkmcnt(6)
	v_mul_f32_e32 v28, v35, v28
	v_fmac_f32_e32 v28, v33, v24
	v_mul_f32_e32 v24, v35, v29
	v_fmac_f32_e32 v24, v33, v25
	s_waitcnt lgkmcnt(5)
	v_fmac_f32_e32 v24, v81, v55
	s_waitcnt lgkmcnt(0)
	v_fmac_f32_e32 v24, v23, v75
	v_add_f32_e32 v75, v79, v24
	v_mul_f32_e32 v24, v35, v30
	v_fmac_f32_e32 v24, v33, v26
	v_fmac_f32_e32 v24, v81, v56
	v_fmac_f32_e32 v24, v23, v76
	v_add_f32_e32 v76, v80, v24
	v_mul_f32_e32 v24, v35, v31
	v_fmac_f32_e32 v24, v33, v27
	v_fmac_f32_e32 v24, v81, v57
	v_fmac_f32_e32 v24, v23, v77
	v_add_f32_e32 v32, v32, v24
	global_load_dwordx4 v[24:27], v[38:39], off offset:3072
	v_mul_f32_e32 v62, v35, v62
	v_fmac_f32_e32 v62, v33, v58
	v_mul_f32_e32 v58, v35, v63
	v_fmac_f32_e32 v58, v33, v59
	v_fmac_f32_e32 v58, v81, v67
	v_fmac_f32_e32 v58, v23, v71
	v_add_f32_e32 v82, v86, v58
	v_mul_f32_e32 v58, v35, v64
	v_fmac_f32_e32 v58, v33, v60
	v_fmac_f32_e32 v58, v81, v68
	v_fmac_f32_e32 v58, v23, v72
	v_add_f32_e32 v83, v87, v58
	v_mul_f32_e32 v58, v35, v65
	v_fmac_f32_e32 v58, v33, v61
	v_fmac_f32_e32 v62, v81, v66
	v_fmac_f32_e32 v58, v81, v69
	v_fmac_f32_e32 v28, v81, v54
	v_fmac_f32_e32 v62, v23, v70
	v_fmac_f32_e32 v58, v23, v73
	v_fmac_f32_e32 v28, v23, v74
	v_add_f32_e32 v53, v53, v62
	v_add_f32_e32 v84, v88, v58
	v_add_f32_e32 v74, v78, v28
	s_waitcnt vmcnt(0)
; __device__ __forceinline__ unsigned pk4_fp8(float a, float b, float c, float d) { int w = 0; w = __builtin_amdgcn_cvt_pk_fp8_f32(a, b, w, false); w = __builtin_amdgcn_cvt_pk_fp8_f32(c, d, w, true); return (unsigned)w; }
; #define GAS __attribute__((address_space(1)))
; #define LAS __attribute__((address_space(3)))
; #define lane (lane_id())
; __device__ __forceinline__ void router_phase(const Ptrs& P, const float* gain, LAS unsigned char* lds, int vcu, int G, int tid, int wave, int lane) {
;     ...
;         for (int j = 0; j < 8; ++j) { const f32x4 g = ((const GAS f32x4*)gain)[lane + 64 * j];
;             const float f0 = v[j].x * r * g.x, f1 = v[j].y * r * g.y, f2 = v[j].z * r * g.z, f3 = v[j].w * r * g.w;
;             o4[64 * j] = pg8::pk4_fp8(f0, f1, f2, f3);
;             const LAS f32x4* rw = LT + 256 * j + 4 * lane;
;             const f32x4 a0 = rw[0], a1 = rw[D], b0 = rw[1], b1 = rw[D + 1], c0 = rw[2], c1 = rw[D + 2], d0 = rw[3], d1 = rw[D + 3];
;             lg[0] += f0 * a0.x + f1 * b0.x + f2 * c0.x + f3 * d0.x; lg[1] += f0 * a0.y + f1 * b0.y + f2 * c0.y + f3 * d0.y;
;             lg[2] += f0 * a0.z + f1 * b0.z + f2 * c0.z + f3 * d0.z; lg[3] += f0 * a0.w + f1 * b0.w + f2 * c0.w + f3 * d0.w;
;             lg[4] += f0 * a1.x + f1 * b1.x + f2 * c1.x + f3 * d1.x; lg[5] += f0 * a1.y + f1 * b1.y + f2 * c1.y + f3 * d1.y;
;             lg[6] += f0 * a1.z + f1 * b1.z + f2 * c1.z + f3 * d1.z; lg[7] += f0 * a1.w + f1 * b1.w + f2 * c1.w + f3 * d1.w; }
	v_mul_f32_e32 v33, v22, v24
	v_mul_f32_e32 v35, v21, v25
	v_mul_f32_e32 v77, v20, v26
	v_mov_b32_e32 v20, v1
	v_cvt_pk_fp8_f32 v20, v33, v35
	v_mul_f32_e32 v19, v19, v27
	v_cvt_pk_fp8_f32 v20, v77, v19 op_sel:[0,0,1]
	global_store_dword v[50:51], v20, off offset:-256 sc0 sc1
	ds_read_b128 v[20:23], v37 offset:49152
	ds_read_b128 v[24:27], v37 offset:49168
	ds_read_b128 v[28:31], v37 offset:49184
	ds_read_b128 v[54:57], v37 offset:16384
	ds_read_b128 v[58:61], v37 offset:16400
	ds_read_b128 v[62:65], v37 offset:16416
	ds_read_b128 v[66:69], v37 offset:16432
	ds_read_b128 v[70:73], v37 offset:49200
	s_waitcnt lgkmcnt(6)
	v_mul_f32_e32 v24, v35, v24
	v_fmac_f32_e32 v24, v33, v20
	v_mul_f32_e32 v20, v35, v25
	v_fmac_f32_e32 v20, v33, v21
	s_waitcnt lgkmcnt(5)
	v_fmac_f32_e32 v20, v77, v29
	s_waitcnt lgkmcnt(0)
	v_fmac_f32_e32 v20, v19, v71
	v_add_f32_e32 v71, v75, v20
	v_mul_f32_e32 v20, v35, v26
	v_fmac_f32_e32 v20, v33, v22
	v_fmac_f32_e32 v20, v77, v30
	v_fmac_f32_e32 v20, v19, v72
	v_add_f32_e32 v72, v76, v20
	v_mul_f32_e32 v20, v35, v27
	v_fmac_f32_e32 v20, v33, v23
	v_fmac_f32_e32 v20, v77, v31
	v_fmac_f32_e32 v20, v19, v73
	v_add_f32_e32 v32, v32, v20
	global_load_dwordx4 v[20:23], v[40:41], off
	v_mul_f32_e32 v58, v35, v58
	v_fmac_f32_e32 v58, v33, v54
	v_mul_f32_e32 v54, v35, v59
	v_fmac_f32_e32 v54, v33, v55
	v_fmac_f32_e32 v54, v77, v63
	v_fmac_f32_e32 v54, v19, v67
	v_add_f32_e32 v78, v82, v54
	v_mul_f32_e32 v54, v35, v60
	v_fmac_f32_e32 v54, v33, v56
	v_fmac_f32_e32 v54, v77, v64
	v_fmac_f32_e32 v54, v19, v68
	v_add_f32_e32 v79, v83, v54
	v_mul_f32_e32 v54, v35, v61
	v_fmac_f32_e32 v54, v33, v57
	v_fmac_f32_e32 v58, v77, v62
	v_fmac_f32_e32 v54, v77, v65
	v_fmac_f32_e32 v24, v77, v28
	v_fmac_f32_e32 v58, v19, v66
	v_fmac_f32_e32 v54, v19, v69
	v_fmac_f32_e32 v24, v19, v70
	v_add_f32_e32 v53, v53, v58
	v_add_f32_e32 v80, v84, v54
	v_add_f32_e32 v70, v74, v24
	s_waitcnt vmcnt(0)
	v_mul_f32_e32 v33, v18, v20
	v_mul_f32_e32 v35, v17, v21
	v_mul_f32_e32 v73, v16, v22
	v_mov_b32_e32 v16, v1
	v_cvt_pk_fp8_f32 v16, v33, v35
	v_mul_f32_e32 v15, v15, v23
	v_cvt_pk_fp8_f32 v16, v73, v15 op_sel:[0,0,1]
	global_store_dword v[50:51], v16, off sc0 sc1
	ds_read_b128 v[16:19], v37 offset:53248
	ds_read_b128 v[20:23], v37 offset:53264
	ds_read_b128 v[24:27], v37 offset:53280
	ds_read_b128 v[28:31], v37 offset:20480
	ds_read_b128 v[54:57], v37 offset:20496
	ds_read_b128 v[58:61], v37 offset:20512
	ds_read_b128 v[62:65], v37 offset:20528
	ds_read_b128 v[66:69], v37 offset:53296
	s_waitcnt lgkmcnt(6)
	v_mul_f32_e32 v20, v35, v20
	v_fmac_f32_e32 v20, v33, v16
	v_mul_f32_e32 v16, v35, v21
	v_fmac_f32_e32 v16, v33, v17
	s_waitcnt lgkmcnt(5)
	v_fmac_f32_e32 v16, v73, v25
	s_waitcnt lgkmcnt(0)
	v_fmac_f32_e32 v16, v15, v67
	v_add_f32_e32 v67, v71, v16
	v_mul_f32_e32 v16, v35, v22
	v_fmac_f32_e32 v16, v33, v18
	v_fmac_f32_e32 v16, v73, v26
	v_fmac_f32_e32 v16, v15, v68
	v_add_f32_e32 v68, v72, v16
	v_mul_f32_e32 v16, v35, v23
	v_fmac_f32_e32 v16, v33, v19
	v_fmac_f32_e32 v16, v73, v27
	v_fmac_f32_e32 v16, v15, v69
	v_add_f32_e32 v32, v32, v16
	global_load_dwordx4 v[16:19], v[42:43], off
	v_mul_f32_e32 v54, v35, v54
	v_fmac_f32_e32 v54, v33, v28
	v_mul_f32_e32 v28, v35, v55
	v_fmac_f32_e32 v28, v33, v29
	v_fmac_f32_e32 v28, v73, v59
	v_fmac_f32_e32 v28, v15, v63
	v_add_f32_e32 v74, v78, v28
	v_mul_f32_e32 v28, v35, v56
	v_fmac_f32_e32 v28, v33, v30
	v_fmac_f32_e32 v28, v73, v60
	v_fmac_f32_e32 v28, v15, v64
	v_add_f32_e32 v75, v79, v28
	v_mul_f32_e32 v28, v35, v57
	v_fmac_f32_e32 v28, v33, v31
	v_fmac_f32_e32 v54, v73, v58
	v_fmac_f32_e32 v28, v73, v61
	v_fmac_f32_e32 v20, v73, v24
	v_fmac_f32_e32 v54, v15, v62
	v_fmac_f32_e32 v28, v15, v65
	v_fmac_f32_e32 v20, v15, v66
	v_add_f32_e32 v53, v53, v54
	v_add_f32_e32 v76, v80, v28
	v_add_f32_e32 v66, v70, v20
	s_waitcnt vmcnt(0)
	v_mul_f32_e32 v33, v14, v16
	v_mul_f32_e32 v35, v13, v17
	v_mul_f32_e32 v69, v12, v18
	v_mov_b32_e32 v12, v1
	v_cvt_pk_fp8_f32 v12, v33, v35
	v_mul_f32_e32 v11, v11, v19
	v_cvt_pk_fp8_f32 v12, v69, v11 op_sel:[0,0,1]
	global_store_dword v[50:51], v12, off offset:256 sc0 sc1
	ds_read_b128 v[12:15], v37 offset:57344
	ds_read_b128 v[16:19], v37 offset:57360
	ds_read_b128 v[20:23], v37 offset:57376
	ds_read_b128 v[24:27], v37 offset:24576
	ds_read_b128 v[28:31], v37 offset:24592
	ds_read_b128 v[54:57], v37 offset:24608
	ds_read_b128 v[58:61], v37 offset:24624
	ds_read_b128 v[62:65], v37 offset:57392
	s_waitcnt lgkmcnt(6)
	v_mul_f32_e32 v16, v35, v16
	v_fmac_f32_e32 v16, v33, v12
	v_mul_f32_e32 v12, v35, v17
	v_fmac_f32_e32 v12, v33, v13
	s_waitcnt lgkmcnt(5)
	v_fmac_f32_e32 v12, v69, v21
	s_waitcnt lgkmcnt(0)
	v_fmac_f32_e32 v12, v11, v63
	v_add_f32_e32 v71, v67, v12
	v_mul_f32_e32 v12, v35, v18
	v_fmac_f32_e32 v12, v33, v14
	v_fmac_f32_e32 v12, v69, v22
	v_fmac_f32_e32 v12, v11, v64
	v_add_f32_e32 v68, v68, v12
	v_mul_f32_e32 v12, v35, v19
	v_fmac_f32_e32 v12, v33, v15
	v_fmac_f32_e32 v12, v69, v23
	v_fmac_f32_e32 v12, v11, v65
	v_add_f32_e32 v32, v32, v12
	global_load_dwordx4 v[12:15], v[44:45], off
	v_mul_f32_e32 v28, v35, v28
	v_fmac_f32_e32 v28, v33, v24
	v_mul_f32_e32 v24, v35, v29
	v_fmac_f32_e32 v24, v33, v25
	v_fmac_f32_e32 v24, v69, v55
	v_fmac_f32_e32 v28, v69, v54
	v_fmac_f32_e32 v24, v11, v59
	v_fmac_f32_e32 v28, v11, v58
	v_add_f32_e32 v58, v74, v24
	v_mul_f32_e32 v24, v35, v30
	v_fmac_f32_e32 v24, v33, v26
	v_fmac_f32_e32 v24, v69, v56
	v_fmac_f32_e32 v24, v11, v60
	v_add_f32_e32 v59, v75, v24
	v_mul_f32_e32 v24, v35, v31
	v_fmac_f32_e32 v24, v33, v27
	v_fmac_f32_e32 v24, v69, v57
	v_fmac_f32_e32 v16, v69, v20
	v_fmac_f32_e32 v24, v11, v61
	v_fmac_f32_e32 v16, v11, v62
	v_add_f32_e32 v53, v53, v28
	v_add_f32_e32 v60, v76, v24
	v_add_f32_e32 v70, v66, v16
	s_waitcnt vmcnt(0)
; __device__ __forceinline__ unsigned pk4_fp8(float a, float b, float c, float d) { int w = 0; w = __builtin_amdgcn_cvt_pk_fp8_f32(a, b, w, false); w = __builtin_amdgcn_cvt_pk_fp8_f32(c, d, w, true); return (unsigned)w; }
; #define GAS __attribute__((address_space(1)))
; #define LAS __attribute__((address_space(3)))
; #define lane (lane_id())
; __device__ __forceinline__ void router_phase(const Ptrs& P, const float* gain, LAS unsigned char* lds, int vcu, int G, int tid, int wave, int lane) {
;     ...
;         for (int j = 0; j < 8; ++j) { const f32x4 g = ((const GAS f32x4*)gain)[lane + 64 * j];
;             const float f0 = v[j].x * r * g.x, f1 = v[j].y * r * g.y, f2 = v[j].z * r * g.z, f3 = v[j].w * r * g.w;
;             o4[64 * j] = pg8::pk4_fp8(f0, f1, f2, f3);
;             const LAS f32x4* rw = LT + 256 * j + 4 * lane;
;             const f32x4 a0 = rw[0], a1 = rw[D], b0 = rw[1], b1 = rw[D + 1], c0 = rw[2], c1 = rw[D + 2], d0 = rw[3], d1 = rw[D + 3];
;             lg[0] += f0 * a0.x + f1 * b0.x + f2 * c0.x + f3 * d0.x; lg[1] += f0 * a0.y + f1 * b0.y + f2 * c0.y + f3 * d0.y;
;             lg[2] += f0 * a0.z + f1 * b0.z + f2 * c0.z + f3 * d0.z; lg[3] += f0 * a0.w + f1 * b0.w + f2 * c0.w + f3 * d0.w;
;             lg[4] += f0 * a1.x + f1 * b1.x + f2 * c1.x + f3 * d1.x; lg[5] += f0 * a1.y + f1 * b1.y + f2 * c1.y + f3 * d1.y;
;             lg[6] += f0 * a1.z + f1 * b1.z + f2 * c1.z + f3 * d1.z; lg[7] += f0 * a1.w + f1 * b1.w + f2 * c1.w + f3 * d1.w; }
; #pragma unroll
;         for (int e = 0; e < 8; ++e) lg[e] = wave_sum(lg[e]);
	v_mul_f32_e32 v33, v10, v12
	v_mul_f32_e32 v35, v9, v13
	v_mul_f32_e32 v69, v8, v14
	v_mov_b32_e32 v8, v1
	v_cvt_pk_fp8_f32 v8, v33, v35
	v_mul_f32_e32 v7, v7, v15
	v_cvt_pk_fp8_f32 v8, v69, v7 op_sel:[0,0,1]
	global_store_dword v[50:51], v8, off offset:512 sc0 sc1
	ds_read_b128 v[8:11], v37 offset:61440
	ds_read_b128 v[12:15], v37 offset:61456
	ds_read_b128 v[16:19], v37 offset:61472
	ds_read_b128 v[20:23], v37 offset:28672
	ds_read_b128 v[24:27], v37 offset:28688
	ds_read_b128 v[28:31], v37 offset:28704
	ds_read_b128 v[54:57], v37 offset:28720
	ds_read_b128 v[64:67], v37 offset:61488
	s_waitcnt lgkmcnt(6)
	v_mul_f32_e32 v12, v35, v12
	s_waitcnt lgkmcnt(3)
	v_mul_f32_e32 v24, v35, v24
	v_fmac_f32_e32 v24, v33, v20
	v_mul_f32_e32 v20, v35, v25
	v_fmac_f32_e32 v20, v33, v21
	s_waitcnt lgkmcnt(2)
	v_fmac_f32_e32 v20, v69, v29
	s_waitcnt lgkmcnt(1)
	v_fmac_f32_e32 v20, v7, v55
	v_fmac_f32_e32 v12, v33, v8
	v_mul_f32_e32 v8, v35, v13
	v_add_f32_e32 v62, v58, v20
	v_mul_f32_e32 v20, v35, v26
	v_fmac_f32_e32 v8, v33, v9
	v_fmac_f32_e32 v20, v33, v22
	v_fmac_f32_e32 v8, v69, v17
	v_fmac_f32_e32 v20, v69, v30
	s_waitcnt lgkmcnt(0)
	v_fmac_f32_e32 v8, v7, v65
	v_fmac_f32_e32 v20, v7, v56
	v_add_f32_e32 v58, v71, v8
	v_mul_f32_e32 v8, v35, v14
	v_add_f32_e32 v61, v59, v20
	v_mul_f32_e32 v20, v35, v27
	v_fmac_f32_e32 v8, v33, v10
	v_fmac_f32_e32 v20, v33, v23
	v_fmac_f32_e32 v8, v69, v18
	v_fmac_f32_e32 v20, v69, v31
	v_fmac_f32_e32 v8, v7, v66
	v_fmac_f32_e32 v20, v7, v57
	v_add_f32_e32 v57, v68, v8
	v_mul_f32_e32 v8, v35, v15
	v_fmac_f32_e32 v8, v33, v11
	v_fmac_f32_e32 v8, v69, v19
	v_fmac_f32_e32 v8, v7, v67
	v_add_f32_e32 v35, v32, v8
	global_load_dwordx4 v[8:11], v[46:47], off
	v_fmac_f32_e32 v24, v69, v28
	v_fmac_f32_e32 v24, v7, v54
	v_add_f32_e32 v63, v53, v24
	v_fmac_f32_e32 v12, v69, v16
	v_fmac_f32_e32 v12, v7, v64
	v_add_f32_e32 v60, v60, v20
	v_add_f32_e32 v59, v70, v12
	s_waitcnt vmcnt(0)
	v_mul_f32_e32 v55, v5, v8
	v_mul_f32_e32 v56, v4, v9
	v_mul_f32_e32 v53, v2, v11
	v_mov_b32_e32 v2, v1
	v_cvt_pk_fp8_f32 v2, v55, v56
	v_mul_f32_e32 v54, v3, v10
	v_cvt_pk_fp8_f32 v2, v54, v53 op_sel:[0,0,1]
	global_store_dword v[50:51], v2, off offset:768 sc0 sc1
	ds_read_b128 v[6:9], v37 offset:32768
	ds_read_b128 v[14:17], v37 offset:32784
	ds_read_b128 v[26:29], v37 offset:32800
	ds_read_b128 v[30:33], v37 offset:32816
	ds_read_b128 v[2:5], v52 offset:61440
	ds_read_b128 v[22:25], v52 offset:61456
	ds_read_b128 v[18:21], v52 offset:61472
	ds_read_b128 v[10:13], v52 offset:61488
	s_waitcnt lgkmcnt(6)
	v_mul_f32_e32 v14, v56, v14
	v_fmac_f32_e32 v14, v55, v6
	s_waitcnt lgkmcnt(5)
	v_fmac_f32_e32 v14, v54, v26
	s_waitcnt lgkmcnt(4)
	v_fmac_f32_e32 v14, v53, v30
	v_add_f32_e32 v6, v63, v14
	v_mul_f32_e32 v14, v56, v15
	v_fmac_f32_e32 v14, v55, v7
	v_fmac_f32_e32 v14, v54, v27
	v_fmac_f32_e32 v14, v53, v31
	v_add_f32_e32 v7, v62, v14
	v_mul_f32_e32 v14, v56, v16
	v_fmac_f32_e32 v14, v55, v8
	v_fmac_f32_e32 v14, v54, v28
	v_fmac_f32_e32 v14, v53, v32
	v_add_f32_e32 v8, v61, v14
	v_mul_f32_e32 v14, v56, v17
	v_fmac_f32_e32 v14, v55, v9
	v_fmac_f32_e32 v14, v54, v29
	v_fmac_f32_e32 v14, v53, v33
	v_add_f32_e32 v9, v60, v14
	s_waitcnt lgkmcnt(2)
	v_mul_f32_e32 v14, v56, v22
	v_fmac_f32_e32 v14, v55, v2
	v_mul_f32_e32 v2, v56, v23
	v_fmac_f32_e32 v2, v55, v3
	s_waitcnt lgkmcnt(1)
	v_fmac_f32_e32 v14, v54, v18
	v_fmac_f32_e32 v2, v54, v19
	s_waitcnt lgkmcnt(0)
	v_fmac_f32_e32 v14, v53, v10
	v_fmac_f32_e32 v2, v53, v11
	v_add_f32_e32 v10, v59, v14
	v_add_f32_e32 v14, v58, v2
	v_mul_f32_e32 v2, v56, v24
	v_fmac_f32_e32 v2, v55, v4
	v_fmac_f32_e32 v2, v54, v20
	v_fmac_f32_e32 v2, v53, v12
	v_add_f32_e32 v15, v57, v2
	v_mul_f32_e32 v2, v56, v25
	v_fmac_f32_e32 v2, v55, v5
	v_fmac_f32_e32 v2, v54, v21
	v_fmac_f32_e32 v2, v53, v13
	v_add_f32_e32 v16, v35, v2
	v_add_f32_dpp v10, v10, v10 quad_perm:[1,0,3,2] row_mask:0xf bank_mask:0xf bound_ctrl:1
	v_add_f32_dpp v2, v6, v6 quad_perm:[1,0,3,2] row_mask:0xf bank_mask:0xf bound_ctrl:1
	v_add_f32_dpp v6, v8, v8 quad_perm:[1,0,3,2] row_mask:0xf bank_mask:0xf bound_ctrl:1
	v_add_f32_dpp v8, v9, v9 quad_perm:[1,0,3,2] row_mask:0xf bank_mask:0xf bound_ctrl:1
	v_add_f32_dpp v2, v2, v2 quad_perm:[2,3,0,1] row_mask:0xf bank_mask:0xf bound_ctrl:1
	ds_swizzle_b32 v3, v2 offset:swizzle(SWAP,4)
	v_add_f32_dpp v12, v14, v14 quad_perm:[1,0,3,2] row_mask:0xf bank_mask:0xf bound_ctrl:1
	v_add_f32_dpp v14, v15, v15 quad_perm:[1,0,3,2] row_mask:0xf bank_mask:0xf bound_ctrl:1
	v_add_f32_dpp v16, v16, v16 quad_perm:[1,0,3,2] row_mask:0xf bank_mask:0xf bound_ctrl:1
	v_add_f32_dpp v6, v6, v6 quad_perm:[2,3,0,1] row_mask:0xf bank_mask:0xf bound_ctrl:1
	s_waitcnt lgkmcnt(0)
	v_add_f32_e32 v2, v2, v3
	ds_swizzle_b32 v3, v2 offset:swizzle(SWAP,8)
	v_add_f32_dpp v8, v8, v8 quad_perm:[2,3,0,1] row_mask:0xf bank_mask:0xf bound_ctrl:1
	v_add_f32_dpp v10, v10, v10 quad_perm:[2,3,0,1] row_mask:0xf bank_mask:0xf bound_ctrl:1
	v_add_f32_dpp v12, v12, v12 quad_perm:[2,3,0,1] row_mask:0xf bank_mask:0xf bound_ctrl:1
	v_add_f32_dpp v14, v14, v14 quad_perm:[2,3,0,1] row_mask:0xf bank_mask:0xf bound_ctrl:1
	s_waitcnt lgkmcnt(0)
	v_add_f32_e32 v2, v2, v3
	ds_swizzle_b32 v3, v2 offset:swizzle(SWAP,16)
	v_add_f32_dpp v16, v16, v16 quad_perm:[2,3,0,1] row_mask:0xf bank_mask:0xf bound_ctrl:1
	ds_swizzle_b32 v9, v8 offset:swizzle(SWAP,4)
	ds_swizzle_b32 v11, v10 offset:swizzle(SWAP,4)
	ds_swizzle_b32 v13, v12 offset:swizzle(SWAP,4)
	s_waitcnt lgkmcnt(3)
	v_add_f32_e32 v3, v2, v3
	v_add_f32_dpp v2, v7, v7 quad_perm:[1,0,3,2] row_mask:0xf bank_mask:0xf bound_ctrl:1
	ds_swizzle_b32 v7, v6 offset:swizzle(SWAP,4)
	ds_swizzle_b32 v15, v14 offset:swizzle(SWAP,4)
	v_add_f32_dpp v2, v2, v2 quad_perm:[2,3,0,1] row_mask:0xf bank_mask:0xf bound_ctrl:1
	ds_swizzle_b32 v4, v2 offset:swizzle(SWAP,4)
	ds_swizzle_b32 v17, v16 offset:swizzle(SWAP,4)
	s_waitcnt lgkmcnt(3)
; #define lane (lane_id())
; __device__ __forceinline__ void router_phase(const Ptrs& P, const float* gain, LAS unsigned char* lds, int vcu, int G, int tid, int wave, int lane) {
;     ...
;         for (int e = 0; e < 8; ++e) lg[e] = wave_sum(lg[e]);
;         int e0 = 0; float b0v = lg[0];
; #pragma unroll
;         for (int e = 1; e < 8; ++e) if (lg[e] > b0v) { b0v = lg[e]; e0 = e; }
;         int e1 = -1; float b1v = -__builtin_inff();
; #pragma unroll
;         for (int e = 0; e < 8; ++e) if (e != e0 && lg[e] > b1v) { b1v = lg[e]; e1 = e; }
;         const float g1 = 1.0f / (1.0f + __expf(b0v - b1v)), g0 = 1.0f - g1;
;         if (lane == 0) {
;             const unsigned k0 = __hip_atomic_fetch_add(lcnt + e0, 1u, __ATOMIC_RELAXED, __HIP_MEMORY_SCOPE_WORKGROUP);
;             const unsigned k1 = __hip_atomic_fetch_add(lcnt + e1, 1u, __ATOMIC_RELAXED, __HIP_MEMORY_SCOPE_WORKGROUP);
;             rinfo[li * 4 + 0] = (unsigned)e0 | ((unsigned)e1 << 8); rinfo[li * 4 + 1] = k0; rinfo[li * 4 + 2] = k1;
;             P.sel_g[2 * m] = g0; P.sel_g[2 * m + 1] = g1;
;         }
	v_add_f32_e32 v6, v6, v7
	v_add_f32_e32 v8, v8, v9
	v_add_f32_e32 v10, v10, v11
	s_waitcnt lgkmcnt(1)
	v_add_f32_e32 v2, v2, v4
	v_add_f32_e32 v12, v12, v13
	v_add_f32_e32 v14, v14, v15
	s_waitcnt lgkmcnt(0)
	v_add_f32_e32 v16, v16, v17
	ds_swizzle_b32 v4, v2 offset:swizzle(SWAP,8)
	ds_swizzle_b32 v7, v6 offset:swizzle(SWAP,8)
	ds_swizzle_b32 v9, v8 offset:swizzle(SWAP,8)
	ds_swizzle_b32 v11, v10 offset:swizzle(SWAP,8)
	ds_swizzle_b32 v13, v12 offset:swizzle(SWAP,8)
	ds_swizzle_b32 v15, v14 offset:swizzle(SWAP,8)
	ds_swizzle_b32 v17, v16 offset:swizzle(SWAP,8)
	s_waitcnt lgkmcnt(6)
	v_add_f32_e32 v2, v2, v4
	s_waitcnt lgkmcnt(5)
	v_add_f32_e32 v6, v6, v7
	s_waitcnt lgkmcnt(4)
	v_add_f32_e32 v8, v8, v9
	s_waitcnt lgkmcnt(3)
	v_add_f32_e32 v10, v10, v11
	s_waitcnt lgkmcnt(2)
	v_add_f32_e32 v12, v12, v13
	s_waitcnt lgkmcnt(1)
	v_add_f32_e32 v14, v14, v15
	s_waitcnt lgkmcnt(0)
	v_add_f32_e32 v16, v16, v17
	ds_swizzle_b32 v4, v2 offset:swizzle(SWAP,16)
	ds_swizzle_b32 v7, v6 offset:swizzle(SWAP,16)
	ds_swizzle_b32 v9, v8 offset:swizzle(SWAP,16)
	ds_swizzle_b32 v11, v10 offset:swizzle(SWAP,16)
	ds_swizzle_b32 v13, v12 offset:swizzle(SWAP,16)
	ds_swizzle_b32 v15, v14 offset:swizzle(SWAP,16)
	ds_swizzle_b32 v17, v16 offset:swizzle(SWAP,16)
	s_waitcnt lgkmcnt(6)
	v_add_f32_e32 v2, v2, v4
	s_waitcnt lgkmcnt(5)
	v_add_f32_e32 v6, v6, v7
	s_waitcnt lgkmcnt(4)
	v_add_f32_e32 v8, v8, v9
	s_waitcnt lgkmcnt(3)
	v_add_f32_e32 v10, v10, v11
	s_waitcnt lgkmcnt(2)
	v_add_f32_e32 v12, v12, v13
	s_waitcnt lgkmcnt(1)
	v_add_f32_e32 v14, v14, v15
	s_waitcnt lgkmcnt(0)
	v_add_f32_e32 v16, v16, v17
	v_mov_b32_e32 v5, v3
	v_mov_b32_e32 v4, v2
	v_mov_b32_e32 v7, v6
	v_mov_b32_e32 v9, v8
	v_mov_b32_e32 v11, v10
	v_mov_b32_e32 v13, v12
	v_mov_b32_e32 v15, v14
	v_mov_b32_e32 v17, v16
	v_permlane32_swap_b32_e32 v3, v5
	v_permlane32_swap_b32_e32 v2, v4
	v_permlane32_swap_b32_e32 v6, v7
	v_permlane32_swap_b32_e32 v8, v9
	v_permlane32_swap_b32_e32 v10, v11
	v_permlane32_swap_b32_e32 v12, v13
	v_permlane32_swap_b32_e32 v14, v15
	v_permlane32_swap_b32_e32 v16, v17
	s_and_saveexec_b64 s[28:29], s[38:39]
	s_cbranch_execz .LBB0_1474
	v_pk_add_f32 v[2:3], v[2:3], v[4:5]
	v_add_f32_e32 v6, v6, v7
	v_cmp_gt_f32_e32 vcc, v2, v3
	v_add_f32_e32 v8, v8, v9
	v_add_f32_e32 v10, v10, v11
	v_cndmask_b32_e32 v4, v3, v2, vcc
	v_cmp_gt_f32_e64 s[40:41], v6, v4
	v_add_f32_e32 v12, v12, v13
	v_cndmask_b32_e64 v5, 0, 1, vcc
	v_cndmask_b32_e64 v4, v4, v6, s[40:41]
	v_cmp_gt_f32_e64 s[42:43], v8, v4
	v_cndmask_b32_e64 v5, v5, 2, s[40:41]
	v_add_f32_e32 v14, v14, v15
	v_cndmask_b32_e64 v4, v4, v8, s[42:43]
	v_cmp_gt_f32_e64 s[44:45], v10, v4
	v_cndmask_b32_e64 v5, v5, 3, s[42:43]
	v_add_f32_e32 v16, v16, v17
	v_cndmask_b32_e64 v4, v4, v10, s[44:45]
	v_cmp_gt_f32_e64 s[46:47], v12, v4
	v_cndmask_b32_e64 v5, v5, 4, s[44:45]
	s_mov_b32 s27, 0xff800000
	v_cndmask_b32_e64 v4, v4, v12, s[46:47]
	v_cmp_gt_f32_e64 s[48:49], v14, v4
	v_cndmask_b32_e64 v5, v5, 5, s[46:47]
	v_cmp_nlg_f32_e64 s[52:53], s27, v3
	v_cndmask_b32_e64 v4, v4, v14, s[48:49]
	v_cndmask_b32_e64 v5, v5, 6, s[48:49]
	v_cmp_ngt_f32_e32 vcc, v16, v4
	s_and_b64 s[34:35], s[48:49], vcc
	s_ashr_i32 s27, s26, 31
	v_cndmask_b32_e32 v5, 7, v5, vcc
	v_cmp_eq_u32_e64 s[50:51], 0, v5
	s_or_b64 s[50:51], s[50:51], s[52:53]
	v_cmp_ne_u32_e64 s[48:49], 1, v5
	v_cndmask_b32_e64 v3, v3, v206, s[50:51]
	v_cmp_gt_f32_e64 s[52:53], v2, v3
	s_and_b64 s[48:49], s[48:49], s[52:53]
	v_cndmask_b32_e64 v2, v3, v2, s[48:49]
	v_cmp_ne_u32_e64 s[46:47], 2, v5
	v_cmp_gt_f32_e64 s[52:53], v6, v2
	s_and_b64 s[46:47], s[46:47], s[52:53]
	v_cndmask_b32_e64 v2, v2, v6, s[46:47]
	v_cmp_ne_u32_e64 s[44:45], 3, v5
	v_cmp_gt_f32_e64 s[52:53], v8, v2
	s_and_b64 s[44:45], s[44:45], s[52:53]
	v_cndmask_b32_e64 v2, v2, v8, s[44:45]
	v_cmp_ne_u32_e64 s[42:43], 4, v5
	v_cmp_gt_f32_e64 s[52:53], v10, v2
	s_and_b64 s[42:43], s[42:43], s[52:53]
	v_cndmask_b32_e64 v2, v2, v10, s[42:43]
	v_cmp_ne_u32_e64 s[40:41], 5, v5
	v_cmp_gt_f32_e64 s[52:53], v12, v2
	s_and_b64 s[40:41], s[40:41], s[52:53]
	v_cndmask_b32_e64 v2, v2, v12, s[40:41]
	v_cmp_ngt_f32_e64 s[52:53], v14, v2
	s_or_b64 s[52:53], s[34:35], s[52:53]
	v_cndmask_b32_e32 v4, v16, v4, vcc
	v_cndmask_b32_e64 v2, v14, v2, s[52:53]
	v_cmp_gt_f32_e64 s[54:55], v16, v2
	s_and_b64 s[54:55], vcc, s[54:55]
	v_cndmask_b32_e64 v3, 0, -1, s[50:51]
	v_cndmask_b32_e64 v2, v2, v16, s[54:55]
	v_sub_f32_e32 v2, v4, v2
	v_mul_f32_e32 v2, 0x3fb8aa3b, v2
	v_exp_f32_e32 v2, v2
	v_cndmask_b32_e64 v3, v3, 1, s[48:49]
	v_cndmask_b32_e64 v3, v3, 2, s[46:47]
	v_cndmask_b32_e64 v3, v3, 3, s[44:45]
	v_add_f32_e32 v2, 1.0, v2
	v_div_scale_f32 v4, s[34:35], v2, v2, 1.0
	v_rcp_f32_e32 v6, v4
	v_cndmask_b32_e64 v3, v3, 4, s[42:43]
	v_cndmask_b32_e64 v3, v3, 5, s[40:41]
	v_cndmask_b32_e64 v3, 6, v3, s[52:53]
	v_cndmask_b32_e64 v8, v3, 7, s[54:55]
	v_fma_f32 v3, -v4, v6, 1.0
	v_fmac_f32_e32 v6, v3, v6
	v_div_scale_f32 v3, vcc, 1.0, v2, 1.0
	v_mul_f32_e32 v7, v3, v6
	v_fma_f32 v9, -v4, v7, v3
	v_fmac_f32_e32 v7, v9, v6
	v_fma_f32 v3, -v4, v7, v3
	v_div_fmas_f32 v6, v3, v6, v7
	v_lshl_add_u32 v3, v5, 2, 0
	v_mov_b32_e32 v7, 1
	ds_add_rtn_u32 v3, v3, v7
	v_lshl_add_u32 v4, v8, 2, 0
	ds_add_rtn_u32 v4, v4, v7
	s_lshl_b64 s[34:35], s[26:27], 2
	v_readlane_b32 s44, v253, 44
	v_div_fixup_f32 v7, v6, v2, 1.0
	s_add_u32 s34, s18, s34
	v_readlane_b32 s53, v254, 43
	v_readlane_b32 s45, v253, 45
	v_readlane_b32 s50, v254, 40
	v_readlane_b32 s48, v254, 38
	v_sub_f32_e32 v6, 1.0, v7
	v_lshl_add_u32 v2, v8, 8, v5
	v_mov_b32_e32 v5, s23
	s_addc_u32 s35, s19, s35
	v_readlane_b32 s51, v254, 41
	v_readlane_b32 s49, v254, 39
	s_waitcnt lgkmcnt(0)
	ds_write_b96 v5, v[2:4]
	global_store_dwordx2 v1, v[6:7], s[34:35] sc0 sc1
	s_branch .LBB0_1474

; #define lane (lane_id())
; __device__ __forceinline__ void router_phase(const Ptrs& P, const float* gain, LAS unsigned char* lds, int vcu, int G, int tid, int wave, int lane) {
;     ...
;     for (int m = gw; m < M; m += NGW, li += NWAVES) {
;         if (lane == 0) { const unsigned ee = rinfo[li * 4 + 0]; const unsigned e0 = ee & 0xffu, e1 = ee >> 8;
;             P.sel_e[m] = ee; P.sel_rel[2 * m] = (int)(lcnt[8 + e0] + rinfo[li * 4 + 1]); P.sel_rel[2 * m + 1] = (int)(lcnt[8 + e1] + rinfo[li * 4 + 2]); }
;     }
.LBB0_1482:
	s_and_saveexec_b64 s[18:19], vcc
	s_cbranch_execz .LBB0_1481
	v_mov_b32_e32 v0, s23
	ds_read_b96 v[2:4], v0
	v_mov_b32_e32 v0, 2
	s_ashr_i32 s25, s24, 31
	s_lshl_b64 s[30:31], s[24:25], 2
	s_add_u32 s30, s28, s30
	s_waitcnt lgkmcnt(0)
	global_store_dword v1, v2, s[26:27] sc0 sc1
	v_lshlrev_b32_sdwa v0, v0, v2 dst_sel:DWORD dst_unused:UNUSED_PAD src0_sel:DWORD src1_sel:BYTE_0
	v_lshrrev_b32_e32 v2, 6, v2
	v_and_b32_e32 v2, 0x3fffffc, v2
	v_add_u32_e32 v0, 0, v0
	v_add_u32_e32 v2, 0, v2
	ds_read_b32 v0, v0 offset:32
	ds_read_b32 v2, v2 offset:32
	s_addc_u32 s31, s29, s31
	s_waitcnt lgkmcnt(0)
	v_add_u32_e32 v5, v4, v2
	v_add_u32_e32 v4, v3, v0
	global_store_dwordx2 v1, v[4:5], s[30:31] sc0 sc1
	s_branch .LBB0_1481

; #define GAS __attribute__((address_space(1)))
; __device__ __forceinline__ f32x4 bf4_to_f32(u32x2_g a) { return (f32x4){__uint_as_float(a.x << 16), __uint_as_float(a.x & 0xffff0000u), __uint_as_float(a.y << 16), __uint_as_float(a.y & 0xffff0000u)}; }
; #define lane (lane_id())
; template <bool F8, bool SRC16, int NR> __device__ __forceinline__ void norm_rows(const void* srcv, const float* gain, void* dstv, int vcu, int G, int wave, int lane) {
;     ...
;     for (int m0 = gw; m0 < M; m0 += NR * NGW) {
;         f32x4 v[NR][8];
; #pragma unroll
;         for (int q = 0; q < NR; ++q) { const int mq = m0 + q * NGW; const int m = mq < M ? mq : m0;
;             if constexpr (SRC16) { const GAS u32x2_g* xr = (const GAS u32x2_g*)((const bf16*)srcv + (size_t)m * D) + lane;
; #pragma unroll
;                 for (int j = 0; j < 8; ++j) v[q][j] = bf4_to_f32(xr[64 * j]); }
;             else { const GAS f32x4* xr = (const GAS f32x4*)((const float*)srcv + (size_t)m * D) + lane;
; #pragma unroll
;                 for (int j = 0; j < 8; ++j) v[q][j] = xr[64 * j]; } }
; #pragma unroll
;         for (int q = 0; q < NR; ++q) { const int m = m0 + q * NGW; if (m >= M) break;
;             float s = 0.f;
; #pragma unroll
;             for (int j = 0; j < 8; ++j) s += (v[q][j].x * v[q][j].x + v[q][j].y * v[q][j].y) + (v[q][j].z * v[q][j].z + v[q][j].w * v[q][j].w);
;             const float r = 1.0f / sqrtf(wave_sum(s) * (1.0f / D) + EPS);
.LBB0_1489:
	global_load_dwordx2 v[42:43], v[40:41], off offset:1536
	global_load_dwordx2 v[44:45], v[40:41], off offset:1024
	global_load_dwordx2 v[46:47], v[40:41], off offset:512
	global_load_dwordx2 v[48:49], v[40:41], off
	global_load_dwordx2 v[50:51], v[40:41], off offset:-512
	global_load_dwordx2 v[52:53], v[40:41], off offset:-1024
	global_load_dwordx2 v[54:55], v[40:41], off offset:-1536
	global_load_dwordx2 v[56:57], v[40:41], off offset:-2048
	s_add_i32 s19, s68, s18
	s_cmpk_lt_i32 s19, 0x2000
	s_cselect_b32 s14, s19, s18
	s_ashr_i32 s15, s14, 31
	s_add_i32 s20, s50, s18
	s_lshl_b64 s[14:15], s[14:15], 12
	s_cmpk_lt_i32 s20, 0x2000
	s_cselect_b64 s[22:23], -1, 0
	s_waitcnt vmcnt(24)
	v_lshl_add_u64 v[58:59], v[34:35], 0, s[14:15]
	s_and_b64 s[14:15], s[22:23], exec
	s_cselect_b32 s16, s20, s18
	s_ashr_i32 s17, s16, 31
	s_lshl_b64 s[26:27], s[16:17], 12
	global_load_dwordx2 v[74:75], v[58:59], off
	global_load_dwordx2 v[76:77], v[58:59], off offset:512
	global_load_dwordx2 v[78:79], v[58:59], off offset:1024
	global_load_dwordx2 v[80:81], v[58:59], off offset:1536
	global_load_dwordx2 v[82:83], v[58:59], off offset:2048
	global_load_dwordx2 v[84:85], v[58:59], off offset:2560
	global_load_dwordx2 v[86:87], v[58:59], off offset:3072
	global_load_dwordx2 v[88:89], v[58:59], off offset:3584
	s_add_i32 s14, s53, s18
	s_cmpk_lt_i32 s14, 0x2000
	s_cselect_b64 s[16:17], -1, 0
	s_and_b64 s[24:25], s[16:17], exec
	s_cselect_b32 s24, s14, s18
	s_ashr_i32 s25, s24, 31
	s_lshl_b64 s[24:25], s[24:25], 12
	s_cmpk_gt_i32 s19, 0x1fff
	s_waitcnt vmcnt(15)
	v_lshlrev_b32_e32 v0, 16, v42
	v_and_b32_e32 v92, 0xffff0000, v42
	v_lshlrev_b32_e32 v93, 16, v43
	v_and_b32_e32 v94, 0xffff0000, v43
	s_waitcnt vmcnt(14)
	v_lshlrev_b32_e32 v95, 16, v44
	v_and_b32_e32 v96, 0xffff0000, v44
	s_waitcnt vmcnt(9)
	v_and_b32_e32 v116, 0xffff0000, v54
	v_and_b32_e32 v118, 0xffff0000, v55
	s_waitcnt vmcnt(8)
	v_and_b32_e32 v120, 0xffff0000, v56
	v_and_b32_e32 v122, 0xffff0000, v57
	v_lshlrev_b32_e32 v97, 16, v45
	v_and_b32_e32 v98, 0xffff0000, v45
	v_and_b32_e32 v112, 0xffff0000, v52
	v_and_b32_e32 v114, 0xffff0000, v53
	v_lshlrev_b32_e32 v115, 16, v54
	v_lshlrev_b32_e32 v117, 16, v55
	v_lshlrev_b32_e32 v119, 16, v56
	v_lshlrev_b32_e32 v121, 16, v57
	v_mul_f32_e32 v42, v120, v120
	v_mul_f32_e32 v43, v122, v122
	v_mul_f32_e32 v44, v116, v116
	v_mul_f32_e32 v45, v118, v118
	v_lshlrev_b32_e32 v99, 16, v46
	v_and_b32_e32 v100, 0xffff0000, v46
	v_lshlrev_b32_e32 v101, 16, v47
	v_and_b32_e32 v102, 0xffff0000, v47
	v_and_b32_e32 v108, 0xffff0000, v50
	v_and_b32_e32 v110, 0xffff0000, v51
	v_lshlrev_b32_e32 v111, 16, v52
	v_lshlrev_b32_e32 v113, 16, v53
	v_mul_f32_e32 v46, v112, v112
	v_mul_f32_e32 v47, v114, v114
	v_fmac_f32_e32 v42, v119, v119
	v_fmac_f32_e32 v43, v121, v121
	v_fmac_f32_e32 v44, v115, v115
	v_fmac_f32_e32 v45, v117, v117
	v_lshlrev_b32_e32 v103, 16, v48
	v_and_b32_e32 v104, 0xffff0000, v48
	v_lshlrev_b32_e32 v105, 16, v49
	v_and_b32_e32 v106, 0xffff0000, v49
	v_lshlrev_b32_e32 v107, 16, v50
	v_lshlrev_b32_e32 v109, 16, v51
	v_mul_f32_e32 v48, v108, v108
	v_mul_f32_e32 v49, v110, v110
	v_fmac_f32_e32 v46, v111, v111
	v_fmac_f32_e32 v47, v113, v113
	v_add_f32_e32 v42, v42, v43
	v_add_f32_e32 v43, v44, v45
	v_fmac_f32_e32 v48, v107, v107
	v_fmac_f32_e32 v49, v109, v109
	v_add_f32_e32 v44, v46, v47
	v_add_f32_e32 v42, v43, v42
	v_add_f32_e32 v42, v44, v42
	v_add_f32_e32 v43, v48, v49
	v_add_f32_e32 v42, v43, v42
	v_mul_f32_e32 v43, v104, v104
	v_mul_f32_e32 v44, v106, v106
	v_fmac_f32_e32 v43, v103, v103
	v_fmac_f32_e32 v44, v105, v105
	v_add_f32_e32 v43, v43, v44
	v_add_f32_e32 v42, v43, v42
	v_mul_f32_e32 v43, v100, v100
	v_mul_f32_e32 v44, v102, v102
	v_fmac_f32_e32 v43, v99, v99
	v_fmac_f32_e32 v44, v101, v101
	v_add_f32_e32 v43, v43, v44
	v_add_f32_e32 v42, v43, v42
	v_mul_f32_e32 v43, v96, v96
	v_mul_f32_e32 v44, v98, v98
	v_fmac_f32_e32 v43, v95, v95
	v_fmac_f32_e32 v44, v97, v97
	v_add_f32_e32 v43, v43, v44
	v_add_f32_e32 v42, v43, v42
	v_mul_f32_e32 v43, v92, v92
	v_mul_f32_e32 v44, v94, v94
	v_fmac_f32_e32 v43, v0, v0
	v_fmac_f32_e32 v44, v93, v93
	v_add_f32_e32 v43, v43, v44
	v_add_f32_e32 v42, v43, v42
	s_nop 1
	v_add_f32_dpp v42, v42, v42 quad_perm:[1,0,3,2] row_mask:0xf bank_mask:0xf bound_ctrl:1
	s_nop 1
	v_add_f32_dpp v44, v42, v42 quad_perm:[2,3,0,1] row_mask:0xf bank_mask:0xf bound_ctrl:1
	ds_swizzle_b32 v45, v44 offset:swizzle(SWAP,4)
	v_lshl_add_u64 v[42:43], v[34:35], 0, s[26:27]
	global_load_dwordx2 v[72:73], v[42:43], off
	global_load_dwordx2 v[70:71], v[42:43], off offset:512
	global_load_dwordx2 v[68:69], v[42:43], off offset:1024
	global_load_dwordx2 v[66:67], v[42:43], off offset:1536
	global_load_dwordx2 v[64:65], v[42:43], off offset:2048
	global_load_dwordx2 v[62:63], v[42:43], off offset:2560
	global_load_dwordx2 v[60:61], v[42:43], off offset:3072
	global_load_dwordx2 v[58:59], v[42:43], off offset:3584
	s_waitcnt lgkmcnt(0)
	v_add_f32_e32 v44, v44, v45
	ds_swizzle_b32 v45, v44 offset:swizzle(SWAP,8)
	s_waitcnt lgkmcnt(0)
	v_add_f32_e32 v46, v44, v45
	ds_swizzle_b32 v47, v46 offset:swizzle(SWAP,16)
	v_lshl_add_u64 v[44:45], v[34:35], 0, s[24:25]
	s_waitcnt lgkmcnt(0)
; __device__ __forceinline__ unsigned pk4_fp8(float a, float b, float c, float d) { int w = 0; w = __builtin_amdgcn_cvt_pk_fp8_f32(a, b, w, false); w = __builtin_amdgcn_cvt_pk_fp8_f32(c, d, w, true); return (unsigned)w; }
; #define GAS __attribute__((address_space(1)))
; #define lane (lane_id())
; template <bool F8, bool SRC16, int NR> __device__ __forceinline__ void norm_rows(const void* srcv, const float* gain, void* dstv, int vcu, int G, int wave, int lane) {
;     ...
;         for (int q = 0; q < NR; ++q) { const int m = m0 + q * NGW; if (m >= M) break;
;             float s = 0.f;
; #pragma unroll
;             for (int j = 0; j < 8; ++j) s += (v[q][j].x * v[q][j].x + v[q][j].y * v[q][j].y) + (v[q][j].z * v[q][j].z + v[q][j].w * v[q][j].w);
;             const float r = 1.0f / sqrtf(wave_sum(s) * (1.0f / D) + EPS);
;             if constexpr (F8) { GAS unsigned* o4 = (GAS unsigned*)((unsigned char*)dstv + (size_t)m * D) + lane;
; #pragma unroll
;                 for (int j = 0; j < 8; ++j) o4[64 * j] = pg8::pk4_fp8(v[q][j].x * r * g[j].x, v[q][j].y * r * g[j].y, v[q][j].z * r * g[j].z, v[q][j].w * r * g[j].w); }
	v_add_f32_e32 v42, v46, v47
	v_mov_b32_e32 v43, v42
	s_nop 1
	v_permlane32_swap_b32_e32 v42, v43
	v_add_f32_e32 v42, v42, v43
	v_fmamk_f32 v42, v42, 0x3a000000, v204
	v_mul_f32_e32 v43, 0x4f800000, v42
	v_cmp_gt_f32_e32 vcc, s9, v42
	s_nop 1
	v_cndmask_b32_e32 v48, v42, v43, vcc
	v_sqrt_f32_e32 v49, v48
	global_load_dwordx2 v[54:55], v[44:45], off
	global_load_dwordx2 v[50:51], v[44:45], off offset:512
	global_load_dwordx2 v[46:47], v[44:45], off offset:1024
	global_load_dwordx2 v[42:43], v[44:45], off offset:1536
	v_add_u32_e32 v52, -1, v49
	v_fma_f32 v53, -v52, v49, v48
	v_cmp_ge_f32_e64 s[38:39], 0, v53
	v_add_u32_e32 v53, 1, v49
	s_nop 0
	v_cndmask_b32_e64 v52, v49, v52, s[38:39]
	v_fma_f32 v49, -v53, v49, v48
	v_cmp_lt_f32_e64 s[38:39], 0, v49
	s_nop 1
	v_cndmask_b32_e64 v49, v52, v53, s[38:39]
	v_mul_f32_e32 v52, 0x37800000, v49
	v_cndmask_b32_e32 v49, v49, v52, vcc
	v_cmp_class_f32_e32 vcc, v48, v205
	s_nop 1
	v_cndmask_b32_e32 v90, v49, v48, vcc
	global_load_dwordx2 v[56:57], v[44:45], off offset:2048
	global_load_dwordx2 v[52:53], v[44:45], off offset:2560
	global_load_dwordx2 v[48:49], v[44:45], off offset:3072
	s_nop 0
	global_load_dwordx2 v[44:45], v[44:45], off offset:3584
	v_div_scale_f32 v91, s[24:25], v90, v90, 1.0
	v_rcp_f32_e32 v123, v91
	v_readlane_b32 s24, v253, 56
	v_readlane_b32 s25, v253, 57
	v_fma_f32 v124, -v91, v123, 1.0
	v_fmac_f32_e32 v123, v124, v123
	v_div_scale_f32 v124, vcc, 1.0, v90, 1.0
	v_mul_f32_e32 v125, v124, v123
	v_fma_f32 v126, -v91, v125, v124
	v_fmac_f32_e32 v125, v126, v123
	v_fma_f32 v91, -v91, v125, v124
	v_div_fmas_f32 v91, v91, v123, v125
	v_div_fixup_f32 v123, v91, v90, 1.0
	v_mul_f32_e32 v119, v123, v119
	v_mul_f32_e32 v120, v123, v120
	v_mul_f32_e32 v119, v30, v119
	v_mul_f32_e32 v120, v31, v120
	v_mov_b32_e32 v124, v1
	v_cvt_pk_fp8_f32 v124, v119, v120
	v_mul_f32_e32 v121, v123, v121
	v_mul_f32_e32 v120, v123, v122
	v_mul_f32_e32 v119, v32, v121
	v_mul_f32_e32 v120, v33, v120
	v_mul_f32_e32 v115, v123, v115
	v_mul_f32_e32 v116, v123, v116
	v_cvt_pk_fp8_f32 v124, v119, v120 op_sel:[0,0,1]
	v_mul_f32_e32 v115, v26, v115
	v_mul_f32_e32 v116, v27, v116
	v_mov_b32_e32 v119, v1
	v_cvt_pk_fp8_f32 v119, v115, v116
	v_mul_f32_e32 v117, v123, v117
	v_mul_f32_e32 v116, v123, v118
	v_mul_f32_e32 v115, v28, v117
	v_mul_f32_e32 v116, v29, v116
	v_mul_f32_e32 v111, v123, v111
	v_mul_f32_e32 v112, v123, v112
	v_cvt_pk_fp8_f32 v119, v115, v116 op_sel:[0,0,1]
	v_mul_f32_e32 v111, v22, v111
	v_mul_f32_e32 v112, v23, v112
	v_mov_b32_e32 v115, v1
	v_cvt_pk_fp8_f32 v115, v111, v112
	v_mul_f32_e32 v113, v123, v113
	v_mul_f32_e32 v112, v123, v114
	v_mul_f32_e32 v111, v24, v113
	v_mul_f32_e32 v112, v25, v112
	v_mul_f32_e32 v107, v123, v107
	v_mul_f32_e32 v108, v123, v108
	v_cvt_pk_fp8_f32 v115, v111, v112 op_sel:[0,0,1]
	v_mul_f32_e32 v107, v18, v107
	v_mul_f32_e32 v108, v19, v108
	v_mov_b32_e32 v111, v1
	v_cvt_pk_fp8_f32 v111, v107, v108
	v_mul_f32_e32 v109, v123, v109
	v_mul_f32_e32 v108, v123, v110
	v_mul_f32_e32 v107, v20, v109
	v_mul_f32_e32 v108, v21, v108
	v_mul_f32_e32 v103, v123, v103
	v_mul_f32_e32 v104, v123, v104
	v_cvt_pk_fp8_f32 v111, v107, v108 op_sel:[0,0,1]
	v_mul_f32_e32 v103, v14, v103
	v_mul_f32_e32 v104, v15, v104
	v_mov_b32_e32 v107, v1
	v_cvt_pk_fp8_f32 v107, v103, v104
	v_mul_f32_e32 v105, v123, v105
	v_mul_f32_e32 v104, v123, v106
	v_mul_f32_e32 v103, v16, v105
	v_mul_f32_e32 v104, v17, v104
	v_mul_f32_e32 v99, v123, v99
	v_mul_f32_e32 v100, v123, v100
	v_cvt_pk_fp8_f32 v107, v103, v104 op_sel:[0,0,1]
	v_mul_f32_e32 v99, v10, v99
	v_mul_f32_e32 v100, v11, v100
	v_mov_b32_e32 v103, v1
	v_cvt_pk_fp8_f32 v103, v99, v100
	v_mul_f32_e32 v101, v123, v101
	v_mul_f32_e32 v100, v123, v102
	v_mul_f32_e32 v99, v12, v101
	v_mul_f32_e32 v100, v13, v100
	v_mul_f32_e32 v95, v123, v95
	v_mul_f32_e32 v96, v123, v96
	v_cvt_pk_fp8_f32 v103, v99, v100 op_sel:[0,0,1]
	v_mul_f32_e32 v95, v6, v95
	v_mul_f32_e32 v96, v7, v96
	v_mov_b32_e32 v99, v1
	v_cvt_pk_fp8_f32 v99, v95, v96
	v_mul_f32_e32 v97, v123, v97
	v_mul_f32_e32 v96, v123, v98
	v_mul_f32_e32 v95, v8, v97
	v_mul_f32_e32 v96, v9, v96
	v_mul_f32_e32 v0, v123, v0
	v_mul_f32_e32 v92, v123, v92
	v_cvt_pk_fp8_f32 v99, v95, v96 op_sel:[0,0,1]
	v_mul_f32_e32 v0, v2, v0
	v_mul_f32_e32 v92, v3, v92
	v_mov_b32_e32 v95, v1
	v_cvt_pk_fp8_f32 v95, v0, v92
	v_mul_f32_e32 v93, v123, v93
	v_mul_f32_e32 v92, v123, v94
	v_mul_f32_e32 v0, v4, v93
	v_mul_f32_e32 v92, v5, v92
	v_lshl_add_u64 v[90:91], v[38:39], 0, s[24:25]
	v_cvt_pk_fp8_f32 v95, v0, v92 op_sel:[0,0,1]
	global_store_dword v[90:91], v124, off offset:-1024 sc0 sc1
	global_store_dword v[90:91], v119, off offset:-768 sc0 sc1
	global_store_dword v[90:91], v115, off offset:-512 sc0 sc1
	global_store_dword v[90:91], v111, off offset:-256 sc0 sc1
	global_store_dword v[90:91], v107, off sc0 sc1
	global_store_dword v[90:91], v103, off offset:256 sc0 sc1
	global_store_dword v[90:91], v99, off offset:512 sc0 sc1
	global_store_dword v[90:91], v95, off offset:768 sc0 sc1
	s_cbranch_scc1 .LBB0_1488
; __device__ __forceinline__ unsigned pk4_fp8(float a, float b, float c, float d) { int w = 0; w = __builtin_amdgcn_cvt_pk_fp8_f32(a, b, w, false); w = __builtin_amdgcn_cvt_pk_fp8_f32(c, d, w, true); return (unsigned)w; }
; #define GAS __attribute__((address_space(1)))
; #define lane (lane_id())
; template <bool F8, bool SRC16, int NR> __device__ __forceinline__ void norm_rows(const void* srcv, const float* gain, void* dstv, int vcu, int G, int wave, int lane) {
;     ...
;         for (int q = 0; q < NR; ++q) { const int m = m0 + q * NGW; if (m >= M) break;
;             float s = 0.f;
; #pragma unroll
;             for (int j = 0; j < 8; ++j) s += (v[q][j].x * v[q][j].x + v[q][j].y * v[q][j].y) + (v[q][j].z * v[q][j].z + v[q][j].w * v[q][j].w);
;             const float r = 1.0f / sqrtf(wave_sum(s) * (1.0f / D) + EPS);
;             if constexpr (F8) { GAS unsigned* o4 = (GAS unsigned*)((unsigned char*)dstv + (size_t)m * D) + lane;
; #pragma unroll
;                 for (int j = 0; j < 8; ++j) o4[64 * j] = pg8::pk4_fp8(v[q][j].x * r * g[j].x, v[q][j].y * r * g[j].y, v[q][j].z * r * g[j].z, v[q][j].w * r * g[j].w); }
	s_waitcnt vmcnt(31)
	v_and_b32_e32 v103, 0xffff0000, v75
	v_and_b32_e32 v104, 0xffff0000, v74
	v_lshlrev_b32_e32 v75, 16, v75
	v_lshlrev_b32_e32 v74, 16, v74
	v_mul_f32_e32 v105, v104, v104
	v_mul_f32_e32 v106, v103, v103
	s_waitcnt vmcnt(30)
	v_and_b32_e32 v101, 0xffff0000, v77
	v_and_b32_e32 v102, 0xffff0000, v76
	v_fmac_f32_e32 v105, v74, v74
	v_fmac_f32_e32 v106, v75, v75
	v_lshlrev_b32_e32 v77, 16, v77
	v_lshlrev_b32_e32 v76, 16, v76
	v_add_f32_e32 v105, v105, v106
	v_mul_f32_e32 v106, v102, v102
	v_mul_f32_e32 v107, v101, v101
	v_fmac_f32_e32 v106, v76, v76
	v_fmac_f32_e32 v107, v77, v77
	s_waitcnt vmcnt(29)
	v_and_b32_e32 v99, 0xffff0000, v79
	v_and_b32_e32 v100, 0xffff0000, v78
	v_add_f32_e32 v106, v106, v107
	v_lshlrev_b32_e32 v79, 16, v79
	v_lshlrev_b32_e32 v78, 16, v78
	v_add_f32_e32 v105, v105, v106
	v_mul_f32_e32 v106, v100, v100
	v_mul_f32_e32 v107, v99, v99
	v_fmac_f32_e32 v106, v78, v78
	v_fmac_f32_e32 v107, v79, v79
	s_waitcnt vmcnt(28)
	v_and_b32_e32 v97, 0xffff0000, v81
	v_and_b32_e32 v98, 0xffff0000, v80
	v_add_f32_e32 v106, v106, v107
	v_lshlrev_b32_e32 v81, 16, v81
	v_lshlrev_b32_e32 v80, 16, v80
	v_add_f32_e32 v105, v105, v106
	v_mul_f32_e32 v106, v98, v98
	v_mul_f32_e32 v107, v97, v97
	v_fmac_f32_e32 v106, v80, v80
	v_fmac_f32_e32 v107, v81, v81
	s_waitcnt vmcnt(27)
	v_and_b32_e32 v95, 0xffff0000, v83
	v_and_b32_e32 v96, 0xffff0000, v82
	v_add_f32_e32 v106, v106, v107
	v_lshlrev_b32_e32 v83, 16, v83
	v_lshlrev_b32_e32 v82, 16, v82
	v_add_f32_e32 v105, v105, v106
	v_mul_f32_e32 v106, v96, v96
	v_mul_f32_e32 v107, v95, v95
	v_fmac_f32_e32 v106, v82, v82
	v_fmac_f32_e32 v107, v83, v83
	s_waitcnt vmcnt(26)
	v_and_b32_e32 v93, 0xffff0000, v85
	v_and_b32_e32 v94, 0xffff0000, v84
	v_add_f32_e32 v106, v106, v107
	v_lshlrev_b32_e32 v85, 16, v85
	v_lshlrev_b32_e32 v84, 16, v84
	v_add_f32_e32 v105, v105, v106
	v_mul_f32_e32 v106, v94, v94
	v_mul_f32_e32 v107, v93, v93
	v_fmac_f32_e32 v106, v84, v84
	v_fmac_f32_e32 v107, v85, v85
	s_waitcnt vmcnt(25)
	v_and_b32_e32 v91, 0xffff0000, v87
	v_and_b32_e32 v92, 0xffff0000, v86
	v_add_f32_e32 v106, v106, v107
	v_lshlrev_b32_e32 v87, 16, v87
	v_lshlrev_b32_e32 v86, 16, v86
	v_add_f32_e32 v105, v105, v106
	v_mul_f32_e32 v106, v92, v92
	v_mul_f32_e32 v107, v91, v91
	v_fmac_f32_e32 v106, v86, v86
	v_fmac_f32_e32 v107, v87, v87
	s_waitcnt vmcnt(24)
	v_and_b32_e32 v0, 0xffff0000, v89
	v_and_b32_e32 v90, 0xffff0000, v88
	v_add_f32_e32 v106, v106, v107
	v_lshlrev_b32_e32 v89, 16, v89
	v_lshlrev_b32_e32 v88, 16, v88
	v_add_f32_e32 v105, v105, v106
	v_mul_f32_e32 v106, v90, v90
	v_mul_f32_e32 v107, v0, v0
	v_fmac_f32_e32 v106, v88, v88
	v_fmac_f32_e32 v107, v89, v89
	v_add_f32_e32 v106, v106, v107
	v_add_f32_e32 v105, v105, v106
	s_nop 1
	v_add_f32_dpp v105, v105, v105 quad_perm:[1,0,3,2] row_mask:0xf bank_mask:0xf bound_ctrl:1
	s_nop 1
	v_add_f32_dpp v105, v105, v105 quad_perm:[2,3,0,1] row_mask:0xf bank_mask:0xf bound_ctrl:1
	ds_swizzle_b32 v106, v105 offset:swizzle(SWAP,4)
	s_waitcnt lgkmcnt(0)
	v_add_f32_e32 v105, v105, v106
	ds_swizzle_b32 v106, v105 offset:swizzle(SWAP,8)
	s_waitcnt lgkmcnt(0)
	v_add_f32_e32 v105, v105, v106
	ds_swizzle_b32 v106, v105 offset:swizzle(SWAP,16)
	s_waitcnt lgkmcnt(0)
	v_add_f32_e32 v105, v105, v106
	v_mov_b32_e32 v106, v105
	s_nop 1
	v_permlane32_swap_b32_e32 v105, v106
	v_add_f32_e32 v105, v105, v106
	v_fmamk_f32 v105, v105, 0x3a000000, v204
	v_mul_f32_e32 v106, 0x4f800000, v105
	v_cmp_gt_f32_e32 vcc, s9, v105
	s_nop 1
	v_cndmask_b32_e32 v105, v105, v106, vcc
	v_sqrt_f32_e32 v106, v105
	s_nop 0
	v_add_u32_e32 v107, -1, v106
	v_fma_f32 v108, -v107, v106, v105
	v_cmp_ge_f32_e64 s[38:39], 0, v108
	v_add_u32_e32 v108, 1, v106
	s_nop 0
	v_cndmask_b32_e64 v107, v106, v107, s[38:39]
	v_fma_f32 v106, -v108, v106, v105
	v_cmp_lt_f32_e64 s[38:39], 0, v106
	s_nop 1
	v_cndmask_b32_e64 v106, v107, v108, s[38:39]
	v_mul_f32_e32 v107, 0x37800000, v106
	v_cndmask_b32_e32 v106, v106, v107, vcc
	v_cmp_class_f32_e32 vcc, v105, v205
	s_nop 1
	v_cndmask_b32_e32 v105, v106, v105, vcc
	v_div_scale_f32 v106, s[24:25], v105, v105, 1.0
	v_rcp_f32_e32 v107, v106
	v_readlane_b32 s24, v253, 40
	v_readlane_b32 s25, v253, 41
	v_fma_f32 v108, -v106, v107, 1.0
	v_fmac_f32_e32 v107, v108, v107
	v_div_scale_f32 v108, vcc, 1.0, v105, 1.0
	v_mul_f32_e32 v109, v108, v107
	v_fma_f32 v110, -v106, v109, v108
	v_fmac_f32_e32 v109, v110, v107
	v_fma_f32 v106, -v106, v109, v108
	v_div_fmas_f32 v106, v106, v107, v109
	v_div_fixup_f32 v105, v106, v105, 1.0
	v_mul_f32_e32 v74, v105, v74
	v_mul_f32_e32 v104, v105, v104
	v_mul_f32_e32 v74, v30, v74
	v_mul_f32_e32 v104, v31, v104
	v_mov_b32_e32 v106, v1
	v_cvt_pk_fp8_f32 v106, v74, v104
	v_mul_f32_e32 v75, v105, v75
	v_mul_f32_e32 v74, v32, v75
	v_mul_f32_e32 v75, v105, v103
	v_mul_f32_e32 v75, v33, v75
	v_cvt_pk_fp8_f32 v106, v74, v75 op_sel:[0,0,1]
	v_mul_f32_e32 v74, v105, v76
	v_mul_f32_e32 v75, v105, v102
	v_mul_f32_e32 v74, v26, v74
	v_mul_f32_e32 v75, v27, v75
	v_mul_f32_e32 v76, v105, v77
	v_mov_b32_e32 v77, v1
	v_cvt_pk_fp8_f32 v77, v74, v75
	v_mul_f32_e32 v75, v105, v101
	v_mul_f32_e32 v74, v28, v76
	v_mul_f32_e32 v75, v29, v75
	v_cvt_pk_fp8_f32 v77, v74, v75 op_sel:[0,0,1]
	v_mul_f32_e32 v74, v105, v78
	v_mul_f32_e32 v75, v105, v100
	v_mul_f32_e32 v74, v22, v74
	v_mul_f32_e32 v75, v23, v75
	v_mov_b32_e32 v78, v1
	v_cvt_pk_fp8_f32 v78, v74, v75
	v_mul_f32_e32 v76, v105, v79
	v_mul_f32_e32 v75, v105, v99
	v_mul_f32_e32 v74, v24, v76
	v_mul_f32_e32 v75, v25, v75
	v_cvt_pk_fp8_f32 v78, v74, v75 op_sel:[0,0,1]
	v_lshl_add_u64 v[74:75], v[38:39], 0, s[24:25]
	global_store_dword v[74:75], v106, off offset:-1024 sc0 sc1
; __device__ __forceinline__ unsigned pk4_fp8(float a, float b, float c, float d) { int w = 0; w = __builtin_amdgcn_cvt_pk_fp8_f32(a, b, w, false); w = __builtin_amdgcn_cvt_pk_fp8_f32(c, d, w, true); return (unsigned)w; }
; #define GAS __attribute__((address_space(1)))
; #define lane (lane_id())
; template <bool F8, bool SRC16, int NR> __device__ __forceinline__ void norm_rows(const void* srcv, const float* gain, void* dstv, int vcu, int G, int wave, int lane) {
;     ...
;         for (int q = 0; q < NR; ++q) { const int m = m0 + q * NGW; if (m >= M) break;
;             float s = 0.f;
; #pragma unroll
;             for (int j = 0; j < 8; ++j) s += (v[q][j].x * v[q][j].x + v[q][j].y * v[q][j].y) + (v[q][j].z * v[q][j].z + v[q][j].w * v[q][j].w);
;             const float r = 1.0f / sqrtf(wave_sum(s) * (1.0f / D) + EPS);
;             if constexpr (F8) { GAS unsigned* o4 = (GAS unsigned*)((unsigned char*)dstv + (size_t)m * D) + lane;
; #pragma unroll
;                 for (int j = 0; j < 8; ++j) o4[64 * j] = pg8::pk4_fp8(v[q][j].x * r * g[j].x, v[q][j].y * r * g[j].y, v[q][j].z * r * g[j].z, v[q][j].w * r * g[j].w); }
	global_store_dword v[74:75], v77, off offset:-768 sc0 sc1
	global_store_dword v[74:75], v78, off offset:-512 sc0 sc1
	v_mul_f32_e32 v76, v105, v80
	v_mul_f32_e32 v77, v105, v98
	v_mul_f32_e32 v76, v18, v76
	v_mul_f32_e32 v77, v19, v77
	v_mov_b32_e32 v79, v1
	v_cvt_pk_fp8_f32 v79, v76, v77
	v_mul_f32_e32 v78, v105, v81
	v_mul_f32_e32 v77, v105, v97
	v_mul_f32_e32 v76, v20, v78
	v_mul_f32_e32 v77, v21, v77
	v_cvt_pk_fp8_f32 v79, v76, v77 op_sel:[0,0,1]
	v_mul_f32_e32 v76, v105, v82
	v_mul_f32_e32 v77, v105, v96
	v_mul_f32_e32 v76, v14, v76
	v_mul_f32_e32 v77, v15, v77
	v_mov_b32_e32 v80, v1
	v_cvt_pk_fp8_f32 v80, v76, v77
	v_mul_f32_e32 v78, v105, v83
	v_mul_f32_e32 v77, v105, v95
	v_mul_f32_e32 v76, v16, v78
	v_mul_f32_e32 v77, v17, v77
	v_cvt_pk_fp8_f32 v80, v76, v77 op_sel:[0,0,1]
	v_mul_f32_e32 v76, v105, v84
	v_mul_f32_e32 v77, v105, v94
	v_mul_f32_e32 v76, v10, v76
	v_mul_f32_e32 v77, v11, v77
	v_mov_b32_e32 v81, v1
	v_cvt_pk_fp8_f32 v81, v76, v77
	v_mul_f32_e32 v78, v105, v85
	v_mul_f32_e32 v77, v105, v93
	v_mul_f32_e32 v76, v12, v78
	v_mul_f32_e32 v77, v13, v77
	v_cvt_pk_fp8_f32 v81, v76, v77 op_sel:[0,0,1]
	v_mul_f32_e32 v76, v105, v86
	v_mul_f32_e32 v77, v105, v92
	v_mul_f32_e32 v76, v6, v76
	v_mul_f32_e32 v77, v7, v77
	v_mov_b32_e32 v82, v1
	v_cvt_pk_fp8_f32 v82, v76, v77
	v_mul_f32_e32 v78, v105, v87
	v_mul_f32_e32 v77, v105, v91
	v_mul_f32_e32 v76, v8, v78
	v_mul_f32_e32 v77, v9, v77
	v_cvt_pk_fp8_f32 v82, v76, v77 op_sel:[0,0,1]
	v_mul_f32_e32 v76, v105, v88
	v_mul_f32_e32 v77, v105, v90
	global_store_dword v[74:75], v79, off offset:-256 sc0 sc1
	global_store_dword v[74:75], v80, off sc0 sc1
	global_store_dword v[74:75], v81, off offset:256 sc0 sc1
	global_store_dword v[74:75], v82, off offset:512 sc0 sc1
	v_mul_f32_e32 v76, v2, v76
	v_mul_f32_e32 v77, v3, v77
	v_mov_b32_e32 v79, v1
	v_cvt_pk_fp8_f32 v79, v76, v77
	v_mul_f32_e32 v78, v105, v89
	v_mul_f32_e32 v0, v105, v0
	v_mul_f32_e32 v76, v4, v78
	v_mul_f32_e32 v0, v5, v0
	v_cvt_pk_fp8_f32 v79, v76, v0 op_sel:[0,0,1]
	s_andn2_b64 vcc, exec, s[22:23]
	global_store_dword v[74:75], v79, off offset:768 sc0 sc1
	s_cbranch_vccnz .LBB0_1488
	s_waitcnt vmcnt(31)
	v_lshlrev_b32_e32 v0, 16, v72
	v_and_b32_e32 v72, 0xffff0000, v72
	v_lshlrev_b32_e32 v74, 16, v73
	v_and_b32_e32 v73, 0xffff0000, v73
	s_waitcnt vmcnt(24)
	v_lshlrev_b32_e32 v87, 16, v58
	v_and_b32_e32 v88, 0xffff0000, v58
	v_lshlrev_b32_e32 v89, 16, v59
	v_and_b32_e32 v90, 0xffff0000, v59
	v_mul_f32_e32 v58, v72, v72
	v_mul_f32_e32 v59, v73, v73
	v_lshlrev_b32_e32 v75, 16, v70
	v_and_b32_e32 v70, 0xffff0000, v70
	v_lshlrev_b32_e32 v76, 16, v71
	v_and_b32_e32 v71, 0xffff0000, v71
	v_fmac_f32_e32 v58, v0, v0
	v_fmac_f32_e32 v59, v74, v74
	v_add_f32_e32 v58, v58, v59
	v_mul_f32_e32 v59, v70, v70
	v_mul_f32_e32 v91, v71, v71
	v_fmac_f32_e32 v59, v75, v75
	v_fmac_f32_e32 v91, v76, v76
	v_lshlrev_b32_e32 v77, 16, v68
	v_and_b32_e32 v68, 0xffff0000, v68
	v_lshlrev_b32_e32 v78, 16, v69
	v_and_b32_e32 v69, 0xffff0000, v69
	v_add_f32_e32 v59, v59, v91
	v_add_f32_e32 v58, v58, v59
	v_mul_f32_e32 v59, v68, v68
	v_mul_f32_e32 v91, v69, v69
	v_fmac_f32_e32 v59, v77, v77
	v_fmac_f32_e32 v91, v78, v78
	v_lshlrev_b32_e32 v79, 16, v66
	v_and_b32_e32 v66, 0xffff0000, v66
	v_lshlrev_b32_e32 v80, 16, v67
	v_and_b32_e32 v67, 0xffff0000, v67
	v_add_f32_e32 v59, v59, v91
	v_add_f32_e32 v58, v58, v59
	v_mul_f32_e32 v59, v66, v66
	v_mul_f32_e32 v91, v67, v67
	v_fmac_f32_e32 v59, v79, v79
	v_fmac_f32_e32 v91, v80, v80
	v_lshlrev_b32_e32 v81, 16, v64
	v_and_b32_e32 v64, 0xffff0000, v64
	v_lshlrev_b32_e32 v82, 16, v65
	v_and_b32_e32 v65, 0xffff0000, v65
	v_add_f32_e32 v59, v59, v91
	v_add_f32_e32 v58, v58, v59
	v_mul_f32_e32 v59, v64, v64
	v_mul_f32_e32 v91, v65, v65
	v_fmac_f32_e32 v59, v81, v81
	v_fmac_f32_e32 v91, v82, v82
	v_lshlrev_b32_e32 v83, 16, v62
	v_and_b32_e32 v62, 0xffff0000, v62
	v_lshlrev_b32_e32 v84, 16, v63
	v_and_b32_e32 v63, 0xffff0000, v63
	v_add_f32_e32 v59, v59, v91
	v_add_f32_e32 v58, v58, v59
	v_mul_f32_e32 v59, v62, v62
	v_mul_f32_e32 v91, v63, v63
	v_fmac_f32_e32 v59, v83, v83
	v_fmac_f32_e32 v91, v84, v84
	v_lshlrev_b32_e32 v85, 16, v60
	v_and_b32_e32 v60, 0xffff0000, v60
	v_lshlrev_b32_e32 v86, 16, v61
	v_and_b32_e32 v61, 0xffff0000, v61
	v_add_f32_e32 v59, v59, v91
	v_add_f32_e32 v58, v58, v59
	v_mul_f32_e32 v59, v60, v60
	v_mul_f32_e32 v91, v61, v61
	v_fmac_f32_e32 v59, v85, v85
	v_fmac_f32_e32 v91, v86, v86
	v_add_f32_e32 v59, v59, v91
	v_add_f32_e32 v58, v58, v59
	v_mul_f32_e32 v59, v88, v88
	v_mul_f32_e32 v91, v90, v90
	v_fmac_f32_e32 v59, v87, v87
	v_fmac_f32_e32 v91, v89, v89
	v_add_f32_e32 v59, v59, v91
	v_add_f32_e32 v58, v58, v59
	s_ashr_i32 s21, s20, 31
	s_lshl_b64 s[20:21], s[20:21], 11
	v_add_f32_dpp v58, v58, v58 quad_perm:[1,0,3,2] row_mask:0xf bank_mask:0xf bound_ctrl:1
	s_nop 1
	v_add_f32_dpp v58, v58, v58 quad_perm:[2,3,0,1] row_mask:0xf bank_mask:0xf bound_ctrl:1
	ds_swizzle_b32 v59, v58 offset:swizzle(SWAP,4)
	s_waitcnt lgkmcnt(0)
	v_add_f32_e32 v58, v58, v59
	ds_swizzle_b32 v59, v58 offset:swizzle(SWAP,8)
	s_waitcnt lgkmcnt(0)
	v_add_f32_e32 v58, v58, v59
	ds_swizzle_b32 v59, v58 offset:swizzle(SWAP,16)
	s_waitcnt lgkmcnt(0)
; __device__ __forceinline__ unsigned pk4_fp8(float a, float b, float c, float d) { int w = 0; w = __builtin_amdgcn_cvt_pk_fp8_f32(a, b, w, false); w = __builtin_amdgcn_cvt_pk_fp8_f32(c, d, w, true); return (unsigned)w; }
; #define GAS __attribute__((address_space(1)))
; #define lane (lane_id())
; template <bool F8, bool SRC16, int NR> __device__ __forceinline__ void norm_rows(const void* srcv, const float* gain, void* dstv, int vcu, int G, int wave, int lane) {
;     ...
;             const float r = 1.0f / sqrtf(wave_sum(s) * (1.0f / D) + EPS);
;             if constexpr (F8) { GAS unsigned* o4 = (GAS unsigned*)((unsigned char*)dstv + (size_t)m * D) + lane;
; #pragma unroll
;                 for (int j = 0; j < 8; ++j) o4[64 * j] = pg8::pk4_fp8(v[q][j].x * r * g[j].x, v[q][j].y * r * g[j].y, v[q][j].z * r * g[j].z, v[q][j].w * r * g[j].w); }
	v_add_f32_e32 v58, v58, v59
	v_mov_b32_e32 v59, v58
	s_nop 1
	v_permlane32_swap_b32_e32 v58, v59
	v_add_f32_e32 v58, v58, v59
	v_fmamk_f32 v58, v58, 0x3a000000, v204
	v_mul_f32_e32 v59, 0x4f800000, v58
	v_cmp_gt_f32_e32 vcc, s9, v58
	s_nop 1
	v_cndmask_b32_e32 v58, v58, v59, vcc
	v_sqrt_f32_e32 v59, v58
	s_nop 0
	v_add_u32_e32 v91, -1, v59
	v_fma_f32 v92, -v91, v59, v58
	v_cmp_ge_f32_e64 s[38:39], 0, v92
	v_add_u32_e32 v92, 1, v59
	s_nop 0
	v_cndmask_b32_e64 v91, v59, v91, s[38:39]
	v_fma_f32 v59, -v92, v59, v58
	v_cmp_lt_f32_e64 s[38:39], 0, v59
	s_nop 1
	v_cndmask_b32_e64 v59, v91, v92, s[38:39]
	v_mul_f32_e32 v91, 0x37800000, v59
	v_cndmask_b32_e32 v59, v59, v91, vcc
	v_cmp_class_f32_e32 vcc, v58, v205
	s_nop 1
	v_cndmask_b32_e32 v58, v59, v58, vcc
	v_div_scale_f32 v59, s[22:23], v58, v58, 1.0
	v_rcp_f32_e32 v91, v59
	s_nop 0
	v_fma_f32 v92, -v59, v91, 1.0
	v_fmac_f32_e32 v91, v92, v91
	v_div_scale_f32 v92, vcc, 1.0, v58, 1.0
	v_mul_f32_e32 v93, v92, v91
	v_fma_f32 v94, -v59, v93, v92
	v_fmac_f32_e32 v93, v94, v91
	v_fma_f32 v59, -v59, v93, v92
	v_div_fmas_f32 v59, v59, v91, v93
	v_div_fixup_f32 v91, v59, v58, 1.0
	v_mul_f32_e32 v0, v91, v0
	v_mul_f32_e32 v58, v91, v72
	v_mul_f32_e32 v0, v30, v0
	v_mul_f32_e32 v58, v31, v58
	v_mov_b32_e32 v72, v1
	v_cvt_pk_fp8_f32 v72, v0, v58
	v_mul_f32_e32 v59, v91, v74
	v_mul_f32_e32 v58, v91, v73
	v_mul_f32_e32 v0, v32, v59
	v_mul_f32_e32 v58, v33, v58
	v_cvt_pk_fp8_f32 v72, v0, v58 op_sel:[0,0,1]
	v_mul_f32_e32 v0, v91, v75
	v_mul_f32_e32 v58, v91, v70
	v_mul_f32_e32 v0, v26, v0
	v_mul_f32_e32 v58, v27, v58
	v_mov_b32_e32 v70, v1
	v_cvt_pk_fp8_f32 v70, v0, v58
	v_mul_f32_e32 v59, v91, v76
	v_mul_f32_e32 v58, v91, v71
	v_mul_f32_e32 v0, v28, v59
	v_mul_f32_e32 v58, v29, v58
	v_cvt_pk_fp8_f32 v70, v0, v58 op_sel:[0,0,1]
	v_mul_f32_e32 v0, v91, v77
	v_mul_f32_e32 v58, v91, v68
	v_mul_f32_e32 v0, v22, v0
	v_mul_f32_e32 v58, v23, v58
	v_mov_b32_e32 v68, v1
	v_cvt_pk_fp8_f32 v68, v0, v58
	v_mul_f32_e32 v59, v91, v78
	v_mul_f32_e32 v58, v91, v69
	v_mul_f32_e32 v0, v24, v59
	v_mul_f32_e32 v58, v25, v58
	v_cvt_pk_fp8_f32 v68, v0, v58 op_sel:[0,0,1]
	v_mul_f32_e32 v0, v91, v79
	v_mul_f32_e32 v66, v91, v66
	v_mul_f32_e32 v0, v18, v0
	v_mul_f32_e32 v66, v19, v66
	v_mov_b32_e32 v69, v1
	v_cvt_pk_fp8_f32 v69, v0, v66
	v_lshl_add_u64 v[58:59], v[36:37], 0, s[20:21]
	global_store_dword v[58:59], v72, off sc0 sc1
	global_store_dword v[58:59], v70, off offset:256 sc0 sc1
	global_store_dword v[58:59], v68, off offset:512 sc0 sc1
	v_mul_f32_e32 v68, v91, v80
	v_mul_f32_e32 v66, v91, v67
	v_mul_f32_e32 v0, v20, v68
	v_mul_f32_e32 v66, v21, v66
	v_cvt_pk_fp8_f32 v69, v0, v66 op_sel:[0,0,1]
	v_mul_f32_e32 v0, v91, v81
	v_mul_f32_e32 v64, v91, v64
	v_mul_f32_e32 v0, v14, v0
	v_mul_f32_e32 v64, v15, v64
	v_mov_b32_e32 v67, v1
	v_cvt_pk_fp8_f32 v67, v0, v64
	v_mul_f32_e32 v66, v91, v82
	v_mul_f32_e32 v64, v91, v65
	v_mul_f32_e32 v0, v16, v66
	v_mul_f32_e32 v64, v17, v64
	v_cvt_pk_fp8_f32 v67, v0, v64 op_sel:[0,0,1]
	v_mul_f32_e32 v0, v91, v83
	v_mul_f32_e32 v62, v91, v62
	v_mul_f32_e32 v0, v10, v0
	v_mul_f32_e32 v62, v11, v62
	v_mov_b32_e32 v65, v1
	v_cvt_pk_fp8_f32 v65, v0, v62
	v_mul_f32_e32 v64, v91, v84
	v_mul_f32_e32 v62, v91, v63
	v_mul_f32_e32 v0, v12, v64
	v_mul_f32_e32 v62, v13, v62
	v_cvt_pk_fp8_f32 v65, v0, v62 op_sel:[0,0,1]
	v_mul_f32_e32 v0, v91, v85
	v_mul_f32_e32 v60, v91, v60
	v_mul_f32_e32 v0, v6, v0
	v_mul_f32_e32 v60, v7, v60
	v_mov_b32_e32 v63, v1
	v_cvt_pk_fp8_f32 v63, v0, v60
	v_mul_f32_e32 v62, v91, v86
	v_mul_f32_e32 v60, v91, v61
	v_mul_f32_e32 v0, v8, v62
	v_mul_f32_e32 v60, v9, v60
	v_cvt_pk_fp8_f32 v63, v0, v60 op_sel:[0,0,1]
	v_mul_f32_e32 v0, v91, v87
	v_mul_f32_e32 v60, v91, v88
	v_mul_f32_e32 v0, v2, v0
	v_mul_f32_e32 v60, v3, v60
	v_mov_b32_e32 v62, v1
	v_cvt_pk_fp8_f32 v62, v0, v60
	v_mul_f32_e32 v61, v91, v89
	v_mul_f32_e32 v60, v91, v90
	v_mul_f32_e32 v0, v4, v61
	v_mul_f32_e32 v60, v5, v60
	v_cvt_pk_fp8_f32 v62, v0, v60 op_sel:[0,0,1]
	s_andn2_b64 vcc, exec, s[16:17]
	global_store_dword v[58:59], v69, off offset:768 sc0 sc1
	global_store_dword v[58:59], v67, off offset:1024 sc0 sc1
	global_store_dword v[58:59], v65, off offset:1280 sc0 sc1
	global_store_dword v[58:59], v63, off offset:1536 sc0 sc1
	global_store_dword v[58:59], v62, off offset:1792 sc0 sc1
	s_cbranch_vccnz .LBB0_1488
; __device__ __forceinline__ float xor32_sum(float v) { auto rr = __builtin_amdgcn_permlane32_swap(__float_as_uint(v), __float_as_uint(v), false, false); return __uint_as_float(rr[0]) + __uint_as_float(rr[1]); }
; __device__ __forceinline__ float wave_sum(float v) {
;     v += xor_get<1>(v); v += xor_get<2>(v); v += xor_get<4>(v); v += xor_get<8>(v); v += xor_get<16>(v);
;     return xor32_sum(v);
; template <bool F8, bool SRC16, int NR> __device__ __forceinline__ void norm_rows(const void* srcv, const float* gain, void* dstv, int vcu, int G, int wave, int lane) {
;     ...
;         for (int q = 0; q < NR; ++q) { const int m = m0 + q * NGW; if (m >= M) break;
;             float s = 0.f;
; #pragma unroll
;             for (int j = 0; j < 8; ++j) s += (v[q][j].x * v[q][j].x + v[q][j].y * v[q][j].y) + (v[q][j].z * v[q][j].z + v[q][j].w * v[q][j].w);
;             const float r = 1.0f / sqrtf(wave_sum(s) * (1.0f / D) + EPS);
	s_waitcnt vmcnt(31)
	v_lshlrev_b32_e32 v0, 16, v54
	v_and_b32_e32 v54, 0xffff0000, v54
	v_lshlrev_b32_e32 v58, 16, v55
	v_and_b32_e32 v55, 0xffff0000, v55
	s_waitcnt vmcnt(28)
	v_lshlrev_b32_e32 v63, 16, v42
	v_and_b32_e32 v64, 0xffff0000, v42
	v_lshlrev_b32_e32 v65, 16, v43
	v_and_b32_e32 v66, 0xffff0000, v43
	v_mul_f32_e32 v42, v54, v54
	v_mul_f32_e32 v43, v55, v55
	v_lshlrev_b32_e32 v59, 16, v50
	v_and_b32_e32 v50, 0xffff0000, v50
	v_lshlrev_b32_e32 v60, 16, v51
	v_and_b32_e32 v51, 0xffff0000, v51
	v_fmac_f32_e32 v42, v0, v0
	v_fmac_f32_e32 v43, v58, v58
	v_add_f32_e32 v42, v42, v43
	v_mul_f32_e32 v43, v50, v50
	v_mul_f32_e32 v75, v51, v51
	v_fmac_f32_e32 v43, v59, v59
	v_fmac_f32_e32 v75, v60, v60
	v_lshlrev_b32_e32 v61, 16, v46
	v_and_b32_e32 v46, 0xffff0000, v46
	v_lshlrev_b32_e32 v62, 16, v47
	v_and_b32_e32 v47, 0xffff0000, v47
	v_add_f32_e32 v43, v43, v75
	v_add_f32_e32 v42, v42, v43
	v_mul_f32_e32 v43, v46, v46
	v_mul_f32_e32 v75, v47, v47
	v_fmac_f32_e32 v43, v61, v61
	v_fmac_f32_e32 v75, v62, v62
	v_add_f32_e32 v43, v43, v75
	v_add_f32_e32 v42, v42, v43
	v_mul_f32_e32 v43, v64, v64
	v_mul_f32_e32 v75, v66, v66
	v_fmac_f32_e32 v43, v63, v63
	v_fmac_f32_e32 v75, v65, v65
	s_waitcnt vmcnt(27)
	v_lshlrev_b32_e32 v67, 16, v56
	v_and_b32_e32 v56, 0xffff0000, v56
	v_lshlrev_b32_e32 v68, 16, v57
	v_and_b32_e32 v57, 0xffff0000, v57
	v_add_f32_e32 v43, v43, v75
	v_add_f32_e32 v42, v42, v43
	v_mul_f32_e32 v43, v56, v56
	v_mul_f32_e32 v75, v57, v57
	v_fmac_f32_e32 v43, v67, v67
	v_fmac_f32_e32 v75, v68, v68
	s_waitcnt vmcnt(26)
	v_lshlrev_b32_e32 v69, 16, v52
	v_and_b32_e32 v52, 0xffff0000, v52
	v_lshlrev_b32_e32 v70, 16, v53
	v_and_b32_e32 v53, 0xffff0000, v53
	v_add_f32_e32 v43, v43, v75
	v_add_f32_e32 v42, v42, v43
	v_mul_f32_e32 v43, v52, v52
	v_mul_f32_e32 v75, v53, v53
	v_fmac_f32_e32 v43, v69, v69
	v_fmac_f32_e32 v75, v70, v70
	s_waitcnt vmcnt(25)
	v_lshlrev_b32_e32 v71, 16, v48
	v_and_b32_e32 v48, 0xffff0000, v48
	v_lshlrev_b32_e32 v72, 16, v49
	v_and_b32_e32 v49, 0xffff0000, v49
	v_add_f32_e32 v43, v43, v75
	v_add_f32_e32 v42, v42, v43
	v_mul_f32_e32 v43, v48, v48
	v_mul_f32_e32 v75, v49, v49
	v_fmac_f32_e32 v43, v71, v71
	v_fmac_f32_e32 v75, v72, v72
	s_waitcnt vmcnt(24)
	v_lshlrev_b32_e32 v73, 16, v44
	v_and_b32_e32 v44, 0xffff0000, v44
	v_lshlrev_b32_e32 v74, 16, v45
	v_and_b32_e32 v45, 0xffff0000, v45
	v_add_f32_e32 v43, v43, v75
	v_add_f32_e32 v42, v42, v43
	v_mul_f32_e32 v43, v44, v44
	v_mul_f32_e32 v75, v45, v45
	v_fmac_f32_e32 v43, v73, v73
	v_fmac_f32_e32 v75, v74, v74
	v_add_f32_e32 v43, v43, v75
	v_add_f32_e32 v42, v42, v43
	s_ashr_i32 s15, s14, 31
	s_lshl_b64 s[14:15], s[14:15], 11
	v_add_f32_dpp v42, v42, v42 quad_perm:[1,0,3,2] row_mask:0xf bank_mask:0xf bound_ctrl:1
	s_nop 1
	v_add_f32_dpp v42, v42, v42 quad_perm:[2,3,0,1] row_mask:0xf bank_mask:0xf bound_ctrl:1
	ds_swizzle_b32 v43, v42 offset:swizzle(SWAP,4)
	s_waitcnt lgkmcnt(0)
	v_add_f32_e32 v42, v42, v43
	ds_swizzle_b32 v43, v42 offset:swizzle(SWAP,8)
	s_waitcnt lgkmcnt(0)
	v_add_f32_e32 v42, v42, v43
	ds_swizzle_b32 v43, v42 offset:swizzle(SWAP,16)
	s_waitcnt lgkmcnt(0)
; __device__ __forceinline__ float xor32_sum(float v) { auto rr = __builtin_amdgcn_permlane32_swap(__float_as_uint(v), __float_as_uint(v), false, false); return __uint_as_float(rr[0]) + __uint_as_float(rr[1]); }
; __device__ __forceinline__ unsigned pk4_fp8(float a, float b, float c, float d) { int w = 0; w = __builtin_amdgcn_cvt_pk_fp8_f32(a, b, w, false); w = __builtin_amdgcn_cvt_pk_fp8_f32(c, d, w, true); return (unsigned)w; }
; #define GAS __attribute__((address_space(1)))
; #define lane (lane_id())
; __device__ __forceinline__ float wave_sum(float v) {
;     v += xor_get<1>(v); v += xor_get<2>(v); v += xor_get<4>(v); v += xor_get<8>(v); v += xor_get<16>(v);
;     return xor32_sum(v);
; template <bool F8, bool SRC16, int NR> __device__ __forceinline__ void norm_rows(const void* srcv, const float* gain, void* dstv, int vcu, int G, int wave, int lane) {
;     ...
;             const float r = 1.0f / sqrtf(wave_sum(s) * (1.0f / D) + EPS);
;             if constexpr (F8) { GAS unsigned* o4 = (GAS unsigned*)((unsigned char*)dstv + (size_t)m * D) + lane;
; #pragma unroll
;                 for (int j = 0; j < 8; ++j) o4[64 * j] = pg8::pk4_fp8(v[q][j].x * r * g[j].x, v[q][j].y * r * g[j].y, v[q][j].z * r * g[j].z, v[q][j].w * r * g[j].w); }
	v_add_f32_e32 v42, v42, v43
	v_mov_b32_e32 v43, v42
	s_nop 1
	v_permlane32_swap_b32_e32 v42, v43
	v_add_f32_e32 v42, v42, v43
	v_fmamk_f32 v42, v42, 0x3a000000, v204
	v_mul_f32_e32 v43, 0x4f800000, v42
	v_cmp_gt_f32_e32 vcc, s9, v42
	s_nop 1
	v_cndmask_b32_e32 v42, v42, v43, vcc
	v_sqrt_f32_e32 v43, v42
	s_nop 0
	v_add_u32_e32 v75, -1, v43
	v_fma_f32 v76, -v75, v43, v42
	v_cmp_ge_f32_e64 s[38:39], 0, v76
	v_add_u32_e32 v76, 1, v43
	s_nop 0
	v_cndmask_b32_e64 v75, v43, v75, s[38:39]
	v_fma_f32 v43, -v76, v43, v42
	v_cmp_lt_f32_e64 s[38:39], 0, v43
	s_nop 1
	v_cndmask_b32_e64 v43, v75, v76, s[38:39]
	v_mul_f32_e32 v75, 0x37800000, v43
	v_cndmask_b32_e32 v43, v43, v75, vcc
	v_cmp_class_f32_e32 vcc, v42, v205
	s_nop 1
	v_cndmask_b32_e32 v42, v43, v42, vcc
	v_div_scale_f32 v43, s[16:17], v42, v42, 1.0
	v_rcp_f32_e32 v75, v43
	s_nop 0
	v_fma_f32 v76, -v43, v75, 1.0
	v_fmac_f32_e32 v75, v76, v75
	v_div_scale_f32 v76, vcc, 1.0, v42, 1.0
	v_mul_f32_e32 v77, v76, v75
	v_fma_f32 v78, -v43, v77, v76
	v_fmac_f32_e32 v77, v78, v75
	v_fma_f32 v43, -v43, v77, v76
	v_div_fmas_f32 v43, v43, v75, v77
	v_div_fixup_f32 v75, v43, v42, 1.0
	v_mul_f32_e32 v0, v75, v0
	v_mul_f32_e32 v54, v75, v54
	v_mul_f32_e32 v0, v30, v0
	v_mul_f32_e32 v54, v31, v54
	v_mov_b32_e32 v76, v1
	v_cvt_pk_fp8_f32 v76, v0, v54
	v_mul_f32_e32 v58, v75, v58
	v_mul_f32_e32 v54, v75, v55
	v_mul_f32_e32 v0, v32, v58
	v_mul_f32_e32 v54, v33, v54
	v_cvt_pk_fp8_f32 v76, v0, v54 op_sel:[0,0,1]
	v_mul_f32_e32 v0, v75, v59
	v_mul_f32_e32 v50, v75, v50
	v_mul_f32_e32 v0, v26, v0
	v_mul_f32_e32 v50, v27, v50
	v_mov_b32_e32 v55, v1
	v_cvt_pk_fp8_f32 v55, v0, v50
	v_mul_f32_e32 v54, v75, v60
	v_mul_f32_e32 v50, v75, v51
	v_mul_f32_e32 v0, v28, v54
	v_mul_f32_e32 v50, v29, v50
	v_cvt_pk_fp8_f32 v55, v0, v50 op_sel:[0,0,1]
	v_mul_f32_e32 v0, v75, v61
	v_mul_f32_e32 v46, v75, v46
	v_mul_f32_e32 v0, v22, v0
	v_mul_f32_e32 v46, v23, v46
	v_mov_b32_e32 v51, v1
	v_cvt_pk_fp8_f32 v51, v0, v46
	v_mul_f32_e32 v50, v75, v62
	v_mul_f32_e32 v46, v75, v47
	v_mul_f32_e32 v0, v24, v50
	v_mul_f32_e32 v46, v25, v46
	v_cvt_pk_fp8_f32 v51, v0, v46 op_sel:[0,0,1]
	v_mul_f32_e32 v0, v75, v63
	v_mul_f32_e32 v46, v75, v64
	v_mul_f32_e32 v0, v18, v0
	v_mul_f32_e32 v46, v19, v46
	v_mov_b32_e32 v50, v1
	v_cvt_pk_fp8_f32 v50, v0, v46
	v_mul_f32_e32 v47, v75, v65
	v_mul_f32_e32 v46, v75, v66
	v_mul_f32_e32 v0, v20, v47
	v_mul_f32_e32 v46, v21, v46
	v_lshl_add_u64 v[42:43], v[36:37], 0, s[14:15]
	v_cvt_pk_fp8_f32 v50, v0, v46 op_sel:[0,0,1]
	v_mul_f32_e32 v0, v75, v67
	v_mul_f32_e32 v46, v75, v56
	global_store_dword v[42:43], v76, off sc0 sc1
	global_store_dword v[42:43], v55, off offset:256 sc0 sc1
	global_store_dword v[42:43], v51, off offset:512 sc0 sc1
	global_store_dword v[42:43], v50, off offset:768 sc0 sc1
	v_mul_f32_e32 v0, v14, v0
	v_mul_f32_e32 v46, v15, v46
	v_mov_b32_e32 v50, v1
	v_cvt_pk_fp8_f32 v50, v0, v46
	v_mul_f32_e32 v47, v75, v68
	v_mul_f32_e32 v46, v75, v57
	v_mul_f32_e32 v0, v16, v47
	v_mul_f32_e32 v46, v17, v46
	v_cvt_pk_fp8_f32 v50, v0, v46 op_sel:[0,0,1]
	v_mul_f32_e32 v0, v75, v69
	v_mul_f32_e32 v46, v75, v52
	v_mul_f32_e32 v0, v10, v0
	v_mul_f32_e32 v46, v11, v46
	v_mov_b32_e32 v51, v1
	v_cvt_pk_fp8_f32 v51, v0, v46
	v_mul_f32_e32 v47, v75, v70
	v_mul_f32_e32 v46, v75, v53
	v_mul_f32_e32 v0, v12, v47
	v_mul_f32_e32 v46, v13, v46
	v_cvt_pk_fp8_f32 v51, v0, v46 op_sel:[0,0,1]
	v_mul_f32_e32 v0, v75, v71
	v_mul_f32_e32 v46, v75, v48
	v_mul_f32_e32 v0, v6, v0
	v_mul_f32_e32 v46, v7, v46
	v_mov_b32_e32 v48, v1
	v_cvt_pk_fp8_f32 v48, v0, v46
	v_mul_f32_e32 v47, v75, v72
	v_mul_f32_e32 v46, v75, v49
	v_mul_f32_e32 v0, v8, v47
	v_mul_f32_e32 v46, v9, v46
	v_cvt_pk_fp8_f32 v48, v0, v46 op_sel:[0,0,1]
	v_mul_f32_e32 v0, v75, v73
	v_mul_f32_e32 v44, v75, v44
	v_mul_f32_e32 v0, v2, v0
	v_mul_f32_e32 v44, v3, v44
	v_mov_b32_e32 v47, v1
	v_cvt_pk_fp8_f32 v47, v0, v44
	v_mul_f32_e32 v46, v75, v74
	v_mul_f32_e32 v44, v75, v45
	v_mul_f32_e32 v0, v4, v46
	v_mul_f32_e32 v44, v5, v44
	v_cvt_pk_fp8_f32 v47, v0, v44 op_sel:[0,0,1]
	global_store_dword v[42:43], v50, off offset:1024 sc0 sc1
	global_store_dword v[42:43], v51, off offset:1280 sc0 sc1
	global_store_dword v[42:43], v48, off offset:1536 sc0 sc1
	global_store_dword v[42:43], v47, off offset:1792 sc0 sc1
	s_branch .LBB0_1488

; #define GAS __attribute__((address_space(1)))
; #define lane (lane_id())
; __device__ __forceinline__ void scatter_phase(const Ptrs& P, volatile LAS unsigned* MISC, int vcu, int G, int wave, int lane) {
;     ...
;             const int p0 = (int)(256u * MISC[16 + (ee[q] & 0xffu)]) + r0[q], p1 = (int)(256u * MISC[16 + ((ee[q] >> 8) & 0xffu)]) + r1[q];
;             if (lane == 0) { P.sel_pos[2 * m] = p0; P.sel_pos[2 * m + 1] = p1; }
;             GAS v4u* d0 = (GAS v4u*)(P.XS + (size_t)p0 * D) + lane; GAS v4u* d1 = (GAS v4u*)(P.XS + (size_t)p1 * D) + lane;
;             d0[0] = a0[q]; d0[64] = a1[q]; d1[0] = a0[q]; d1[64] = a1[q]; }
.LBB0_1615:
	s_or_b64 exec, exec, s[16:17]
	v_ashrrev_i32_e32 v13, 31, v10
	v_mov_b32_e32 v12, v10
	v_lshlrev_b64 v[12:13], 11, v[12:13]
	v_ashrrev_i32_e32 v15, 31, v11
	v_mov_b32_e32 v14, v11
	v_lshl_add_u64 v[12:13], v[36:37], 0, v[12:13]
	v_lshlrev_b64 v[10:11], 11, v[14:15]
	v_lshl_add_u64 v[10:11], v[36:37], 0, v[10:11]
	global_store_dwordx4 v[12:13], v[2:5], off sc0 sc1
	global_store_dwordx4 v[12:13], v[6:9], off offset:1024 sc0 sc1
	global_store_dwordx4 v[10:11], v[2:5], off sc0 sc1
	global_store_dwordx4 v[10:11], v[6:9], off offset:1024 sc0 sc1

; #define GAS __attribute__((address_space(1)))
; #define lane (lane_id())
; __device__ __forceinline__ void scatter_phase(const Ptrs& P, volatile LAS unsigned* MISC, int vcu, int G, int wave, int lane) {
;     ...
;     for (int m0 = gw; m0 < M; m0 += NR * NGW) {
;         unsigned ee[NR]; int r0[NR], r1[NR]; v4u a0[NR], a1[NR];
; #pragma unroll
;         for (int q = 0; q < NR; ++q) { const int mq = m0 + q * NGW; const int m = mq < M ? mq : m0;
;             ee[q] = P.sel_e[m]; r0[q] = P.sel_rel[2 * m]; r1[q] = P.sel_rel[2 * m + 1];
;             const GAS v4u* sp = (const GAS v4u*)(P.AB8 + (size_t)m * D) + lane; a0[q] = sp[0]; a1[q] = sp[64]; }
; #pragma unroll
;         for (int q = 0; q < NR; ++q) { const int m = m0 + q * NGW; if (m >= M) break;
;             const int p0 = (int)(256u * MISC[16 + (ee[q] & 0xffu)]) + r0[q], p1 = (int)(256u * MISC[16 + ((ee[q] >> 8) & 0xffu)]) + r1[q];
;             if (lane == 0) { P.sel_pos[2 * m] = p0; P.sel_pos[2 * m + 1] = p1; }
;             GAS v4u* d0 = (GAS v4u*)(P.XS + (size_t)p0 * D) + lane; GAS v4u* d1 = (GAS v4u*)(P.XS + (size_t)p1 * D) + lane;
;             d0[0] = a0[q]; d0[64] = a1[q]; d1[0] = a0[q]; d1[64] = a1[q]; }
.LBB0_1617:
	global_load_dword v0, v1, s[0:1]
	s_ashr_i32 s15, s14, 31
	s_add_i32 s18, s68, s34
	s_cmpk_lt_i32 s18, 0x2000
	s_cselect_b64 s[22:23], -1, 0
	s_and_b64 s[16:17], s[22:23], exec
	s_cselect_b32 s16, s18, s34
	s_ashr_i32 s17, s16, 31
	s_lshl_b64 s[18:19], s[16:17], 2
	s_add_u32 s18, s26, s18
	s_addc_u32 s19, s27, s19
	s_lshl_b32 s20, s16, 1
	s_ashr_i32 s21, s20, 31
	global_load_dwordx4 v[30:33], v[38:39], off
	global_load_dwordx4 v[26:29], v[38:39], off offset:1024
	global_load_dword v48, v1, s[18:19]
	s_lshl_b64 s[18:19], s[20:21], 2
	s_add_u32 s18, s28, s18
	s_addc_u32 s19, s29, s19
	s_lshl_b64 s[16:17], s[16:17], 11
	s_add_i32 s24, s50, s34
	s_cmpk_lt_i32 s24, 0x2000
	s_cselect_b64 s[20:21], -1, 0
	v_lshl_add_u64 v[2:3], v[34:35], 0, s[16:17]
	s_and_b64 s[16:17], s[20:21], exec
	s_cselect_b32 s16, s24, s34
	s_ashr_i32 s17, s16, 31
	global_load_dwordx2 v[44:45], v1, s[18:19]
	s_lshl_b64 s[18:19], s[16:17], 2
	s_add_u32 s18, s26, s18
	s_addc_u32 s19, s27, s19
	s_lshl_b32 s24, s16, 1
	s_ashr_i32 s25, s24, 31
	global_load_dwordx4 v[22:25], v[2:3], off
	global_load_dwordx4 v[18:21], v[2:3], off offset:1024
	global_load_dword v49, v1, s[18:19]
	s_lshl_b64 s[18:19], s[24:25], 2
	s_add_u32 s18, s28, s18
	s_addc_u32 s19, s29, s19
	s_lshl_b64 s[16:17], s[16:17], 11
	s_add_i32 s24, s53, s34
	s_cmpk_lt_i32 s24, 0x2000
	v_lshl_add_u64 v[2:3], v[34:35], 0, s[16:17]
	s_cselect_b64 s[16:17], -1, 0
	global_load_dwordx2 v[42:43], v1, s[18:19]
	s_and_b64 s[18:19], s[16:17], exec
	s_cselect_b32 s18, s24, s34
	s_ashr_i32 s19, s18, 31
	s_lshl_b64 s[24:25], s[18:19], 2
	s_add_u32 s24, s26, s24
	s_addc_u32 s25, s27, s25
	s_lshl_b32 s40, s18, 1
	s_ashr_i32 s41, s40, 31
	global_load_dwordx4 v[14:17], v[2:3], off
	global_load_dwordx4 v[10:13], v[2:3], off offset:1024
	global_load_dword v50, v1, s[24:25]
	s_lshl_b64 s[24:25], s[40:41], 2
	s_add_u32 s40, s28, s24
	s_addc_u32 s41, s29, s25
	s_lshl_b64 s[18:19], s[18:19], 11
	s_lshl_b64 s[24:25], s[14:15], 2
	v_mov_b32_e32 v47, 2
	v_lshl_add_u64 v[6:7], v[34:35], 0, s[18:19]
	s_add_u32 s18, s28, s24
	v_readlane_b32 s15, v254, 17
	s_addc_u32 s19, s29, s25
	global_load_dwordx2 v[40:41], v1, s[40:41]
	global_load_dwordx4 v[2:5], v[6:7], off
	s_nop 0
	global_load_dwordx4 v[6:9], v[6:7], off offset:1024
	s_waitcnt vmcnt(14)
	v_lshlrev_b32_sdwa v46, v47, v0 dst_sel:DWORD dst_unused:UNUSED_PAD src0_sel:DWORD src1_sel:BYTE_0
	v_lshlrev_b32_sdwa v0, v47, v0 dst_sel:DWORD dst_unused:UNUSED_PAD src0_sel:DWORD src1_sel:BYTE_1
	v_add_u32_e32 v46, s15, v46
	v_add_u32_e32 v0, s15, v0
	ds_read_b32 v51, v46 offset:64
	ds_read_b32 v0, v0 offset:64
	global_load_dwordx2 v[46:47], v1, s[18:19]
	s_waitcnt lgkmcnt(1)
	v_lshlrev_b32_e32 v51, 8, v51
	s_waitcnt lgkmcnt(0)
	v_lshlrev_b32_e32 v0, 8, v0
	s_waitcnt vmcnt(12)
	v_readfirstlane_b32 s40, v48
	s_waitcnt vmcnt(8)
	v_readfirstlane_b32 s35, v49
	s_waitcnt vmcnt(4)
	v_readfirstlane_b32 s15, v50
	s_waitcnt vmcnt(0)
	v_add_u32_e32 v47, v0, v47
	v_add_u32_e32 v46, v51, v46
	s_and_saveexec_b64 s[18:19], s[38:39]
	s_cbranch_execz .LBB0_1619
	s_add_u32 s24, s30, s24
	s_addc_u32 s25, s31, s25
	global_store_dwordx2 v1, v[46:47], s[24:25] sc0 sc1
; #define GAS __attribute__((address_space(1)))
; #define lane (lane_id())
; __device__ __forceinline__ void scatter_phase(const Ptrs& P, volatile LAS unsigned* MISC, int vcu, int G, int wave, int lane) {
;     ...
; #pragma unroll
;         for (int q = 0; q < NR; ++q) { const int m = m0 + q * NGW; if (m >= M) break;
;             const int p0 = (int)(256u * MISC[16 + (ee[q] & 0xffu)]) + r0[q], p1 = (int)(256u * MISC[16 + ((ee[q] >> 8) & 0xffu)]) + r1[q];
;             if (lane == 0) { P.sel_pos[2 * m] = p0; P.sel_pos[2 * m + 1] = p1; }
;             GAS v4u* d0 = (GAS v4u*)(P.XS + (size_t)p0 * D) + lane; GAS v4u* d1 = (GAS v4u*)(P.XS + (size_t)p1 * D) + lane;
;             d0[0] = a0[q]; d0[64] = a1[q]; d1[0] = a0[q]; d1[64] = a1[q]; }
.LBB0_1619:
	s_or_b64 exec, exec, s[18:19]
	v_ashrrev_i32_e32 v49, 31, v46
	v_mov_b32_e32 v48, v46
	v_ashrrev_i32_e32 v51, 31, v47
	v_mov_b32_e32 v50, v47
	v_lshlrev_b64 v[48:49], 11, v[48:49]
	v_lshlrev_b64 v[46:47], 11, v[50:51]
	v_lshl_add_u64 v[48:49], v[36:37], 0, v[48:49]
	v_lshl_add_u64 v[46:47], v[36:37], 0, v[46:47]
	s_andn2_b64 vcc, exec, s[22:23]
	global_store_dwordx4 v[48:49], v[30:33], off sc0 sc1
	global_store_dwordx4 v[48:49], v[26:29], off offset:1024 sc0 sc1
	global_store_dwordx4 v[46:47], v[30:33], off sc0 sc1
	global_store_dwordx4 v[46:47], v[26:29], off offset:1024 sc0 sc1
	s_cbranch_vccnz .LBB0_1616
	s_and_b32 s18, s40, 0xff
	s_lshl_b32 s18, s18, 2
	v_readlane_b32 s19, v254, 17
	s_add_i32 s18, s19, s18
	v_mov_b32_e32 v0, s18
	s_bfe_u32 s18, s40, 0x80008
	s_lshl_b32 s18, s18, 2
	s_add_i32 s18, s19, s18
	v_mov_b32_e32 v26, s18
	ds_read_b32 v0, v0 offset:64
	ds_read_b32 v26, v26 offset:64
	s_waitcnt lgkmcnt(1)
	v_lshlrev_b32_e32 v0, 8, v0
	s_waitcnt lgkmcnt(0)
	v_lshlrev_b32_e32 v27, 8, v26
	v_add_u32_e32 v26, v0, v44
	v_add_u32_e32 v27, v27, v45
	s_and_saveexec_b64 s[18:19], s[38:39]
	s_cbranch_execz .LBB0_1622
	s_add_i32 s22, s50, s14
	s_ashr_i32 s23, s22, 31
	s_lshl_b64 s[22:23], s[22:23], 2
	s_add_u32 s22, s30, s22
	s_addc_u32 s23, s31, s23
	global_store_dwordx2 v1, v[26:27], s[22:23] sc0 sc1
.LBB0_1622:
	s_or_b64 exec, exec, s[18:19]
	v_ashrrev_i32_e32 v29, 31, v26
	v_mov_b32_e32 v28, v26
	v_ashrrev_i32_e32 v31, 31, v27
	v_mov_b32_e32 v30, v27
	v_lshlrev_b64 v[28:29], 11, v[28:29]
	v_lshlrev_b64 v[26:27], 11, v[30:31]
	v_lshl_add_u64 v[28:29], v[36:37], 0, v[28:29]
	v_lshl_add_u64 v[26:27], v[36:37], 0, v[26:27]
	s_andn2_b64 vcc, exec, s[20:21]
	global_store_dwordx4 v[28:29], v[22:25], off sc0 sc1
	global_store_dwordx4 v[28:29], v[18:21], off offset:1024 sc0 sc1
	global_store_dwordx4 v[26:27], v[22:25], off sc0 sc1
	global_store_dwordx4 v[26:27], v[18:21], off offset:1024 sc0 sc1
	s_cbranch_vccnz .LBB0_1616
	s_and_b32 s18, s35, 0xff
	s_lshl_b32 s18, s18, 2
	v_readlane_b32 s19, v254, 17
	s_add_i32 s18, s19, s18
	v_mov_b32_e32 v0, s18
	s_bfe_u32 s18, s35, 0x80008
	s_lshl_b32 s18, s18, 2
	s_add_i32 s18, s19, s18
	v_mov_b32_e32 v18, s18
	ds_read_b32 v0, v0 offset:64
	ds_read_b32 v18, v18 offset:64
	s_waitcnt lgkmcnt(1)
	v_lshlrev_b32_e32 v0, 8, v0
	s_waitcnt lgkmcnt(0)
	v_lshlrev_b32_e32 v19, 8, v18
	v_add_u32_e32 v18, v0, v42
	v_add_u32_e32 v19, v19, v43
	s_and_saveexec_b64 s[18:19], s[38:39]
	s_cbranch_execz .LBB0_1625
	s_add_i32 s20, s48, s14
	s_ashr_i32 s21, s20, 31
	s_lshl_b64 s[20:21], s[20:21], 2
	s_add_u32 s20, s30, s20
	s_addc_u32 s21, s31, s21
	global_store_dwordx2 v1, v[18:19], s[20:21] sc0 sc1
.LBB0_1625:
	s_or_b64 exec, exec, s[18:19]
	v_ashrrev_i32_e32 v21, 31, v18
	v_mov_b32_e32 v20, v18
	v_ashrrev_i32_e32 v23, 31, v19
	v_mov_b32_e32 v22, v19
	v_lshlrev_b64 v[20:21], 11, v[20:21]
	v_lshlrev_b64 v[18:19], 11, v[22:23]
	v_lshl_add_u64 v[20:21], v[36:37], 0, v[20:21]
	v_lshl_add_u64 v[18:19], v[36:37], 0, v[18:19]
	s_andn2_b64 vcc, exec, s[16:17]
	global_store_dwordx4 v[20:21], v[14:17], off sc0 sc1
	global_store_dwordx4 v[20:21], v[10:13], off offset:1024 sc0 sc1
	global_store_dwordx4 v[18:19], v[14:17], off sc0 sc1
	global_store_dwordx4 v[18:19], v[10:13], off offset:1024 sc0 sc1
	s_cbranch_vccnz .LBB0_1616
	s_and_b32 s16, s15, 0xff
	s_bfe_u32 s15, s15, 0x80008
	s_lshl_b32 s16, s16, 2
	v_readlane_b32 s17, v254, 17
	s_lshl_b32 s15, s15, 2
	s_add_i32 s16, s17, s16
	s_add_i32 s15, s17, s15
	v_mov_b32_e32 v0, s16
	v_mov_b32_e32 v10, s15
	ds_read_b32 v0, v0 offset:64
	ds_read_b32 v10, v10 offset:64
	s_waitcnt lgkmcnt(1)
	v_lshlrev_b32_e32 v0, 8, v0
	s_waitcnt lgkmcnt(0)
	v_lshlrev_b32_e32 v11, 8, v10
	v_add_u32_e32 v10, v0, v40
	v_add_u32_e32 v11, v11, v41
	s_and_saveexec_b64 s[16:17], s[38:39]
	s_cbranch_execz .LBB0_1615
	s_mul_i32 s15, s87, 48
	s_add_i32 s18, s15, s14
	s_ashr_i32 s19, s18, 31
	s_lshl_b64 s[18:19], s[18:19], 2
	s_add_u32 s18, s30, s18
	s_addc_u32 s19, s31, s19
	global_store_dwordx2 v1, v[10:11], s[18:19] sc0 sc1
	s_branch .LBB0_1615
